# all fp8 GEMMs use the unscaled f8f6f4 MFMA (no per-MFMA ld_scale); the constant 2^-6 weight scale is folded exactly into epilogue constants (power-of-two, bit-identical)
# speedup vs baseline: 1.0115x; 1.0115x over previous
.LBB0_710:
	s_add_u32 s46, s46, 0x20080
	s_addc_u32 s47, s47, 0
	s_add_u32 s37, s52, 0x100
	s_addc_u32 s39, s53, 0
	s_mov_b32 s79, -2
	ds_read_b128 v[18:21], v192
	ds_read_b128 v[22:25], v192 offset:1024
	ds_read_b128 v[26:29], v192 offset:2048
	ds_read_b128 v[30:33], v192 offset:3072
	ds_read_b128 v[2:5], v193
	ds_read_b128 v[6:9], v193 offset:1024
	ds_read_b128 v[10:13], v193 offset:2048
	ds_read_b128 v[14:17], v193 offset:3072
	s_add_u32 s52, s46, 0xfffe0080
	s_addc_u32 s53, s47, -1
	s_cmp_eq_u32 s79, 4
	s_cselect_b32 s55, s41, s53
	s_cselect_b32 s54, s40, s52
	s_cselect_b32 s53, s43, s39
	s_cselect_b32 s52, s42, s37
	v_lshl_add_u64 v[220:221], s[46:47], 0, v[174:175]
	s_add_i32 m0, s35, 0xc000
	ds_read_b128 v[182:185], v194
	ds_read_b128 v[186:189], v194 offset:1024
	ds_read_b128 v[196:199], v194 offset:2048
	ds_read_b128 v[200:203], v194 offset:3072
	ds_read_b128 v[204:207], v194 offset:4096
	ds_read_b128 v[208:211], v194 offset:5120
	ds_read_b128 v[212:215], v194 offset:6144
	ds_read_b128 v[216:219], v194 offset:7168
	global_load_lds_dwordx4 v[220:221], off
	v_lshl_add_u64 v[220:221], s[46:47], 0, v[176:177]
	s_add_i32 m0, s35, 0xe000
	s_nop 0
	global_load_lds_dwordx4 v[220:221], off
	s_waitcnt vmcnt(8)
	s_waitcnt lgkmcnt(0)
	s_barrier
	s_setprio 1
	s_waitcnt lgkmcnt(0)
	v_mfma_f32_16x16x128_f8f6f4 v[158:161], v[18:25], v[182:189], 0
	v_mfma_f32_16x16x128_f8f6f4 v[150:153], v[26:33], v[182:189], 0
	v_mfma_f32_16x16x128_f8f6f4 v[142:145], v[18:25], v[196:203], 0
	v_mfma_f32_16x16x128_f8f6f4 v[134:137], v[26:33], v[196:203], 0
	v_mfma_f32_16x16x128_f8f6f4 v[126:129], v[18:25], v[204:211], 0
	v_mfma_f32_16x16x128_f8f6f4 v[118:121], v[26:33], v[204:211], 0
	v_mfma_f32_16x16x128_f8f6f4 v[110:113], v[18:25], v[212:219], 0
	v_mfma_f32_16x16x128_f8f6f4 v[102:105], v[26:33], v[212:219], 0
	s_setprio 0
	s_setprio 1
	v_mfma_f32_16x16x128_f8f6f4 v[154:157], v[2:9], v[182:189], 0
	v_mfma_f32_16x16x128_f8f6f4 v[146:149], v[10:17], v[182:189], 0
	v_mfma_f32_16x16x128_f8f6f4 v[138:141], v[2:9], v[196:203], 0
	v_mfma_f32_16x16x128_f8f6f4 v[130:133], v[10:17], v[196:203], 0
	v_mfma_f32_16x16x128_f8f6f4 v[122:125], v[2:9], v[204:211], 0
	v_mfma_f32_16x16x128_f8f6f4 v[114:117], v[10:17], v[204:211], 0
	v_mfma_f32_16x16x128_f8f6f4 v[106:109], v[2:9], v[212:219], 0
	v_mfma_f32_16x16x128_f8f6f4 v[98:101], v[10:17], v[212:219], 0
	s_setprio 0
	s_barrier
	s_add_i32 s76, s66, s31
	v_lshl_add_u64 v[182:183], s[52:53], 0, v[168:169]
	s_mov_b32 m0, s76
	ds_read_b128 v[196:199], v194 offset:16384
	ds_read_b128 v[200:203], v194 offset:17408
	ds_read_b128 v[204:207], v194 offset:18432
	ds_read_b128 v[208:211], v194 offset:19456
	ds_read_b128 v[212:215], v194 offset:20480
	ds_read_b128 v[216:219], v194 offset:21504
	ds_read_b128 v[220:223], v194 offset:22528
	ds_read_b128 v[224:227], v194 offset:23552
	global_load_lds_dwordx4 v[182:183], off
	s_add_i32 m0, s76, 0x2000
	s_add_u32 s80, s52, 0x20000
	v_lshl_add_u64 v[184:185], s[52:53], 0, v[164:165]
	s_addc_u32 s81, s53, 0
	s_add_i32 s76, s67, s31
	global_load_lds_dwordx4 v[184:185], off
	v_lshl_add_u64 v[186:187], s[80:81], 0, v[168:169]
	s_mov_b32 m0, s76
	v_lshl_add_u64 v[188:189], s[54:55], 0, v[166:167]
	global_load_lds_dwordx4 v[186:187], off
	v_lshl_add_u64 v[186:187], s[80:81], 0, v[164:165]
	s_add_i32 m0, s76, 0x2000
	s_nop 0
	global_load_lds_dwordx4 v[186:187], off
	v_lshl_add_u64 v[186:187], s[54:55], 0, v[172:173]
	s_mov_b32 m0, s35
	s_nop 0
	global_load_lds_dwordx4 v[186:187], off
	s_mov_b32 m0, s45
	s_nop 0
	global_load_lds_dwordx4 v[188:189], off
	s_waitcnt vmcnt(8)
	s_waitcnt lgkmcnt(0)
	s_barrier
	s_setprio 1
	s_waitcnt lgkmcnt(0)
	v_mfma_f32_16x16x128_f8f6f4 v[94:97], v[18:25], v[196:203], 0
	v_mfma_f32_16x16x128_f8f6f4 v[86:89], v[26:33], v[196:203], 0
	v_mfma_f32_16x16x128_f8f6f4 v[78:81], v[18:25], v[204:211], 0
	v_mfma_f32_16x16x128_f8f6f4 v[70:73], v[26:33], v[204:211], 0
	v_mfma_f32_16x16x128_f8f6f4 v[62:65], v[18:25], v[212:219], 0
	v_mfma_f32_16x16x128_f8f6f4 v[54:57], v[26:33], v[212:219], 0
	v_mfma_f32_16x16x128_f8f6f4 v[46:49], v[18:25], v[220:227], 0
	v_mfma_f32_16x16x128_f8f6f4 v[38:41], v[26:33], v[220:227], 0
	s_setprio 0
	s_setprio 1
	v_mfma_f32_16x16x128_f8f6f4 v[90:93], v[2:9], v[196:203], 0
	v_mfma_f32_16x16x128_f8f6f4 v[82:85], v[10:17], v[196:203], 0
	v_mfma_f32_16x16x128_f8f6f4 v[74:77], v[2:9], v[204:211], 0
	v_mfma_f32_16x16x128_f8f6f4 v[66:69], v[10:17], v[204:211], 0
	v_mfma_f32_16x16x128_f8f6f4 v[58:61], v[2:9], v[212:219], 0
	v_mfma_f32_16x16x128_f8f6f4 v[50:53], v[10:17], v[212:219], 0
	v_mfma_f32_16x16x128_f8f6f4 v[42:45], v[2:9], v[220:227], 0
	v_mfma_f32_16x16x128_f8f6f4 v[34:37], v[10:17], v[220:227], 0
	s_setprio 0
	s_barrier
	s_add_i32 s76, 0, 0x18000
	s_add_i32 s80, 0, 0x1c000
	v_add_u32_e32 v14, s76, v171
	v_add_u32_e32 v30, s80, v171
	ds_read_b128 v[2:5], v14
	ds_read_b128 v[6:9], v14 offset:1024
	ds_read_b128 v[10:13], v14 offset:2048
	ds_read_b128 v[14:17], v14 offset:3072
	ds_read_b128 v[18:21], v30
	ds_read_b128 v[22:25], v30 offset:1024
	ds_read_b128 v[26:29], v30 offset:2048
	ds_read_b128 v[30:33], v30 offset:3072
	s_add_u32 s54, s54, 0x20000
	s_addc_u32 s55, s55, 0
	s_mov_b32 m0, s56
	v_lshl_add_u64 v[228:229], s[54:55], 0, v[172:173]
	ds_read_b128 v[196:199], v194 offset:32768
	ds_read_b128 v[200:203], v194 offset:33792
	ds_read_b128 v[204:207], v194 offset:34816
	ds_read_b128 v[208:211], v194 offset:35840
	ds_read_b128 v[212:215], v194 offset:36864
	ds_read_b128 v[216:219], v194 offset:37888
	ds_read_b128 v[220:223], v194 offset:38912
	ds_read_b128 v[224:227], v194 offset:39936
	global_load_lds_dwordx4 v[228:229], off
	v_lshl_add_u64 v[228:229], s[54:55], 0, v[166:167]
	s_mov_b32 m0, s57
	s_nop 0
	global_load_lds_dwordx4 v[228:229], off
	s_waitcnt vmcnt(8)
	s_waitcnt lgkmcnt(0)
	s_barrier
	s_setprio 1
	s_waitcnt lgkmcnt(0)
	v_mfma_f32_16x16x128_f8f6f4 v[158:161], v[2:9], v[196:203], v[158:161]
	v_mfma_f32_16x16x128_f8f6f4 v[150:153], v[10:17], v[196:203], v[150:153]
	v_mfma_f32_16x16x128_f8f6f4 v[142:145], v[2:9], v[204:211], v[142:145]
	v_mfma_f32_16x16x128_f8f6f4 v[134:137], v[10:17], v[204:211], v[134:137]
	v_mfma_f32_16x16x128_f8f6f4 v[126:129], v[2:9], v[212:219], v[126:129]
	v_mfma_f32_16x16x128_f8f6f4 v[118:121], v[10:17], v[212:219], v[118:121]
	v_mfma_f32_16x16x128_f8f6f4 v[110:113], v[2:9], v[220:227], v[110:113]
	v_mfma_f32_16x16x128_f8f6f4 v[102:105], v[10:17], v[220:227], v[102:105]
	s_setprio 0
	s_setprio 1
	v_mfma_f32_16x16x128_f8f6f4 v[154:157], v[18:25], v[196:203], v[154:157]
	v_mfma_f32_16x16x128_f8f6f4 v[146:149], v[26:33], v[196:203], v[146:149]
	v_mfma_f32_16x16x128_f8f6f4 v[138:141], v[18:25], v[204:211], v[138:141]
	v_mfma_f32_16x16x128_f8f6f4 v[130:133], v[26:33], v[204:211], v[130:133]
	v_mfma_f32_16x16x128_f8f6f4 v[122:125], v[18:25], v[212:219], v[122:125]
	v_mfma_f32_16x16x128_f8f6f4 v[114:117], v[26:33], v[212:219], v[114:117]
	v_mfma_f32_16x16x128_f8f6f4 v[106:109], v[18:25], v[220:227], v[106:109]
	v_mfma_f32_16x16x128_f8f6f4 v[98:101], v[26:33], v[220:227], v[98:101]
	s_setprio 0
	s_barrier
	s_add_i32 s54, s76, s31
	v_lshl_add_u64 v[182:183], v[182:183], 0, s[10:11]
	s_mov_b32 m0, s54
	ds_read_b128 v[196:199], v194 offset:49152
	ds_read_b128 v[200:203], v194 offset:50176
	ds_read_b128 v[204:207], v194 offset:51200
	ds_read_b128 v[208:211], v194 offset:52224
	ds_read_b128 v[212:215], v194 offset:53248
	ds_read_b128 v[216:219], v194 offset:54272
	ds_read_b128 v[220:223], v194 offset:55296
	ds_read_b128 v[224:227], v194 offset:56320
	global_load_lds_dwordx4 v[182:183], off
	s_add_i32 m0, s54, 0x2000
	s_add_u32 s52, s52, 0x20080
	v_lshl_add_u64 v[182:183], v[184:185], 0, s[10:11]
	s_addc_u32 s53, s53, 0
	s_add_i32 s54, s80, s31
	global_load_lds_dwordx4 v[182:183], off
	v_lshl_add_u64 v[182:183], s[52:53], 0, v[168:169]
	s_mov_b32 m0, s54
	s_nop 0
	global_load_lds_dwordx4 v[182:183], off
	v_lshl_add_u64 v[182:183], s[52:53], 0, v[164:165]
	s_add_i32 m0, s54, 0x2000
	s_nop 0
	global_load_lds_dwordx4 v[182:183], off
	v_lshl_add_u64 v[182:183], v[186:187], 0, s[10:11]
	s_mov_b32 m0, s59
	s_nop 0
	global_load_lds_dwordx4 v[182:183], off
	v_lshl_add_u64 v[182:183], v[188:189], 0, s[10:11]
	s_mov_b32 m0, s60
	s_nop 0
	global_load_lds_dwordx4 v[182:183], off
	s_waitcnt vmcnt(8)
	s_waitcnt lgkmcnt(0)
	s_barrier
	s_setprio 1
	s_waitcnt lgkmcnt(0)
	v_mfma_f32_16x16x128_f8f6f4 v[94:97], v[2:9], v[196:203], v[94:97]
	v_mfma_f32_16x16x128_f8f6f4 v[86:89], v[10:17], v[196:203], v[86:89]
	v_mfma_f32_16x16x128_f8f6f4 v[78:81], v[2:9], v[204:211], v[78:81]
	v_mfma_f32_16x16x128_f8f6f4 v[70:73], v[10:17], v[204:211], v[70:73]
	v_mfma_f32_16x16x128_f8f6f4 v[62:65], v[2:9], v[212:219], v[62:65]
	v_mfma_f32_16x16x128_f8f6f4 v[54:57], v[10:17], v[212:219], v[54:57]
	v_mfma_f32_16x16x128_f8f6f4 v[46:49], v[2:9], v[220:227], v[46:49]
	v_mfma_f32_16x16x128_f8f6f4 v[38:41], v[10:17], v[220:227], v[38:41]
	s_setprio 0
	s_setprio 1
	v_mfma_f32_16x16x128_f8f6f4 v[90:93], v[18:25], v[196:203], v[90:93]
	v_mfma_f32_16x16x128_f8f6f4 v[82:85], v[26:33], v[196:203], v[82:85]
	v_mfma_f32_16x16x128_f8f6f4 v[74:77], v[18:25], v[204:211], v[74:77]
	v_mfma_f32_16x16x128_f8f6f4 v[66:69], v[26:33], v[204:211], v[66:69]
	v_mfma_f32_16x16x128_f8f6f4 v[58:61], v[18:25], v[212:219], v[58:61]
	v_mfma_f32_16x16x128_f8f6f4 v[50:53], v[26:33], v[212:219], v[50:53]
	v_mfma_f32_16x16x128_f8f6f4 v[42:45], v[18:25], v[220:227], v[42:45]
	v_mfma_f32_16x16x128_f8f6f4 v[34:37], v[26:33], v[220:227], v[34:37]
	s_setprio 0
	s_barrier
	s_add_i32 s79, s79, 2
	s_add_u32 s46, s46, 0x100
	s_addc_u32 s47, s47, 0
	s_add_u32 s37, s37, 0x100
	s_addc_u32 s39, s39, 0
	s_cmp_gt_u32 s79, 5
.LBB0_711:
	ds_read_b128 v[18:21], v192
	ds_read_b128 v[22:25], v192 offset:1024
	ds_read_b128 v[26:29], v192 offset:2048
	ds_read_b128 v[30:33], v192 offset:3072
	ds_read_b128 v[2:5], v193
	ds_read_b128 v[6:9], v193 offset:1024
	ds_read_b128 v[10:13], v193 offset:2048
	ds_read_b128 v[14:17], v193 offset:3072
	s_add_u32 s52, s46, 0xfffe0080
	s_addc_u32 s53, s47, -1
	s_cmp_eq_u32 s79, 4
	s_cselect_b32 s55, s41, s53
	s_cselect_b32 s54, s40, s52
	s_cselect_b32 s53, s43, s39
	s_cselect_b32 s52, s42, s37
	v_lshl_add_u64 v[220:221], s[46:47], 0, v[174:175]
	s_add_i32 m0, s35, 0xc000
	ds_read_b128 v[182:185], v194
	ds_read_b128 v[186:189], v194 offset:1024
	ds_read_b128 v[196:199], v194 offset:2048
	ds_read_b128 v[200:203], v194 offset:3072
	ds_read_b128 v[204:207], v194 offset:4096
	ds_read_b128 v[208:211], v194 offset:5120
	ds_read_b128 v[212:215], v194 offset:6144
	ds_read_b128 v[216:219], v194 offset:7168
	global_load_lds_dwordx4 v[220:221], off
	v_lshl_add_u64 v[220:221], s[46:47], 0, v[176:177]
	s_add_i32 m0, s35, 0xe000
	s_nop 0
	global_load_lds_dwordx4 v[220:221], off
	s_waitcnt vmcnt(8)
	s_waitcnt lgkmcnt(0)
	s_barrier
	s_setprio 1
	s_waitcnt lgkmcnt(0)
	v_mfma_f32_16x16x128_f8f6f4 v[158:161], v[18:25], v[182:189], v[158:161]
	v_mfma_f32_16x16x128_f8f6f4 v[150:153], v[26:33], v[182:189], v[150:153]
	v_mfma_f32_16x16x128_f8f6f4 v[142:145], v[18:25], v[196:203], v[142:145]
	v_mfma_f32_16x16x128_f8f6f4 v[134:137], v[26:33], v[196:203], v[134:137]
	v_mfma_f32_16x16x128_f8f6f4 v[126:129], v[18:25], v[204:211], v[126:129]
	v_mfma_f32_16x16x128_f8f6f4 v[118:121], v[26:33], v[204:211], v[118:121]
	v_mfma_f32_16x16x128_f8f6f4 v[110:113], v[18:25], v[212:219], v[110:113]
	v_mfma_f32_16x16x128_f8f6f4 v[102:105], v[26:33], v[212:219], v[102:105]
	s_setprio 0
	s_setprio 1
	v_mfma_f32_16x16x128_f8f6f4 v[154:157], v[2:9], v[182:189], v[154:157]
	v_mfma_f32_16x16x128_f8f6f4 v[146:149], v[10:17], v[182:189], v[146:149]
	v_mfma_f32_16x16x128_f8f6f4 v[138:141], v[2:9], v[196:203], v[138:141]
	v_mfma_f32_16x16x128_f8f6f4 v[130:133], v[10:17], v[196:203], v[130:133]
	v_mfma_f32_16x16x128_f8f6f4 v[122:125], v[2:9], v[204:211], v[122:125]
	v_mfma_f32_16x16x128_f8f6f4 v[114:117], v[10:17], v[204:211], v[114:117]
	v_mfma_f32_16x16x128_f8f6f4 v[106:109], v[2:9], v[212:219], v[106:109]
	v_mfma_f32_16x16x128_f8f6f4 v[98:101], v[10:17], v[212:219], v[98:101]
	s_setprio 0
	s_barrier
	s_add_i32 s76, s66, s31
	v_lshl_add_u64 v[182:183], s[52:53], 0, v[168:169]
	s_mov_b32 m0, s76
	ds_read_b128 v[196:199], v194 offset:16384
	ds_read_b128 v[200:203], v194 offset:17408
	ds_read_b128 v[204:207], v194 offset:18432
	ds_read_b128 v[208:211], v194 offset:19456
	ds_read_b128 v[212:215], v194 offset:20480
	ds_read_b128 v[216:219], v194 offset:21504
	ds_read_b128 v[220:223], v194 offset:22528
	ds_read_b128 v[224:227], v194 offset:23552
	global_load_lds_dwordx4 v[182:183], off
	s_add_i32 m0, s76, 0x2000
	s_add_u32 s80, s52, 0x20000
	v_lshl_add_u64 v[184:185], s[52:53], 0, v[164:165]
	s_addc_u32 s81, s53, 0
	s_add_i32 s76, s67, s31
	global_load_lds_dwordx4 v[184:185], off
	v_lshl_add_u64 v[186:187], s[80:81], 0, v[168:169]
	s_mov_b32 m0, s76
	v_lshl_add_u64 v[188:189], s[54:55], 0, v[166:167]
	global_load_lds_dwordx4 v[186:187], off
	v_lshl_add_u64 v[186:187], s[80:81], 0, v[164:165]
	s_add_i32 m0, s76, 0x2000
	s_nop 0
	global_load_lds_dwordx4 v[186:187], off
	v_lshl_add_u64 v[186:187], s[54:55], 0, v[172:173]
	s_mov_b32 m0, s35
	s_nop 0
	global_load_lds_dwordx4 v[186:187], off
	s_mov_b32 m0, s45
	s_nop 0
	global_load_lds_dwordx4 v[188:189], off
	s_waitcnt vmcnt(8)
	s_waitcnt lgkmcnt(0)
	s_barrier
	s_setprio 1
	s_waitcnt lgkmcnt(0)
	v_mfma_f32_16x16x128_f8f6f4 v[94:97], v[18:25], v[196:203], v[94:97]
	v_mfma_f32_16x16x128_f8f6f4 v[86:89], v[26:33], v[196:203], v[86:89]
	v_mfma_f32_16x16x128_f8f6f4 v[78:81], v[18:25], v[204:211], v[78:81]
	v_mfma_f32_16x16x128_f8f6f4 v[70:73], v[26:33], v[204:211], v[70:73]
	v_mfma_f32_16x16x128_f8f6f4 v[62:65], v[18:25], v[212:219], v[62:65]
	v_mfma_f32_16x16x128_f8f6f4 v[54:57], v[26:33], v[212:219], v[54:57]
	v_mfma_f32_16x16x128_f8f6f4 v[46:49], v[18:25], v[220:227], v[46:49]
	v_mfma_f32_16x16x128_f8f6f4 v[38:41], v[26:33], v[220:227], v[38:41]
	s_setprio 0
	s_setprio 1
	v_mfma_f32_16x16x128_f8f6f4 v[90:93], v[2:9], v[196:203], v[90:93]
	v_mfma_f32_16x16x128_f8f6f4 v[82:85], v[10:17], v[196:203], v[82:85]
	v_mfma_f32_16x16x128_f8f6f4 v[74:77], v[2:9], v[204:211], v[74:77]
	v_mfma_f32_16x16x128_f8f6f4 v[66:69], v[10:17], v[204:211], v[66:69]
	v_mfma_f32_16x16x128_f8f6f4 v[58:61], v[2:9], v[212:219], v[58:61]
	v_mfma_f32_16x16x128_f8f6f4 v[50:53], v[10:17], v[212:219], v[50:53]
	v_mfma_f32_16x16x128_f8f6f4 v[42:45], v[2:9], v[220:227], v[42:45]
	v_mfma_f32_16x16x128_f8f6f4 v[34:37], v[10:17], v[220:227], v[34:37]
	s_setprio 0
	s_barrier
	s_add_i32 s76, 0, 0x18000
	s_add_i32 s80, 0, 0x1c000
	v_add_u32_e32 v14, s76, v171
	v_add_u32_e32 v30, s80, v171
	ds_read_b128 v[2:5], v14
	ds_read_b128 v[6:9], v14 offset:1024
	ds_read_b128 v[10:13], v14 offset:2048
	ds_read_b128 v[14:17], v14 offset:3072
	ds_read_b128 v[18:21], v30
	ds_read_b128 v[22:25], v30 offset:1024
	ds_read_b128 v[26:29], v30 offset:2048
	ds_read_b128 v[30:33], v30 offset:3072
	s_add_u32 s54, s54, 0x20000
	s_addc_u32 s55, s55, 0
	s_mov_b32 m0, s56
	v_lshl_add_u64 v[228:229], s[54:55], 0, v[172:173]
	ds_read_b128 v[196:199], v194 offset:32768
	ds_read_b128 v[200:203], v194 offset:33792
	ds_read_b128 v[204:207], v194 offset:34816
	ds_read_b128 v[208:211], v194 offset:35840
	ds_read_b128 v[212:215], v194 offset:36864
	ds_read_b128 v[216:219], v194 offset:37888
	ds_read_b128 v[220:223], v194 offset:38912
	ds_read_b128 v[224:227], v194 offset:39936
	global_load_lds_dwordx4 v[228:229], off
	v_lshl_add_u64 v[228:229], s[54:55], 0, v[166:167]
	s_mov_b32 m0, s57
	s_nop 0
	global_load_lds_dwordx4 v[228:229], off
	s_waitcnt vmcnt(8)
	s_waitcnt lgkmcnt(0)
	s_barrier
	s_setprio 1
	s_waitcnt lgkmcnt(0)
	v_mfma_f32_16x16x128_f8f6f4 v[158:161], v[2:9], v[196:203], v[158:161]
	v_mfma_f32_16x16x128_f8f6f4 v[150:153], v[10:17], v[196:203], v[150:153]
	v_mfma_f32_16x16x128_f8f6f4 v[142:145], v[2:9], v[204:211], v[142:145]
	v_mfma_f32_16x16x128_f8f6f4 v[134:137], v[10:17], v[204:211], v[134:137]
	v_mfma_f32_16x16x128_f8f6f4 v[126:129], v[2:9], v[212:219], v[126:129]
	v_mfma_f32_16x16x128_f8f6f4 v[118:121], v[10:17], v[212:219], v[118:121]
	v_mfma_f32_16x16x128_f8f6f4 v[110:113], v[2:9], v[220:227], v[110:113]
	v_mfma_f32_16x16x128_f8f6f4 v[102:105], v[10:17], v[220:227], v[102:105]
	s_setprio 0
	s_setprio 1
	v_mfma_f32_16x16x128_f8f6f4 v[154:157], v[18:25], v[196:203], v[154:157]
	v_mfma_f32_16x16x128_f8f6f4 v[146:149], v[26:33], v[196:203], v[146:149]
	v_mfma_f32_16x16x128_f8f6f4 v[138:141], v[18:25], v[204:211], v[138:141]
	v_mfma_f32_16x16x128_f8f6f4 v[130:133], v[26:33], v[204:211], v[130:133]
	v_mfma_f32_16x16x128_f8f6f4 v[122:125], v[18:25], v[212:219], v[122:125]
	v_mfma_f32_16x16x128_f8f6f4 v[114:117], v[26:33], v[212:219], v[114:117]
	v_mfma_f32_16x16x128_f8f6f4 v[106:109], v[18:25], v[220:227], v[106:109]
	v_mfma_f32_16x16x128_f8f6f4 v[98:101], v[26:33], v[220:227], v[98:101]
	s_setprio 0
	s_barrier
	s_add_i32 s54, s76, s31
	v_lshl_add_u64 v[182:183], v[182:183], 0, s[10:11]
	s_mov_b32 m0, s54
	ds_read_b128 v[196:199], v194 offset:49152
	ds_read_b128 v[200:203], v194 offset:50176
	ds_read_b128 v[204:207], v194 offset:51200
	ds_read_b128 v[208:211], v194 offset:52224
	ds_read_b128 v[212:215], v194 offset:53248
	ds_read_b128 v[216:219], v194 offset:54272
	ds_read_b128 v[220:223], v194 offset:55296
	ds_read_b128 v[224:227], v194 offset:56320
	global_load_lds_dwordx4 v[182:183], off
	s_add_i32 m0, s54, 0x2000
	s_add_u32 s52, s52, 0x20080
	v_lshl_add_u64 v[182:183], v[184:185], 0, s[10:11]
	s_addc_u32 s53, s53, 0
	s_add_i32 s54, s80, s31
	global_load_lds_dwordx4 v[182:183], off
	v_lshl_add_u64 v[182:183], s[52:53], 0, v[168:169]
	s_mov_b32 m0, s54
	s_nop 0
	global_load_lds_dwordx4 v[182:183], off
	v_lshl_add_u64 v[182:183], s[52:53], 0, v[164:165]
	s_add_i32 m0, s54, 0x2000
	s_nop 0
	global_load_lds_dwordx4 v[182:183], off
	v_lshl_add_u64 v[182:183], v[186:187], 0, s[10:11]
	s_mov_b32 m0, s59
	s_nop 0
	global_load_lds_dwordx4 v[182:183], off
	v_lshl_add_u64 v[182:183], v[188:189], 0, s[10:11]
	s_mov_b32 m0, s60
	s_nop 0
	global_load_lds_dwordx4 v[182:183], off
	s_waitcnt vmcnt(8)
	s_waitcnt lgkmcnt(0)
	s_barrier
	s_setprio 1
	s_waitcnt lgkmcnt(0)
	v_mfma_f32_16x16x128_f8f6f4 v[94:97], v[2:9], v[196:203], v[94:97]
	v_mfma_f32_16x16x128_f8f6f4 v[86:89], v[10:17], v[196:203], v[86:89]
	v_mfma_f32_16x16x128_f8f6f4 v[78:81], v[2:9], v[204:211], v[78:81]
	v_mfma_f32_16x16x128_f8f6f4 v[70:73], v[10:17], v[204:211], v[70:73]
	v_mfma_f32_16x16x128_f8f6f4 v[62:65], v[2:9], v[212:219], v[62:65]
	v_mfma_f32_16x16x128_f8f6f4 v[54:57], v[10:17], v[212:219], v[54:57]
	v_mfma_f32_16x16x128_f8f6f4 v[46:49], v[2:9], v[220:227], v[46:49]
	v_mfma_f32_16x16x128_f8f6f4 v[38:41], v[10:17], v[220:227], v[38:41]
	s_setprio 0
	s_setprio 1
	v_mfma_f32_16x16x128_f8f6f4 v[90:93], v[18:25], v[196:203], v[90:93]
	v_mfma_f32_16x16x128_f8f6f4 v[82:85], v[26:33], v[196:203], v[82:85]
	v_mfma_f32_16x16x128_f8f6f4 v[74:77], v[18:25], v[204:211], v[74:77]
	v_mfma_f32_16x16x128_f8f6f4 v[66:69], v[26:33], v[204:211], v[66:69]
	v_mfma_f32_16x16x128_f8f6f4 v[58:61], v[18:25], v[212:219], v[58:61]
	v_mfma_f32_16x16x128_f8f6f4 v[50:53], v[26:33], v[212:219], v[50:53]
	v_mfma_f32_16x16x128_f8f6f4 v[42:45], v[18:25], v[220:227], v[42:45]
	v_mfma_f32_16x16x128_f8f6f4 v[34:37], v[26:33], v[220:227], v[34:37]
	s_setprio 0
	s_barrier
	s_add_i32 s79, s79, 2
	s_add_u32 s46, s46, 0x100
	s_addc_u32 s47, s47, 0
	s_add_u32 s37, s37, 0x100
	s_addc_u32 s39, s39, 0
	s_cmp_gt_u32 s79, 5
	s_cbranch_scc0 .LBB0_711
	s_and_b64 vcc, exec, s[18:19]
	s_cbranch_vccz .LBB0_714
	s_barrier
.LBB0_714:
	s_mov_b32 s100, 0xbcb8aa3b
	s_mov_b32 s101, 0x45800000
	v_pk_mul_f32 v[16:17], v[158:159], s[100:101] op_sel_hi:[1,0]
	v_pk_mul_f32 v[18:19], v[160:161], s[100:101] op_sel_hi:[1,0]
	v_pk_mul_f32 v[20:21], v[150:151], s[100:101] op_sel_hi:[1,0]
	v_pk_mul_f32 v[22:23], v[152:153], s[100:101] op_sel_hi:[1,0]
	v_exp_f32_e32 v16, v16
	v_exp_f32_e32 v17, v17
	v_exp_f32_e32 v18, v18
	v_exp_f32_e32 v19, v19
	v_exp_f32_e32 v20, v20
	v_exp_f32_e32 v21, v21
	v_exp_f32_e32 v22, v22
	v_exp_f32_e32 v23, v23
	v_pk_fma_f32 v[16:17], v[16:17], s[100:101], s[100:101] op_sel:[0,1,1] op_sel_hi:[1,1,1]
	v_pk_fma_f32 v[18:19], v[18:19], s[100:101], s[100:101] op_sel:[0,1,1] op_sel_hi:[1,1,1]
	v_pk_fma_f32 v[20:21], v[20:21], s[100:101], s[100:101] op_sel:[0,1,1] op_sel_hi:[1,1,1]
	v_pk_fma_f32 v[22:23], v[22:23], s[100:101], s[100:101] op_sel:[0,1,1] op_sel_hi:[1,1,1]
	v_rcp_f32_e32 v16, v16
	v_rcp_f32_e32 v17, v17
	v_rcp_f32_e32 v18, v18
	v_rcp_f32_e32 v19, v19
	v_rcp_f32_e32 v20, v20
	v_rcp_f32_e32 v21, v21
	v_rcp_f32_e32 v22, v22
	v_rcp_f32_e32 v23, v23
	v_pk_mul_f32 v[158:159], v[158:159], v[154:155]
	v_pk_mul_f32 v[160:161], v[160:161], v[156:157]
	v_pk_mul_f32 v[150:151], v[150:151], v[146:147]
	v_pk_mul_f32 v[152:153], v[152:153], v[148:149]
	v_pk_mul_f32 v[158:159], v[158:159], v[16:17]
	v_pk_mul_f32 v[160:161], v[160:161], v[18:19]
	v_pk_mul_f32 v[150:151], v[150:151], v[20:21]
	v_pk_mul_f32 v[152:153], v[152:153], v[22:23]
	v_cvt_pk_fp8_f32 v8, v158, v159
	v_cvt_pk_fp8_f32 v9, v150, v151
	v_cvt_pk_fp8_f32 v8, v160, v161 op_sel:[0,0,1]
	v_cvt_pk_fp8_f32 v9, v152, v153 op_sel:[0,0,1]
	v_pk_mul_f32 v[16:17], v[142:143], s[100:101] op_sel_hi:[1,0]
	v_pk_mul_f32 v[18:19], v[144:145], s[100:101] op_sel_hi:[1,0]
	v_pk_mul_f32 v[20:21], v[134:135], s[100:101] op_sel_hi:[1,0]
	v_pk_mul_f32 v[22:23], v[136:137], s[100:101] op_sel_hi:[1,0]
	v_exp_f32_e32 v16, v16
	v_exp_f32_e32 v17, v17
	v_exp_f32_e32 v18, v18
	v_exp_f32_e32 v19, v19
	v_exp_f32_e32 v20, v20
	v_exp_f32_e32 v21, v21
	v_exp_f32_e32 v22, v22
	v_exp_f32_e32 v23, v23
	v_pk_fma_f32 v[16:17], v[16:17], s[100:101], s[100:101] op_sel:[0,1,1] op_sel_hi:[1,1,1]
	v_pk_fma_f32 v[18:19], v[18:19], s[100:101], s[100:101] op_sel:[0,1,1] op_sel_hi:[1,1,1]
	v_pk_fma_f32 v[20:21], v[20:21], s[100:101], s[100:101] op_sel:[0,1,1] op_sel_hi:[1,1,1]
	v_pk_fma_f32 v[22:23], v[22:23], s[100:101], s[100:101] op_sel:[0,1,1] op_sel_hi:[1,1,1]
	v_rcp_f32_e32 v16, v16
	v_rcp_f32_e32 v17, v17
	v_rcp_f32_e32 v18, v18
	v_rcp_f32_e32 v19, v19
	v_rcp_f32_e32 v20, v20
	v_rcp_f32_e32 v21, v21
	v_rcp_f32_e32 v22, v22
	v_rcp_f32_e32 v23, v23
	v_pk_mul_f32 v[142:143], v[142:143], v[138:139]
	v_pk_mul_f32 v[144:145], v[144:145], v[140:141]
	v_pk_mul_f32 v[134:135], v[134:135], v[130:131]
	v_pk_mul_f32 v[136:137], v[136:137], v[132:133]
	v_pk_mul_f32 v[142:143], v[142:143], v[16:17]
	v_pk_mul_f32 v[144:145], v[144:145], v[18:19]
	v_pk_mul_f32 v[134:135], v[134:135], v[20:21]
	v_pk_mul_f32 v[136:137], v[136:137], v[22:23]
	v_cvt_pk_fp8_f32 v10, v142, v143
	v_cvt_pk_fp8_f32 v11, v134, v135
	v_cvt_pk_fp8_f32 v10, v144, v145 op_sel:[0,0,1]
	v_cvt_pk_fp8_f32 v11, v136, v137 op_sel:[0,0,1]
	v_lshl_or_b32 v2, s78, 7, v191
	v_lshl_add_u32 v6, s44, 8, v190
	v_mov_b64_e32 v[4:5], s[8:9]
	v_ashrrev_i32_e32 v3, 31, v2
	v_mad_i64_i32 v[14:15], s[46:47], v6, s77, v[4:5]
	v_permlane16_swap_b32_e32 v8, v10
	v_permlane16_swap_b32_e32 v9, v11
	v_lshl_add_u64 v[14:15], v[14:15], 0, v[2:3]
	global_store_dwordx4 v[14:15], v[8:11], off
	v_pk_mul_f32 v[16:17], v[126:127], s[100:101] op_sel_hi:[1,0]
	v_pk_mul_f32 v[18:19], v[128:129], s[100:101] op_sel_hi:[1,0]
	v_pk_mul_f32 v[20:21], v[118:119], s[100:101] op_sel_hi:[1,0]
	v_pk_mul_f32 v[22:23], v[120:121], s[100:101] op_sel_hi:[1,0]
	v_exp_f32_e32 v16, v16
	v_exp_f32_e32 v17, v17
	v_exp_f32_e32 v18, v18
	v_exp_f32_e32 v19, v19
	v_exp_f32_e32 v20, v20
	v_exp_f32_e32 v21, v21
	v_exp_f32_e32 v22, v22
	v_exp_f32_e32 v23, v23
	v_pk_fma_f32 v[16:17], v[16:17], s[100:101], s[100:101] op_sel:[0,1,1] op_sel_hi:[1,1,1]
	v_pk_fma_f32 v[18:19], v[18:19], s[100:101], s[100:101] op_sel:[0,1,1] op_sel_hi:[1,1,1]
	v_pk_fma_f32 v[20:21], v[20:21], s[100:101], s[100:101] op_sel:[0,1,1] op_sel_hi:[1,1,1]
	v_pk_fma_f32 v[22:23], v[22:23], s[100:101], s[100:101] op_sel:[0,1,1] op_sel_hi:[1,1,1]
	v_rcp_f32_e32 v16, v16
	v_rcp_f32_e32 v17, v17
	v_rcp_f32_e32 v18, v18
	v_rcp_f32_e32 v19, v19
	v_rcp_f32_e32 v20, v20
	v_rcp_f32_e32 v21, v21
	v_rcp_f32_e32 v22, v22
	v_rcp_f32_e32 v23, v23
	v_pk_mul_f32 v[126:127], v[126:127], v[122:123]
	v_pk_mul_f32 v[128:129], v[128:129], v[124:125]
	v_pk_mul_f32 v[118:119], v[118:119], v[114:115]
	v_pk_mul_f32 v[120:121], v[120:121], v[116:117]
	v_pk_mul_f32 v[126:127], v[126:127], v[16:17]
	v_pk_mul_f32 v[128:129], v[128:129], v[18:19]
	v_pk_mul_f32 v[118:119], v[118:119], v[20:21]
	v_pk_mul_f32 v[120:121], v[120:121], v[22:23]
	v_cvt_pk_fp8_f32 v8, v126, v127
	v_cvt_pk_fp8_f32 v9, v118, v119
	v_cvt_pk_fp8_f32 v8, v128, v129 op_sel:[0,0,1]
	v_cvt_pk_fp8_f32 v9, v120, v121 op_sel:[0,0,1]
	v_pk_mul_f32 v[16:17], v[110:111], s[100:101] op_sel_hi:[1,0]
	v_pk_mul_f32 v[18:19], v[112:113], s[100:101] op_sel_hi:[1,0]
	v_pk_mul_f32 v[20:21], v[102:103], s[100:101] op_sel_hi:[1,0]
	v_pk_mul_f32 v[22:23], v[104:105], s[100:101] op_sel_hi:[1,0]
	v_exp_f32_e32 v16, v16
	v_exp_f32_e32 v17, v17
	v_exp_f32_e32 v18, v18
	v_exp_f32_e32 v19, v19
	v_exp_f32_e32 v20, v20
	v_exp_f32_e32 v21, v21
	v_exp_f32_e32 v22, v22
	v_exp_f32_e32 v23, v23
	v_pk_fma_f32 v[16:17], v[16:17], s[100:101], s[100:101] op_sel:[0,1,1] op_sel_hi:[1,1,1]
	v_pk_fma_f32 v[18:19], v[18:19], s[100:101], s[100:101] op_sel:[0,1,1] op_sel_hi:[1,1,1]
	v_pk_fma_f32 v[20:21], v[20:21], s[100:101], s[100:101] op_sel:[0,1,1] op_sel_hi:[1,1,1]
	v_pk_fma_f32 v[22:23], v[22:23], s[100:101], s[100:101] op_sel:[0,1,1] op_sel_hi:[1,1,1]
	v_rcp_f32_e32 v16, v16
	v_rcp_f32_e32 v17, v17
	v_rcp_f32_e32 v18, v18
	v_rcp_f32_e32 v19, v19
	v_rcp_f32_e32 v20, v20
	v_rcp_f32_e32 v21, v21
	v_rcp_f32_e32 v22, v22
	v_rcp_f32_e32 v23, v23
	v_pk_mul_f32 v[110:111], v[110:111], v[106:107]
	v_pk_mul_f32 v[112:113], v[112:113], v[108:109]
	v_pk_mul_f32 v[102:103], v[102:103], v[98:99]
	v_pk_mul_f32 v[104:105], v[104:105], v[100:101]
	v_pk_mul_f32 v[110:111], v[110:111], v[16:17]
	v_pk_mul_f32 v[112:113], v[112:113], v[18:19]
	v_pk_mul_f32 v[102:103], v[102:103], v[20:21]
	v_pk_mul_f32 v[104:105], v[104:105], v[22:23]
	v_cvt_pk_fp8_f32 v10, v110, v111
	v_cvt_pk_fp8_f32 v11, v102, v103
	v_cvt_pk_fp8_f32 v10, v112, v113 op_sel:[0,0,1]
	v_cvt_pk_fp8_f32 v11, v104, v105 op_sel:[0,0,1]
	v_or_b32_e32 v7, 32, v6
	v_mad_i64_i32 v[12:13], s[46:47], v7, s77, v[4:5]
	v_permlane16_swap_b32_e32 v8, v10
	v_permlane16_swap_b32_e32 v9, v11
	v_lshl_add_u64 v[12:13], v[12:13], 0, v[2:3]
	global_store_dwordx4 v[12:13], v[8:11], off
	v_pk_mul_f32 v[16:17], v[94:95], s[100:101] op_sel_hi:[1,0]
	v_pk_mul_f32 v[18:19], v[96:97], s[100:101] op_sel_hi:[1,0]
	v_pk_mul_f32 v[20:21], v[86:87], s[100:101] op_sel_hi:[1,0]
	v_pk_mul_f32 v[22:23], v[88:89], s[100:101] op_sel_hi:[1,0]
	v_exp_f32_e32 v16, v16
	v_exp_f32_e32 v17, v17
	v_exp_f32_e32 v18, v18
	v_exp_f32_e32 v19, v19
	v_exp_f32_e32 v20, v20
	v_exp_f32_e32 v21, v21
	v_exp_f32_e32 v22, v22
	v_exp_f32_e32 v23, v23
	v_pk_fma_f32 v[16:17], v[16:17], s[100:101], s[100:101] op_sel:[0,1,1] op_sel_hi:[1,1,1]
	v_pk_fma_f32 v[18:19], v[18:19], s[100:101], s[100:101] op_sel:[0,1,1] op_sel_hi:[1,1,1]
	v_pk_fma_f32 v[20:21], v[20:21], s[100:101], s[100:101] op_sel:[0,1,1] op_sel_hi:[1,1,1]
	v_pk_fma_f32 v[22:23], v[22:23], s[100:101], s[100:101] op_sel:[0,1,1] op_sel_hi:[1,1,1]
	v_rcp_f32_e32 v16, v16
	v_rcp_f32_e32 v17, v17
	v_rcp_f32_e32 v18, v18
	v_rcp_f32_e32 v19, v19
	v_rcp_f32_e32 v20, v20
	v_rcp_f32_e32 v21, v21
	v_rcp_f32_e32 v22, v22
	v_rcp_f32_e32 v23, v23
	v_pk_mul_f32 v[94:95], v[94:95], v[90:91]
	v_pk_mul_f32 v[96:97], v[96:97], v[92:93]
	v_pk_mul_f32 v[86:87], v[86:87], v[82:83]
	v_pk_mul_f32 v[88:89], v[88:89], v[84:85]
	v_pk_mul_f32 v[94:95], v[94:95], v[16:17]
	v_pk_mul_f32 v[96:97], v[96:97], v[18:19]
	v_pk_mul_f32 v[86:87], v[86:87], v[20:21]
	v_pk_mul_f32 v[88:89], v[88:89], v[22:23]
	v_cvt_pk_fp8_f32 v8, v94, v95
	v_cvt_pk_fp8_f32 v9, v86, v87
	v_cvt_pk_fp8_f32 v8, v96, v97 op_sel:[0,0,1]
	v_cvt_pk_fp8_f32 v9, v88, v89 op_sel:[0,0,1]
	v_pk_mul_f32 v[16:17], v[78:79], s[100:101] op_sel_hi:[1,0]
	v_pk_mul_f32 v[18:19], v[80:81], s[100:101] op_sel_hi:[1,0]
	v_pk_mul_f32 v[20:21], v[70:71], s[100:101] op_sel_hi:[1,0]
	v_pk_mul_f32 v[22:23], v[72:73], s[100:101] op_sel_hi:[1,0]
	v_exp_f32_e32 v16, v16
	v_exp_f32_e32 v17, v17
	v_exp_f32_e32 v18, v18
	v_exp_f32_e32 v19, v19
	v_exp_f32_e32 v20, v20
	v_exp_f32_e32 v21, v21
	v_exp_f32_e32 v22, v22
	v_exp_f32_e32 v23, v23
	v_pk_fma_f32 v[16:17], v[16:17], s[100:101], s[100:101] op_sel:[0,1,1] op_sel_hi:[1,1,1]
	v_pk_fma_f32 v[18:19], v[18:19], s[100:101], s[100:101] op_sel:[0,1,1] op_sel_hi:[1,1,1]
	v_pk_fma_f32 v[20:21], v[20:21], s[100:101], s[100:101] op_sel:[0,1,1] op_sel_hi:[1,1,1]
	v_pk_fma_f32 v[22:23], v[22:23], s[100:101], s[100:101] op_sel:[0,1,1] op_sel_hi:[1,1,1]
	v_rcp_f32_e32 v16, v16
	v_rcp_f32_e32 v17, v17
	v_rcp_f32_e32 v18, v18
	v_rcp_f32_e32 v19, v19
	v_rcp_f32_e32 v20, v20
	v_rcp_f32_e32 v21, v21
	v_rcp_f32_e32 v22, v22
	v_rcp_f32_e32 v23, v23
	v_pk_mul_f32 v[78:79], v[78:79], v[74:75]
	v_pk_mul_f32 v[80:81], v[80:81], v[76:77]
	v_pk_mul_f32 v[70:71], v[70:71], v[66:67]
	v_pk_mul_f32 v[72:73], v[72:73], v[68:69]
	v_pk_mul_f32 v[78:79], v[78:79], v[16:17]
	v_pk_mul_f32 v[80:81], v[80:81], v[18:19]
	v_pk_mul_f32 v[70:71], v[70:71], v[20:21]
	v_pk_mul_f32 v[72:73], v[72:73], v[22:23]
	v_cvt_pk_fp8_f32 v10, v78, v79
	v_cvt_pk_fp8_f32 v11, v70, v71
	v_cvt_pk_fp8_f32 v10, v80, v81 op_sel:[0,0,1]
	v_cvt_pk_fp8_f32 v11, v72, v73 op_sel:[0,0,1]
	v_add_u32_e32 v7, 0x80, v6
	v_mad_i64_i32 v[12:13], s[46:47], v7, s77, v[4:5]
	v_permlane16_swap_b32_e32 v8, v10
	v_permlane16_swap_b32_e32 v9, v11
	v_lshl_add_u64 v[12:13], v[12:13], 0, v[2:3]
	global_store_dwordx4 v[12:13], v[8:11], off
	v_pk_mul_f32 v[16:17], v[62:63], s[100:101] op_sel_hi:[1,0]
	v_pk_mul_f32 v[18:19], v[64:65], s[100:101] op_sel_hi:[1,0]
	v_pk_mul_f32 v[20:21], v[54:55], s[100:101] op_sel_hi:[1,0]
	v_pk_mul_f32 v[22:23], v[56:57], s[100:101] op_sel_hi:[1,0]
	v_exp_f32_e32 v16, v16
	v_exp_f32_e32 v17, v17
	v_exp_f32_e32 v18, v18
	v_exp_f32_e32 v19, v19
	v_exp_f32_e32 v20, v20
	v_exp_f32_e32 v21, v21
	v_exp_f32_e32 v22, v22
	v_exp_f32_e32 v23, v23
	v_pk_fma_f32 v[16:17], v[16:17], s[100:101], s[100:101] op_sel:[0,1,1] op_sel_hi:[1,1,1]
	v_pk_fma_f32 v[18:19], v[18:19], s[100:101], s[100:101] op_sel:[0,1,1] op_sel_hi:[1,1,1]
	v_pk_fma_f32 v[20:21], v[20:21], s[100:101], s[100:101] op_sel:[0,1,1] op_sel_hi:[1,1,1]
	v_pk_fma_f32 v[22:23], v[22:23], s[100:101], s[100:101] op_sel:[0,1,1] op_sel_hi:[1,1,1]
	v_rcp_f32_e32 v16, v16
	v_rcp_f32_e32 v17, v17
	v_rcp_f32_e32 v18, v18
	v_rcp_f32_e32 v19, v19
	v_rcp_f32_e32 v20, v20
	v_rcp_f32_e32 v21, v21
	v_rcp_f32_e32 v22, v22
	v_rcp_f32_e32 v23, v23
	v_pk_mul_f32 v[62:63], v[62:63], v[58:59]
	v_pk_mul_f32 v[64:65], v[64:65], v[60:61]
	v_pk_mul_f32 v[54:55], v[54:55], v[50:51]
	v_pk_mul_f32 v[56:57], v[56:57], v[52:53]
	v_pk_mul_f32 v[62:63], v[62:63], v[16:17]
	v_pk_mul_f32 v[64:65], v[64:65], v[18:19]
	v_pk_mul_f32 v[54:55], v[54:55], v[20:21]
	v_pk_mul_f32 v[56:57], v[56:57], v[22:23]
	v_cvt_pk_fp8_f32 v8, v62, v63
	v_cvt_pk_fp8_f32 v9, v54, v55
	v_cvt_pk_fp8_f32 v8, v64, v65 op_sel:[0,0,1]
	v_cvt_pk_fp8_f32 v9, v56, v57 op_sel:[0,0,1]
	v_pk_mul_f32 v[16:17], v[46:47], s[100:101] op_sel_hi:[1,0]
	v_pk_mul_f32 v[18:19], v[48:49], s[100:101] op_sel_hi:[1,0]
	v_pk_mul_f32 v[20:21], v[38:39], s[100:101] op_sel_hi:[1,0]
	v_pk_mul_f32 v[22:23], v[40:41], s[100:101] op_sel_hi:[1,0]
	v_exp_f32_e32 v16, v16
	v_exp_f32_e32 v17, v17
	v_exp_f32_e32 v18, v18
	v_exp_f32_e32 v19, v19
	v_exp_f32_e32 v20, v20
	v_exp_f32_e32 v21, v21
	v_exp_f32_e32 v22, v22
	v_exp_f32_e32 v23, v23
	v_pk_fma_f32 v[16:17], v[16:17], s[100:101], s[100:101] op_sel:[0,1,1] op_sel_hi:[1,1,1]
	v_pk_fma_f32 v[18:19], v[18:19], s[100:101], s[100:101] op_sel:[0,1,1] op_sel_hi:[1,1,1]
	v_pk_fma_f32 v[20:21], v[20:21], s[100:101], s[100:101] op_sel:[0,1,1] op_sel_hi:[1,1,1]
	v_pk_fma_f32 v[22:23], v[22:23], s[100:101], s[100:101] op_sel:[0,1,1] op_sel_hi:[1,1,1]
	v_rcp_f32_e32 v16, v16
	v_rcp_f32_e32 v17, v17
	v_rcp_f32_e32 v18, v18
	v_rcp_f32_e32 v19, v19
	v_rcp_f32_e32 v20, v20
	v_rcp_f32_e32 v21, v21
	v_rcp_f32_e32 v22, v22
	v_rcp_f32_e32 v23, v23
	v_pk_mul_f32 v[46:47], v[46:47], v[42:43]
	v_pk_mul_f32 v[48:49], v[48:49], v[44:45]
	v_pk_mul_f32 v[38:39], v[38:39], v[34:35]
	v_pk_mul_f32 v[40:41], v[40:41], v[36:37]
	v_pk_mul_f32 v[46:47], v[46:47], v[16:17]
	v_pk_mul_f32 v[48:49], v[48:49], v[18:19]
	v_pk_mul_f32 v[38:39], v[38:39], v[20:21]
	v_pk_mul_f32 v[40:41], v[40:41], v[22:23]
	v_cvt_pk_fp8_f32 v10, v46, v47
	v_cvt_pk_fp8_f32 v11, v38, v39
	v_cvt_pk_fp8_f32 v10, v48, v49 op_sel:[0,0,1]
	v_cvt_pk_fp8_f32 v11, v40, v41 op_sel:[0,0,1]
	v_add_u32_e32 v6, 0xa0, v6
	v_mad_i64_i32 v[4:5], s[46:47], v6, s77, v[4:5]
	v_permlane16_swap_b32_e32 v8, v10
	v_permlane16_swap_b32_e32 v9, v11
	v_lshl_add_u64 v[2:3], v[4:5], 0, v[2:3]
	s_andn2_b64 vcc, exec, s[0:1]
	s_mov_b64 s[0:1], -1
	global_store_dwordx4 v[2:3], v[8:11], off
	s_cbranch_vccnz .LBB0_707
	s_andn2_b64 vcc, exec, s[6:7]
	s_cbranch_vccnz .LBB0_706
	s_barrier
	s_branch .LBB0_706

.LBB0_872:
	s_add_u32 s40, s40, 0x58080
	s_addc_u32 s41, s41, 0
	s_add_u32 s79, s42, 0x100
	s_addc_u32 s80, s43, 0
	s_mov_b32 s81, -2
	s_waitcnt vmcnt(0)
	ds_read_b128 v[18:21], v192
	ds_read_b128 v[22:25], v192 offset:1024
	ds_read_b128 v[26:29], v192 offset:2048
	ds_read_b128 v[30:33], v192 offset:3072
	ds_read_b128 v[2:5], v193
	ds_read_b128 v[6:9], v193 offset:1024
	ds_read_b128 v[10:13], v193 offset:2048
	ds_read_b128 v[14:17], v193 offset:3072
	s_add_u32 s42, s40, 0xfffa8080
	s_addc_u32 s43, s41, -1
	s_cmp_eq_u32 s81, 18
	s_cselect_b32 s45, s37, s43
	s_cselect_b32 s44, s36, s42
	s_cselect_b32 s43, s39, s80
	s_cselect_b32 s42, s38, s79
	v_lshl_add_u64 v[220:221], s[40:41], 0, v[174:175]
	s_add_i32 m0, s46, 0xc000
	ds_read_b128 v[182:185], v194
	ds_read_b128 v[186:189], v194 offset:1024
	ds_read_b128 v[196:199], v194 offset:2048
	ds_read_b128 v[200:203], v194 offset:3072
	ds_read_b128 v[204:207], v194 offset:4096
	ds_read_b128 v[208:211], v194 offset:5120
	ds_read_b128 v[212:215], v194 offset:6144
	ds_read_b128 v[216:219], v194 offset:7168
	global_load_lds_dwordx4 v[220:221], off
	v_lshl_add_u64 v[220:221], s[40:41], 0, v[176:177]
	s_add_i32 m0, s46, 0xe000
	s_nop 0
	global_load_lds_dwordx4 v[220:221], off
	s_waitcnt vmcnt(8)
	s_waitcnt lgkmcnt(0)
	s_barrier
	s_setprio 1
	s_waitcnt lgkmcnt(0)
	v_mfma_f32_16x16x128_f8f6f4 v[158:161], v[18:25], v[182:189], 0
	v_mfma_f32_16x16x128_f8f6f4 v[154:157], v[26:33], v[182:189], 0
	v_mfma_f32_16x16x128_f8f6f4 v[146:149], v[18:25], v[196:203], 0
	v_mfma_f32_16x16x128_f8f6f4 v[138:141], v[26:33], v[196:203], 0
	v_mfma_f32_16x16x128_f8f6f4 v[130:133], v[18:25], v[204:211], 0
	v_mfma_f32_16x16x128_f8f6f4 v[122:125], v[26:33], v[204:211], 0
	v_mfma_f32_16x16x128_f8f6f4 v[114:117], v[18:25], v[212:219], 0
	v_mfma_f32_16x16x128_f8f6f4 v[106:109], v[26:33], v[212:219], 0
	s_setprio 0
	s_setprio 1
	v_mfma_f32_16x16x128_f8f6f4 v[150:153], v[2:9], v[182:189], 0
	v_mfma_f32_16x16x128_f8f6f4 v[142:145], v[10:17], v[182:189], 0
	v_mfma_f32_16x16x128_f8f6f4 v[134:137], v[2:9], v[196:203], 0
	v_mfma_f32_16x16x128_f8f6f4 v[126:129], v[10:17], v[196:203], 0
	v_mfma_f32_16x16x128_f8f6f4 v[118:121], v[2:9], v[204:211], 0
	v_mfma_f32_16x16x128_f8f6f4 v[110:113], v[10:17], v[204:211], 0
	v_mfma_f32_16x16x128_f8f6f4 v[102:105], v[2:9], v[212:219], 0
	v_mfma_f32_16x16x128_f8f6f4 v[98:101], v[10:17], v[212:219], 0
	s_setprio 0
	s_barrier
	s_add_i32 s76, s60, s3
	v_lshl_add_u64 v[182:183], s[42:43], 0, v[168:169]
	s_mov_b32 m0, s76
	ds_read_b128 v[196:199], v194 offset:16384
	ds_read_b128 v[200:203], v194 offset:17408
	ds_read_b128 v[204:207], v194 offset:18432
	ds_read_b128 v[208:211], v194 offset:19456
	ds_read_b128 v[212:215], v194 offset:20480
	ds_read_b128 v[216:219], v194 offset:21504
	ds_read_b128 v[220:223], v194 offset:22528
	ds_read_b128 v[224:227], v194 offset:23552
	global_load_lds_dwordx4 v[182:183], off
	s_add_i32 m0, s76, 0x2000
	s_add_u32 s82, s42, 0x58000
	v_lshl_add_u64 v[184:185], s[42:43], 0, v[164:165]
	s_addc_u32 s83, s43, 0
	s_add_i32 s76, s61, s3
	global_load_lds_dwordx4 v[184:185], off
	v_lshl_add_u64 v[186:187], s[82:83], 0, v[168:169]
	s_mov_b32 m0, s76
	v_lshl_add_u64 v[188:189], s[44:45], 0, v[166:167]
	global_load_lds_dwordx4 v[186:187], off
	v_lshl_add_u64 v[186:187], s[82:83], 0, v[164:165]
	s_add_i32 m0, s76, 0x2000
	s_nop 0
	global_load_lds_dwordx4 v[186:187], off
	v_lshl_add_u64 v[186:187], s[44:45], 0, v[172:173]
	s_mov_b32 m0, s46
	s_nop 0
	global_load_lds_dwordx4 v[186:187], off
	s_mov_b32 m0, s47
	s_nop 0
	global_load_lds_dwordx4 v[188:189], off
	s_waitcnt vmcnt(8)
	s_waitcnt lgkmcnt(0)
	s_barrier
	s_setprio 1
	s_waitcnt lgkmcnt(0)
	v_mfma_f32_16x16x128_f8f6f4 v[94:97], v[18:25], v[196:203], 0
	v_mfma_f32_16x16x128_f8f6f4 v[90:93], v[26:33], v[196:203], 0
	v_mfma_f32_16x16x128_f8f6f4 v[82:85], v[18:25], v[204:211], 0
	v_mfma_f32_16x16x128_f8f6f4 v[74:77], v[26:33], v[204:211], 0
	v_mfma_f32_16x16x128_f8f6f4 v[66:69], v[18:25], v[212:219], 0
	v_mfma_f32_16x16x128_f8f6f4 v[58:61], v[26:33], v[212:219], 0
	v_mfma_f32_16x16x128_f8f6f4 v[50:53], v[18:25], v[220:227], 0
	v_mfma_f32_16x16x128_f8f6f4 v[42:45], v[26:33], v[220:227], 0
	s_setprio 0
	s_setprio 1
	v_mfma_f32_16x16x128_f8f6f4 v[86:89], v[2:9], v[196:203], 0
	v_mfma_f32_16x16x128_f8f6f4 v[78:81], v[10:17], v[196:203], 0
	v_mfma_f32_16x16x128_f8f6f4 v[70:73], v[2:9], v[204:211], 0
	v_mfma_f32_16x16x128_f8f6f4 v[62:65], v[10:17], v[204:211], 0
	v_mfma_f32_16x16x128_f8f6f4 v[54:57], v[2:9], v[212:219], 0
	v_mfma_f32_16x16x128_f8f6f4 v[46:49], v[10:17], v[212:219], 0
	v_mfma_f32_16x16x128_f8f6f4 v[38:41], v[2:9], v[220:227], 0
	v_mfma_f32_16x16x128_f8f6f4 v[34:37], v[10:17], v[220:227], 0
	s_setprio 0
	s_barrier
	s_add_i32 s76, 0, 0x18000
	s_add_i32 s82, 0, 0x1c000
	v_add_u32_e32 v14, s76, v190
	v_add_u32_e32 v30, s82, v190
	ds_read_b128 v[2:5], v14
	ds_read_b128 v[6:9], v14 offset:1024
	ds_read_b128 v[10:13], v14 offset:2048
	ds_read_b128 v[14:17], v14 offset:3072
	ds_read_b128 v[18:21], v30
	ds_read_b128 v[22:25], v30 offset:1024
	ds_read_b128 v[26:29], v30 offset:2048
	ds_read_b128 v[30:33], v30 offset:3072
	s_add_u32 s44, s44, 0x58000
	s_addc_u32 s45, s45, 0
	s_mov_b32 m0, s52
	v_lshl_add_u64 v[228:229], s[44:45], 0, v[172:173]
	ds_read_b128 v[196:199], v194 offset:32768
	ds_read_b128 v[200:203], v194 offset:33792
	ds_read_b128 v[204:207], v194 offset:34816
	ds_read_b128 v[208:211], v194 offset:35840
	ds_read_b128 v[212:215], v194 offset:36864
	ds_read_b128 v[216:219], v194 offset:37888
	ds_read_b128 v[220:223], v194 offset:38912
	ds_read_b128 v[224:227], v194 offset:39936
	global_load_lds_dwordx4 v[228:229], off
	v_lshl_add_u64 v[228:229], s[44:45], 0, v[166:167]
	s_mov_b32 m0, s53
	s_nop 0
	global_load_lds_dwordx4 v[228:229], off
	s_waitcnt vmcnt(8)
	s_waitcnt lgkmcnt(0)
	s_barrier
	s_setprio 1
	s_waitcnt lgkmcnt(0)
	v_mfma_f32_16x16x128_f8f6f4 v[158:161], v[2:9], v[196:203], v[158:161]
	v_mfma_f32_16x16x128_f8f6f4 v[154:157], v[10:17], v[196:203], v[154:157]
	v_mfma_f32_16x16x128_f8f6f4 v[146:149], v[2:9], v[204:211], v[146:149]
	v_mfma_f32_16x16x128_f8f6f4 v[138:141], v[10:17], v[204:211], v[138:141]
	v_mfma_f32_16x16x128_f8f6f4 v[130:133], v[2:9], v[212:219], v[130:133]
	v_mfma_f32_16x16x128_f8f6f4 v[122:125], v[10:17], v[212:219], v[122:125]
	v_mfma_f32_16x16x128_f8f6f4 v[114:117], v[2:9], v[220:227], v[114:117]
	v_mfma_f32_16x16x128_f8f6f4 v[106:109], v[10:17], v[220:227], v[106:109]
	s_setprio 0
	s_setprio 1
	v_mfma_f32_16x16x128_f8f6f4 v[150:153], v[18:25], v[196:203], v[150:153]
	v_mfma_f32_16x16x128_f8f6f4 v[142:145], v[26:33], v[196:203], v[142:145]
	v_mfma_f32_16x16x128_f8f6f4 v[134:137], v[18:25], v[204:211], v[134:137]
	v_mfma_f32_16x16x128_f8f6f4 v[126:129], v[26:33], v[204:211], v[126:129]
	v_mfma_f32_16x16x128_f8f6f4 v[118:121], v[18:25], v[212:219], v[118:121]
	v_mfma_f32_16x16x128_f8f6f4 v[110:113], v[26:33], v[212:219], v[110:113]
	v_mfma_f32_16x16x128_f8f6f4 v[102:105], v[18:25], v[220:227], v[102:105]
	v_mfma_f32_16x16x128_f8f6f4 v[98:101], v[26:33], v[220:227], v[98:101]
	s_setprio 0
	s_barrier
	s_add_i32 s44, s76, s3
	v_lshl_add_u64 v[182:183], v[182:183], 0, s[18:19]
	s_mov_b32 m0, s44
	ds_read_b128 v[196:199], v194 offset:49152
	ds_read_b128 v[200:203], v194 offset:50176
	ds_read_b128 v[204:207], v194 offset:51200
	ds_read_b128 v[208:211], v194 offset:52224
	ds_read_b128 v[212:215], v194 offset:53248
	ds_read_b128 v[216:219], v194 offset:54272
	ds_read_b128 v[220:223], v194 offset:55296
	ds_read_b128 v[224:227], v194 offset:56320
	global_load_lds_dwordx4 v[182:183], off
	s_add_i32 m0, s44, 0x2000
	s_add_u32 s42, s42, 0x58080
	v_lshl_add_u64 v[182:183], v[184:185], 0, s[18:19]
	s_addc_u32 s43, s43, 0
	s_add_i32 s44, s82, s3
	global_load_lds_dwordx4 v[182:183], off
	v_lshl_add_u64 v[182:183], s[42:43], 0, v[168:169]
	s_mov_b32 m0, s44
	s_nop 0
	global_load_lds_dwordx4 v[182:183], off
	v_lshl_add_u64 v[182:183], s[42:43], 0, v[164:165]
	s_add_i32 m0, s44, 0x2000
	s_nop 0
	global_load_lds_dwordx4 v[182:183], off
	v_lshl_add_u64 v[182:183], v[186:187], 0, s[18:19]
	s_mov_b32 m0, s57
	s_nop 0
	global_load_lds_dwordx4 v[182:183], off
	v_lshl_add_u64 v[182:183], v[188:189], 0, s[18:19]
	s_mov_b32 m0, s58
	s_nop 0
	global_load_lds_dwordx4 v[182:183], off
	s_waitcnt vmcnt(8)
	s_waitcnt lgkmcnt(0)
	s_barrier
	s_setprio 1
	s_waitcnt lgkmcnt(0)
	v_mfma_f32_16x16x128_f8f6f4 v[94:97], v[2:9], v[196:203], v[94:97]
	v_mfma_f32_16x16x128_f8f6f4 v[90:93], v[10:17], v[196:203], v[90:93]
	v_mfma_f32_16x16x128_f8f6f4 v[82:85], v[2:9], v[204:211], v[82:85]
	v_mfma_f32_16x16x128_f8f6f4 v[74:77], v[10:17], v[204:211], v[74:77]
	v_mfma_f32_16x16x128_f8f6f4 v[66:69], v[2:9], v[212:219], v[66:69]
	v_mfma_f32_16x16x128_f8f6f4 v[58:61], v[10:17], v[212:219], v[58:61]
	v_mfma_f32_16x16x128_f8f6f4 v[50:53], v[2:9], v[220:227], v[50:53]
	v_mfma_f32_16x16x128_f8f6f4 v[42:45], v[10:17], v[220:227], v[42:45]
	s_setprio 0
	s_setprio 1
	v_mfma_f32_16x16x128_f8f6f4 v[86:89], v[18:25], v[196:203], v[86:89]
	v_mfma_f32_16x16x128_f8f6f4 v[78:81], v[26:33], v[196:203], v[78:81]
	v_mfma_f32_16x16x128_f8f6f4 v[70:73], v[18:25], v[204:211], v[70:73]
	v_mfma_f32_16x16x128_f8f6f4 v[62:65], v[26:33], v[204:211], v[62:65]
	v_mfma_f32_16x16x128_f8f6f4 v[54:57], v[18:25], v[212:219], v[54:57]
	v_mfma_f32_16x16x128_f8f6f4 v[46:49], v[26:33], v[212:219], v[46:49]
	v_mfma_f32_16x16x128_f8f6f4 v[38:41], v[18:25], v[220:227], v[38:41]
	v_mfma_f32_16x16x128_f8f6f4 v[34:37], v[26:33], v[220:227], v[34:37]
	s_setprio 0
	s_barrier
	s_add_i32 s81, s81, 2
	s_add_u32 s40, s40, 0x100
	s_addc_u32 s41, s41, 0
	s_add_u32 s79, s79, 0x100
	s_addc_u32 s80, s80, 0
	s_cmp_gt_u32 s81, 19
.LBB0_873:
	ds_read_b128 v[18:21], v192
	ds_read_b128 v[22:25], v192 offset:1024
	ds_read_b128 v[26:29], v192 offset:2048
	ds_read_b128 v[30:33], v192 offset:3072
	ds_read_b128 v[2:5], v193
	ds_read_b128 v[6:9], v193 offset:1024
	ds_read_b128 v[10:13], v193 offset:2048
	ds_read_b128 v[14:17], v193 offset:3072
	s_add_u32 s42, s40, 0xfffa8080
	s_addc_u32 s43, s41, -1
	s_cmp_eq_u32 s81, 18
	s_cselect_b32 s45, s37, s43
	s_cselect_b32 s44, s36, s42
	s_cselect_b32 s43, s39, s80
	s_cselect_b32 s42, s38, s79
	v_lshl_add_u64 v[220:221], s[40:41], 0, v[174:175]
	s_add_i32 m0, s46, 0xc000
	ds_read_b128 v[182:185], v194
	ds_read_b128 v[186:189], v194 offset:1024
	ds_read_b128 v[196:199], v194 offset:2048
	ds_read_b128 v[200:203], v194 offset:3072
	ds_read_b128 v[204:207], v194 offset:4096
	ds_read_b128 v[208:211], v194 offset:5120
	ds_read_b128 v[212:215], v194 offset:6144
	ds_read_b128 v[216:219], v194 offset:7168
	global_load_lds_dwordx4 v[220:221], off
	v_lshl_add_u64 v[220:221], s[40:41], 0, v[176:177]
	s_add_i32 m0, s46, 0xe000
	s_nop 0
	global_load_lds_dwordx4 v[220:221], off
	s_waitcnt vmcnt(8)
	s_waitcnt lgkmcnt(0)
	s_barrier
	s_setprio 1
	s_waitcnt lgkmcnt(0)
	v_mfma_f32_16x16x128_f8f6f4 v[158:161], v[18:25], v[182:189], v[158:161]
	v_mfma_f32_16x16x128_f8f6f4 v[154:157], v[26:33], v[182:189], v[154:157]
	v_mfma_f32_16x16x128_f8f6f4 v[146:149], v[18:25], v[196:203], v[146:149]
	v_mfma_f32_16x16x128_f8f6f4 v[138:141], v[26:33], v[196:203], v[138:141]
	v_mfma_f32_16x16x128_f8f6f4 v[130:133], v[18:25], v[204:211], v[130:133]
	v_mfma_f32_16x16x128_f8f6f4 v[122:125], v[26:33], v[204:211], v[122:125]
	v_mfma_f32_16x16x128_f8f6f4 v[114:117], v[18:25], v[212:219], v[114:117]
	v_mfma_f32_16x16x128_f8f6f4 v[106:109], v[26:33], v[212:219], v[106:109]
	s_setprio 0
	s_setprio 1
	v_mfma_f32_16x16x128_f8f6f4 v[150:153], v[2:9], v[182:189], v[150:153]
	v_mfma_f32_16x16x128_f8f6f4 v[142:145], v[10:17], v[182:189], v[142:145]
	v_mfma_f32_16x16x128_f8f6f4 v[134:137], v[2:9], v[196:203], v[134:137]
	v_mfma_f32_16x16x128_f8f6f4 v[126:129], v[10:17], v[196:203], v[126:129]
	v_mfma_f32_16x16x128_f8f6f4 v[118:121], v[2:9], v[204:211], v[118:121]
	v_mfma_f32_16x16x128_f8f6f4 v[110:113], v[10:17], v[204:211], v[110:113]
	v_mfma_f32_16x16x128_f8f6f4 v[102:105], v[2:9], v[212:219], v[102:105]
	v_mfma_f32_16x16x128_f8f6f4 v[98:101], v[10:17], v[212:219], v[98:101]
	s_setprio 0
	s_barrier
	s_add_i32 s76, s60, s3
	v_lshl_add_u64 v[182:183], s[42:43], 0, v[168:169]
	s_mov_b32 m0, s76
	ds_read_b128 v[196:199], v194 offset:16384
	ds_read_b128 v[200:203], v194 offset:17408
	ds_read_b128 v[204:207], v194 offset:18432
	ds_read_b128 v[208:211], v194 offset:19456
	ds_read_b128 v[212:215], v194 offset:20480
	ds_read_b128 v[216:219], v194 offset:21504
	ds_read_b128 v[220:223], v194 offset:22528
	ds_read_b128 v[224:227], v194 offset:23552
	global_load_lds_dwordx4 v[182:183], off
	s_add_i32 m0, s76, 0x2000
	s_add_u32 s82, s42, 0x58000
	v_lshl_add_u64 v[184:185], s[42:43], 0, v[164:165]
	s_addc_u32 s83, s43, 0
	s_add_i32 s76, s61, s3
	global_load_lds_dwordx4 v[184:185], off
	v_lshl_add_u64 v[186:187], s[82:83], 0, v[168:169]
	s_mov_b32 m0, s76
	v_lshl_add_u64 v[188:189], s[44:45], 0, v[166:167]
	global_load_lds_dwordx4 v[186:187], off
	v_lshl_add_u64 v[186:187], s[82:83], 0, v[164:165]
	s_add_i32 m0, s76, 0x2000
	s_nop 0
	global_load_lds_dwordx4 v[186:187], off
	v_lshl_add_u64 v[186:187], s[44:45], 0, v[172:173]
	s_mov_b32 m0, s46
	s_nop 0
	global_load_lds_dwordx4 v[186:187], off
	s_mov_b32 m0, s47
	s_nop 0
	global_load_lds_dwordx4 v[188:189], off
	s_waitcnt vmcnt(8)
	s_waitcnt lgkmcnt(0)
	s_barrier
	s_setprio 1
	s_waitcnt lgkmcnt(0)
	v_mfma_f32_16x16x128_f8f6f4 v[94:97], v[18:25], v[196:203], v[94:97]
	v_mfma_f32_16x16x128_f8f6f4 v[90:93], v[26:33], v[196:203], v[90:93]
	v_mfma_f32_16x16x128_f8f6f4 v[82:85], v[18:25], v[204:211], v[82:85]
	v_mfma_f32_16x16x128_f8f6f4 v[74:77], v[26:33], v[204:211], v[74:77]
	v_mfma_f32_16x16x128_f8f6f4 v[66:69], v[18:25], v[212:219], v[66:69]
	v_mfma_f32_16x16x128_f8f6f4 v[58:61], v[26:33], v[212:219], v[58:61]
	v_mfma_f32_16x16x128_f8f6f4 v[50:53], v[18:25], v[220:227], v[50:53]
	v_mfma_f32_16x16x128_f8f6f4 v[42:45], v[26:33], v[220:227], v[42:45]
	s_setprio 0
	s_setprio 1
	v_mfma_f32_16x16x128_f8f6f4 v[86:89], v[2:9], v[196:203], v[86:89]
	v_mfma_f32_16x16x128_f8f6f4 v[78:81], v[10:17], v[196:203], v[78:81]
	v_mfma_f32_16x16x128_f8f6f4 v[70:73], v[2:9], v[204:211], v[70:73]
	v_mfma_f32_16x16x128_f8f6f4 v[62:65], v[10:17], v[204:211], v[62:65]
	v_mfma_f32_16x16x128_f8f6f4 v[54:57], v[2:9], v[212:219], v[54:57]
	v_mfma_f32_16x16x128_f8f6f4 v[46:49], v[10:17], v[212:219], v[46:49]
	v_mfma_f32_16x16x128_f8f6f4 v[38:41], v[2:9], v[220:227], v[38:41]
	v_mfma_f32_16x16x128_f8f6f4 v[34:37], v[10:17], v[220:227], v[34:37]
	s_setprio 0
	s_barrier
	s_add_i32 s76, 0, 0x18000
	s_add_i32 s82, 0, 0x1c000
	v_add_u32_e32 v14, s76, v190
	v_add_u32_e32 v30, s82, v190
	ds_read_b128 v[2:5], v14
	ds_read_b128 v[6:9], v14 offset:1024
	ds_read_b128 v[10:13], v14 offset:2048
	ds_read_b128 v[14:17], v14 offset:3072
	ds_read_b128 v[18:21], v30
	ds_read_b128 v[22:25], v30 offset:1024
	ds_read_b128 v[26:29], v30 offset:2048
	ds_read_b128 v[30:33], v30 offset:3072
	s_add_u32 s44, s44, 0x58000
	s_addc_u32 s45, s45, 0
	s_mov_b32 m0, s52
	v_lshl_add_u64 v[228:229], s[44:45], 0, v[172:173]
	ds_read_b128 v[196:199], v194 offset:32768
	ds_read_b128 v[200:203], v194 offset:33792
	ds_read_b128 v[204:207], v194 offset:34816
	ds_read_b128 v[208:211], v194 offset:35840
	ds_read_b128 v[212:215], v194 offset:36864
	ds_read_b128 v[216:219], v194 offset:37888
	ds_read_b128 v[220:223], v194 offset:38912
	ds_read_b128 v[224:227], v194 offset:39936
	global_load_lds_dwordx4 v[228:229], off
	v_lshl_add_u64 v[228:229], s[44:45], 0, v[166:167]
	s_mov_b32 m0, s53
	s_nop 0
	global_load_lds_dwordx4 v[228:229], off
	s_waitcnt vmcnt(8)
	s_waitcnt lgkmcnt(0)
	s_barrier
	s_setprio 1
	s_waitcnt lgkmcnt(0)
	v_mfma_f32_16x16x128_f8f6f4 v[158:161], v[2:9], v[196:203], v[158:161]
	v_mfma_f32_16x16x128_f8f6f4 v[154:157], v[10:17], v[196:203], v[154:157]
	v_mfma_f32_16x16x128_f8f6f4 v[146:149], v[2:9], v[204:211], v[146:149]
	v_mfma_f32_16x16x128_f8f6f4 v[138:141], v[10:17], v[204:211], v[138:141]
	v_mfma_f32_16x16x128_f8f6f4 v[130:133], v[2:9], v[212:219], v[130:133]
	v_mfma_f32_16x16x128_f8f6f4 v[122:125], v[10:17], v[212:219], v[122:125]
	v_mfma_f32_16x16x128_f8f6f4 v[114:117], v[2:9], v[220:227], v[114:117]
	v_mfma_f32_16x16x128_f8f6f4 v[106:109], v[10:17], v[220:227], v[106:109]
	s_setprio 0
	s_setprio 1
	v_mfma_f32_16x16x128_f8f6f4 v[150:153], v[18:25], v[196:203], v[150:153]
	v_mfma_f32_16x16x128_f8f6f4 v[142:145], v[26:33], v[196:203], v[142:145]
	v_mfma_f32_16x16x128_f8f6f4 v[134:137], v[18:25], v[204:211], v[134:137]
	v_mfma_f32_16x16x128_f8f6f4 v[126:129], v[26:33], v[204:211], v[126:129]
	v_mfma_f32_16x16x128_f8f6f4 v[118:121], v[18:25], v[212:219], v[118:121]
	v_mfma_f32_16x16x128_f8f6f4 v[110:113], v[26:33], v[212:219], v[110:113]
	v_mfma_f32_16x16x128_f8f6f4 v[102:105], v[18:25], v[220:227], v[102:105]
	v_mfma_f32_16x16x128_f8f6f4 v[98:101], v[26:33], v[220:227], v[98:101]
	s_setprio 0
	s_barrier
	s_add_i32 s44, s76, s3
	v_lshl_add_u64 v[182:183], v[182:183], 0, s[18:19]
	s_mov_b32 m0, s44
	ds_read_b128 v[196:199], v194 offset:49152
	ds_read_b128 v[200:203], v194 offset:50176
	ds_read_b128 v[204:207], v194 offset:51200
	ds_read_b128 v[208:211], v194 offset:52224
	ds_read_b128 v[212:215], v194 offset:53248
	ds_read_b128 v[216:219], v194 offset:54272
	ds_read_b128 v[220:223], v194 offset:55296
	ds_read_b128 v[224:227], v194 offset:56320
	global_load_lds_dwordx4 v[182:183], off
	s_add_i32 m0, s44, 0x2000
	s_add_u32 s42, s42, 0x58080
	v_lshl_add_u64 v[182:183], v[184:185], 0, s[18:19]
	s_addc_u32 s43, s43, 0
	s_add_i32 s44, s82, s3
	global_load_lds_dwordx4 v[182:183], off
	v_lshl_add_u64 v[182:183], s[42:43], 0, v[168:169]
	s_mov_b32 m0, s44
	s_nop 0
	global_load_lds_dwordx4 v[182:183], off
	v_lshl_add_u64 v[182:183], s[42:43], 0, v[164:165]
	s_add_i32 m0, s44, 0x2000
	s_nop 0
	global_load_lds_dwordx4 v[182:183], off
	v_lshl_add_u64 v[182:183], v[186:187], 0, s[18:19]
	s_mov_b32 m0, s57
	s_nop 0
	global_load_lds_dwordx4 v[182:183], off
	v_lshl_add_u64 v[182:183], v[188:189], 0, s[18:19]
	s_mov_b32 m0, s58
	s_nop 0
	global_load_lds_dwordx4 v[182:183], off
	s_waitcnt vmcnt(8)
	s_waitcnt lgkmcnt(0)
	s_barrier
	s_setprio 1
	s_waitcnt lgkmcnt(0)
	v_mfma_f32_16x16x128_f8f6f4 v[94:97], v[2:9], v[196:203], v[94:97]
	v_mfma_f32_16x16x128_f8f6f4 v[90:93], v[10:17], v[196:203], v[90:93]
	v_mfma_f32_16x16x128_f8f6f4 v[82:85], v[2:9], v[204:211], v[82:85]
	v_mfma_f32_16x16x128_f8f6f4 v[74:77], v[10:17], v[204:211], v[74:77]
	v_mfma_f32_16x16x128_f8f6f4 v[66:69], v[2:9], v[212:219], v[66:69]
	v_mfma_f32_16x16x128_f8f6f4 v[58:61], v[10:17], v[212:219], v[58:61]
	v_mfma_f32_16x16x128_f8f6f4 v[50:53], v[2:9], v[220:227], v[50:53]
	v_mfma_f32_16x16x128_f8f6f4 v[42:45], v[10:17], v[220:227], v[42:45]
	s_setprio 0
	s_setprio 1
	v_mfma_f32_16x16x128_f8f6f4 v[86:89], v[18:25], v[196:203], v[86:89]
	v_mfma_f32_16x16x128_f8f6f4 v[78:81], v[26:33], v[196:203], v[78:81]
	v_mfma_f32_16x16x128_f8f6f4 v[70:73], v[18:25], v[204:211], v[70:73]
	v_mfma_f32_16x16x128_f8f6f4 v[62:65], v[26:33], v[204:211], v[62:65]
	v_mfma_f32_16x16x128_f8f6f4 v[54:57], v[18:25], v[212:219], v[54:57]
	v_mfma_f32_16x16x128_f8f6f4 v[46:49], v[26:33], v[212:219], v[46:49]
	v_mfma_f32_16x16x128_f8f6f4 v[38:41], v[18:25], v[220:227], v[38:41]
	v_mfma_f32_16x16x128_f8f6f4 v[34:37], v[26:33], v[220:227], v[34:37]
	s_setprio 0
	s_barrier
	s_add_i32 s81, s81, 2
	s_add_u32 s40, s40, 0x100
	s_addc_u32 s41, s41, 0
	s_add_u32 s79, s79, 0x100
	s_addc_u32 s80, s80, 0
	s_cmp_gt_u32 s81, 19
	s_cbranch_scc0 .LBB0_873
	s_and_b64 vcc, exec, s[20:21]
	s_cbranch_vccz .LBB0_876
	s_barrier

.LBB0_878:
	v_lshl_add_u32 v18, s77, 8, v171
	v_lshl_or_b32 v2, s78, 8, v191
	v_ashrrev_i32_e32 v19, 31, v18
	v_ashrrev_i32_e32 v3, 31, v2
	v_lshlrev_b64 v[4:5], 11, v[18:19]
	v_lshl_add_u64 v[4:5], s[14:15], 0, v[4:5]
	v_lshlrev_b64 v[20:21], 1, v[2:3]
	v_lshl_add_u64 v[30:31], v[4:5], 0, v[20:21]
	s_lshl_b64 s[40:41], s[40:41], 2
	global_load_dwordx4 v[22:25], v[30:31], off
	s_add_u32 s40, s55, s40
	s_addc_u32 s41, s56, s41
	v_lshl_add_u64 v[6:7], v[2:3], 2, s[40:41]
	global_load_dwordx4 v[14:17], v[6:7], off
	global_load_dwordx4 v[10:13], v[6:7], off offset:16
	global_load_dwordx4 v[2:5], v[6:7], off offset:528
	s_nop 0
	global_load_dwordx4 v[6:9], v[6:7], off offset:512
	s_andn2_b64 vcc, exec, s[0:1]
	s_mov_b64 s[0:1], -1
	s_waitcnt vmcnt(0)
	s_mov_b32 s100, 0x3c800000
	v_pk_mul_f32 v[2:3], v[2:3], s[100:101] op_sel_hi:[1,0]
	v_pk_mul_f32 v[4:5], v[4:5], s[100:101] op_sel_hi:[1,0]
	v_pk_mul_f32 v[6:7], v[6:7], s[100:101] op_sel_hi:[1,0]
	v_pk_mul_f32 v[8:9], v[8:9], s[100:101] op_sel_hi:[1,0]
	v_pk_mul_f32 v[10:11], v[10:11], s[100:101] op_sel_hi:[1,0]
	v_pk_mul_f32 v[12:13], v[12:13], s[100:101] op_sel_hi:[1,0]
	v_pk_mul_f32 v[14:15], v[14:15], s[100:101] op_sel_hi:[1,0]
	v_pk_mul_f32 v[16:17], v[16:17], s[100:101] op_sel_hi:[1,0]
	v_lshlrev_b32_e32 v26, 16, v22
	v_and_b32_e32 v27, 0xffff0000, v22
	v_lshlrev_b32_e32 v22, 16, v23
	v_and_b32_e32 v23, 0xffff0000, v23
	v_lshlrev_b32_e32 v28, 16, v24
	v_and_b32_e32 v29, 0xffff0000, v24
	v_lshlrev_b32_e32 v24, 16, v25
	v_and_b32_e32 v25, 0xffff0000, v25
	v_pk_fma_f32 v[32:33], v[160:161], v[16:17], v[22:23]
	v_pk_fma_f32 v[22:23], v[158:159], v[14:15], v[26:27]
	v_pk_fma_f32 v[26:27], v[156:157], v[12:13], v[24:25]
	v_pk_fma_f32 v[24:25], v[154:155], v[10:11], v[28:29]
	v_cvt_pk_bf16_f32 v22, v22, v23
	v_cvt_pk_bf16_f32 v23, v32, v33
	v_or_b32_e32 v32, 16, v18
	v_cvt_pk_bf16_f32 v24, v24, v25
	v_cvt_pk_bf16_f32 v25, v26, v27
	global_load_dwordx4 v[26:29], v[30:31], off offset:256
	v_ashrrev_i32_e32 v33, 31, v32
	v_lshlrev_b64 v[32:33], 11, v[32:33]
	v_lshl_add_u64 v[32:33], s[14:15], 0, v[32:33]
	global_store_dwordx4 v[30:31], v[22:25], off
	v_lshl_add_u64 v[32:33], v[32:33], 0, v[20:21]
	s_waitcnt vmcnt(1)
	v_lshlrev_b32_e32 v22, 16, v26
	v_and_b32_e32 v23, 0xffff0000, v26
	v_lshlrev_b32_e32 v24, 16, v27
	v_and_b32_e32 v25, 0xffff0000, v27
	v_lshlrev_b32_e32 v26, 16, v28
	v_and_b32_e32 v27, 0xffff0000, v28
	v_lshlrev_b32_e32 v28, 16, v29
	v_and_b32_e32 v29, 0xffff0000, v29
	v_pk_fma_f32 v[24:25], v[152:153], v[8:9], v[24:25]
	v_pk_fma_f32 v[22:23], v[150:151], v[6:7], v[22:23]
	v_pk_fma_f32 v[28:29], v[144:145], v[4:5], v[28:29]
	v_pk_fma_f32 v[26:27], v[142:143], v[2:3], v[26:27]
	v_cvt_pk_bf16_f32 v22, v22, v23
	v_cvt_pk_bf16_f32 v23, v24, v25
	s_nop 0
	v_cvt_pk_bf16_f32 v24, v26, v27
	v_cvt_pk_bf16_f32 v25, v28, v29
	global_load_dwordx4 v[26:29], v[32:33], off
	s_nop 0
	global_store_dwordx4 v[30:31], v[22:25], off offset:256
	v_or_b32_e32 v30, 32, v18
	v_ashrrev_i32_e32 v31, 31, v30
	v_lshlrev_b64 v[30:31], 11, v[30:31]
	v_lshl_add_u64 v[30:31], s[14:15], 0, v[30:31]
	v_lshl_add_u64 v[30:31], v[30:31], 0, v[20:21]
	s_waitcnt vmcnt(1)
	v_lshlrev_b32_e32 v22, 16, v26
	v_and_b32_e32 v23, 0xffff0000, v26
	v_lshlrev_b32_e32 v24, 16, v27
	v_and_b32_e32 v25, 0xffff0000, v27
	v_lshlrev_b32_e32 v26, 16, v28
	v_and_b32_e32 v27, 0xffff0000, v28
	v_lshlrev_b32_e32 v28, 16, v29
	v_and_b32_e32 v29, 0xffff0000, v29
	v_pk_fma_f32 v[24:25], v[148:149], v[16:17], v[24:25]
	v_pk_fma_f32 v[22:23], v[146:147], v[14:15], v[22:23]
	v_pk_fma_f32 v[28:29], v[140:141], v[12:13], v[28:29]
	v_pk_fma_f32 v[26:27], v[138:139], v[10:11], v[26:27]
	v_cvt_pk_bf16_f32 v22, v22, v23
	v_cvt_pk_bf16_f32 v23, v24, v25
	s_nop 0
	v_cvt_pk_bf16_f32 v24, v26, v27
	v_cvt_pk_bf16_f32 v25, v28, v29
	global_load_dwordx4 v[26:29], v[32:33], off offset:256
	s_nop 0
	global_store_dwordx4 v[32:33], v[22:25], off
	s_waitcnt vmcnt(1)
	s_nop 0
	v_lshlrev_b32_e32 v22, 16, v26
	v_and_b32_e32 v23, 0xffff0000, v26
	v_lshlrev_b32_e32 v24, 16, v27
	v_and_b32_e32 v25, 0xffff0000, v27
	v_lshlrev_b32_e32 v26, 16, v28
	v_and_b32_e32 v27, 0xffff0000, v28
	v_lshlrev_b32_e32 v28, 16, v29
	v_and_b32_e32 v29, 0xffff0000, v29
	v_pk_fma_f32 v[24:25], v[136:137], v[8:9], v[24:25]
	v_pk_fma_f32 v[22:23], v[134:135], v[6:7], v[22:23]
	v_pk_fma_f32 v[28:29], v[128:129], v[4:5], v[28:29]
	v_pk_fma_f32 v[26:27], v[126:127], v[2:3], v[26:27]
	v_cvt_pk_bf16_f32 v22, v22, v23
	v_cvt_pk_bf16_f32 v23, v24, v25
	s_nop 0
	v_cvt_pk_bf16_f32 v24, v26, v27
	v_cvt_pk_bf16_f32 v25, v28, v29
	global_load_dwordx4 v[26:29], v[30:31], off
	s_nop 0
	global_store_dwordx4 v[32:33], v[22:25], off offset:256
	v_or_b32_e32 v32, 48, v18
	v_ashrrev_i32_e32 v33, 31, v32
	v_lshlrev_b64 v[32:33], 11, v[32:33]
	v_lshl_add_u64 v[32:33], s[14:15], 0, v[32:33]
	v_lshl_add_u64 v[32:33], v[32:33], 0, v[20:21]
	s_waitcnt vmcnt(1)
	v_lshlrev_b32_e32 v22, 16, v26
	v_and_b32_e32 v23, 0xffff0000, v26
	v_lshlrev_b32_e32 v24, 16, v27
	v_and_b32_e32 v25, 0xffff0000, v27
	v_lshlrev_b32_e32 v26, 16, v28
	v_and_b32_e32 v27, 0xffff0000, v28
	v_lshlrev_b32_e32 v28, 16, v29
	v_and_b32_e32 v29, 0xffff0000, v29
	v_pk_fma_f32 v[24:25], v[132:133], v[16:17], v[24:25]
	v_pk_fma_f32 v[22:23], v[130:131], v[14:15], v[22:23]
	v_pk_fma_f32 v[28:29], v[124:125], v[12:13], v[28:29]
	v_pk_fma_f32 v[26:27], v[122:123], v[10:11], v[26:27]
	v_cvt_pk_bf16_f32 v22, v22, v23
	v_cvt_pk_bf16_f32 v23, v24, v25
	s_nop 0
	v_cvt_pk_bf16_f32 v24, v26, v27
	v_cvt_pk_bf16_f32 v25, v28, v29
	global_load_dwordx4 v[26:29], v[30:31], off offset:256
	s_nop 0
	global_store_dwordx4 v[30:31], v[22:25], off
	s_waitcnt vmcnt(1)
	s_nop 0
	v_lshlrev_b32_e32 v22, 16, v26
	v_and_b32_e32 v23, 0xffff0000, v26
	v_lshlrev_b32_e32 v24, 16, v27
	v_and_b32_e32 v25, 0xffff0000, v27
	v_lshlrev_b32_e32 v26, 16, v28
	v_and_b32_e32 v27, 0xffff0000, v28
	v_lshlrev_b32_e32 v28, 16, v29
	v_and_b32_e32 v29, 0xffff0000, v29
	v_pk_fma_f32 v[24:25], v[120:121], v[8:9], v[24:25]
	v_pk_fma_f32 v[22:23], v[118:119], v[6:7], v[22:23]
	v_pk_fma_f32 v[28:29], v[112:113], v[4:5], v[28:29]
	v_pk_fma_f32 v[26:27], v[110:111], v[2:3], v[26:27]
	v_cvt_pk_bf16_f32 v22, v22, v23
	v_cvt_pk_bf16_f32 v23, v24, v25
	s_nop 0
	v_cvt_pk_bf16_f32 v24, v26, v27
	v_cvt_pk_bf16_f32 v25, v28, v29
	global_load_dwordx4 v[26:29], v[32:33], off
	s_nop 0
	global_store_dwordx4 v[30:31], v[22:25], off offset:256
	v_add_u32_e32 v30, 0x80, v18
	v_ashrrev_i32_e32 v31, 31, v30
	v_lshlrev_b64 v[30:31], 11, v[30:31]
	v_lshl_add_u64 v[30:31], s[14:15], 0, v[30:31]
	v_lshl_add_u64 v[30:31], v[30:31], 0, v[20:21]
	s_waitcnt vmcnt(1)
	v_lshlrev_b32_e32 v22, 16, v26
	v_and_b32_e32 v23, 0xffff0000, v26
	v_lshlrev_b32_e32 v24, 16, v27
	v_and_b32_e32 v25, 0xffff0000, v27
	v_lshlrev_b32_e32 v26, 16, v28
	v_and_b32_e32 v27, 0xffff0000, v28
	v_lshlrev_b32_e32 v28, 16, v29
	v_and_b32_e32 v29, 0xffff0000, v29
	v_pk_fma_f32 v[24:25], v[116:117], v[16:17], v[24:25]
	v_pk_fma_f32 v[22:23], v[114:115], v[14:15], v[22:23]
	v_pk_fma_f32 v[28:29], v[108:109], v[12:13], v[28:29]
	v_pk_fma_f32 v[26:27], v[106:107], v[10:11], v[26:27]
	v_cvt_pk_bf16_f32 v22, v22, v23
	v_cvt_pk_bf16_f32 v23, v24, v25
	s_nop 0
	v_cvt_pk_bf16_f32 v24, v26, v27
	v_cvt_pk_bf16_f32 v25, v28, v29
	global_load_dwordx4 v[26:29], v[32:33], off offset:256
	s_nop 0
	global_store_dwordx4 v[32:33], v[22:25], off
	s_waitcnt vmcnt(1)
	s_nop 0
	v_lshlrev_b32_e32 v22, 16, v26
	v_and_b32_e32 v23, 0xffff0000, v26
	v_lshlrev_b32_e32 v24, 16, v27
	v_and_b32_e32 v25, 0xffff0000, v27
	v_lshlrev_b32_e32 v26, 16, v28
	v_and_b32_e32 v27, 0xffff0000, v28
	v_lshlrev_b32_e32 v28, 16, v29
	v_and_b32_e32 v29, 0xffff0000, v29
	v_pk_fma_f32 v[24:25], v[104:105], v[8:9], v[24:25]
	v_pk_fma_f32 v[22:23], v[102:103], v[6:7], v[22:23]
	v_pk_fma_f32 v[28:29], v[100:101], v[4:5], v[28:29]
	v_pk_fma_f32 v[26:27], v[98:99], v[2:3], v[26:27]
	v_cvt_pk_bf16_f32 v22, v22, v23
	v_cvt_pk_bf16_f32 v23, v24, v25
	s_nop 0
	v_cvt_pk_bf16_f32 v24, v26, v27
	v_cvt_pk_bf16_f32 v25, v28, v29
	global_load_dwordx4 v[26:29], v[30:31], off
	s_nop 0
	global_store_dwordx4 v[32:33], v[22:25], off offset:256
	v_add_u32_e32 v32, 0x90, v18
	v_ashrrev_i32_e32 v33, 31, v32
	v_lshlrev_b64 v[32:33], 11, v[32:33]
	v_lshl_add_u64 v[32:33], s[14:15], 0, v[32:33]
	v_lshl_add_u64 v[32:33], v[32:33], 0, v[20:21]
	s_waitcnt vmcnt(1)
	v_lshlrev_b32_e32 v22, 16, v26
	v_and_b32_e32 v23, 0xffff0000, v26
	v_lshlrev_b32_e32 v24, 16, v27
	v_and_b32_e32 v25, 0xffff0000, v27
	v_lshlrev_b32_e32 v26, 16, v28
	v_and_b32_e32 v27, 0xffff0000, v28
	v_lshlrev_b32_e32 v28, 16, v29
	v_and_b32_e32 v29, 0xffff0000, v29
	v_pk_fma_f32 v[24:25], v[96:97], v[16:17], v[24:25]
	v_pk_fma_f32 v[22:23], v[94:95], v[14:15], v[22:23]
	v_pk_fma_f32 v[28:29], v[92:93], v[12:13], v[28:29]
	v_pk_fma_f32 v[26:27], v[90:91], v[10:11], v[26:27]
	v_cvt_pk_bf16_f32 v22, v22, v23
	v_cvt_pk_bf16_f32 v23, v24, v25
	s_nop 0
	v_cvt_pk_bf16_f32 v24, v26, v27
	v_cvt_pk_bf16_f32 v25, v28, v29
	global_load_dwordx4 v[26:29], v[30:31], off offset:256
	s_nop 0
	global_store_dwordx4 v[30:31], v[22:25], off
	s_waitcnt vmcnt(1)
	s_nop 0
	v_lshlrev_b32_e32 v22, 16, v26
	v_and_b32_e32 v23, 0xffff0000, v26
	v_lshlrev_b32_e32 v24, 16, v27
	v_and_b32_e32 v25, 0xffff0000, v27
	v_lshlrev_b32_e32 v26, 16, v28
	v_and_b32_e32 v27, 0xffff0000, v28
	v_lshlrev_b32_e32 v28, 16, v29
	v_and_b32_e32 v29, 0xffff0000, v29
	v_pk_fma_f32 v[24:25], v[88:89], v[8:9], v[24:25]
	v_pk_fma_f32 v[22:23], v[86:87], v[6:7], v[22:23]
	v_pk_fma_f32 v[28:29], v[80:81], v[4:5], v[28:29]
	v_pk_fma_f32 v[26:27], v[78:79], v[2:3], v[26:27]
	v_cvt_pk_bf16_f32 v22, v22, v23
	v_cvt_pk_bf16_f32 v23, v24, v25
	s_nop 0
	v_cvt_pk_bf16_f32 v24, v26, v27
	v_cvt_pk_bf16_f32 v25, v28, v29
	global_load_dwordx4 v[26:29], v[32:33], off
	s_nop 0
	global_store_dwordx4 v[30:31], v[22:25], off offset:256
	v_add_u32_e32 v30, 0xa0, v18
	v_ashrrev_i32_e32 v31, 31, v30
	v_lshlrev_b64 v[30:31], 11, v[30:31]
	v_lshl_add_u64 v[30:31], s[14:15], 0, v[30:31]
	v_lshl_add_u64 v[30:31], v[30:31], 0, v[20:21]
	v_add_u32_e32 v18, 0xb0, v18
	v_ashrrev_i32_e32 v19, 31, v18
	v_lshlrev_b64 v[18:19], 11, v[18:19]
	v_lshl_add_u64 v[18:19], s[14:15], 0, v[18:19]
	s_waitcnt vmcnt(1)
	v_lshlrev_b32_e32 v22, 16, v26
	v_and_b32_e32 v23, 0xffff0000, v26
	v_lshlrev_b32_e32 v24, 16, v27
	v_and_b32_e32 v25, 0xffff0000, v27
	v_lshlrev_b32_e32 v26, 16, v28
	v_and_b32_e32 v27, 0xffff0000, v28
	v_lshlrev_b32_e32 v28, 16, v29
	v_and_b32_e32 v29, 0xffff0000, v29
	v_pk_fma_f32 v[24:25], v[84:85], v[16:17], v[24:25]
	v_pk_fma_f32 v[22:23], v[82:83], v[14:15], v[22:23]
	v_pk_fma_f32 v[28:29], v[76:77], v[12:13], v[28:29]
	v_pk_fma_f32 v[26:27], v[74:75], v[10:11], v[26:27]
	v_cvt_pk_bf16_f32 v22, v22, v23
	v_cvt_pk_bf16_f32 v23, v24, v25
	s_nop 0
	v_cvt_pk_bf16_f32 v24, v26, v27
	v_cvt_pk_bf16_f32 v25, v28, v29
	global_load_dwordx4 v[26:29], v[32:33], off offset:256
	s_nop 0
	global_store_dwordx4 v[32:33], v[22:25], off
	s_waitcnt vmcnt(1)
	s_nop 0
	v_lshlrev_b32_e32 v22, 16, v26
	v_and_b32_e32 v23, 0xffff0000, v26
	v_lshlrev_b32_e32 v24, 16, v27
	v_and_b32_e32 v25, 0xffff0000, v27
	v_lshlrev_b32_e32 v26, 16, v28
	v_and_b32_e32 v27, 0xffff0000, v28
	v_lshlrev_b32_e32 v28, 16, v29
	v_and_b32_e32 v29, 0xffff0000, v29
	v_pk_fma_f32 v[24:25], v[72:73], v[8:9], v[24:25]
	v_pk_fma_f32 v[22:23], v[70:71], v[6:7], v[22:23]
	v_pk_fma_f32 v[28:29], v[64:65], v[4:5], v[28:29]
	v_pk_fma_f32 v[26:27], v[62:63], v[2:3], v[26:27]
	v_cvt_pk_bf16_f32 v22, v22, v23
	v_cvt_pk_bf16_f32 v23, v24, v25
	s_nop 0
	v_cvt_pk_bf16_f32 v24, v26, v27
	v_cvt_pk_bf16_f32 v25, v28, v29
	global_load_dwordx4 v[26:29], v[30:31], off
	s_nop 0
	global_store_dwordx4 v[32:33], v[22:25], off offset:256
	v_lshl_add_u64 v[32:33], v[18:19], 0, v[20:21]
	s_waitcnt vmcnt(1)
	v_lshlrev_b32_e32 v22, 16, v26
	v_and_b32_e32 v23, 0xffff0000, v26
	v_lshlrev_b32_e32 v24, 16, v27
	v_and_b32_e32 v25, 0xffff0000, v27
	v_lshlrev_b32_e32 v26, 16, v28
	v_and_b32_e32 v27, 0xffff0000, v28
	v_lshlrev_b32_e32 v28, 16, v29
	v_and_b32_e32 v29, 0xffff0000, v29
	v_pk_fma_f32 v[24:25], v[68:69], v[16:17], v[24:25]
	v_pk_fma_f32 v[22:23], v[66:67], v[14:15], v[22:23]
	v_pk_fma_f32 v[28:29], v[60:61], v[12:13], v[28:29]
	v_pk_fma_f32 v[26:27], v[58:59], v[10:11], v[26:27]
	v_cvt_pk_bf16_f32 v22, v22, v23
	v_cvt_pk_bf16_f32 v23, v24, v25
	s_nop 0
	v_cvt_pk_bf16_f32 v24, v26, v27
	v_cvt_pk_bf16_f32 v25, v28, v29
	global_load_dwordx4 v[26:29], v[30:31], off offset:256
	s_waitcnt vmcnt(0)
	v_lshlrev_b32_e32 v18, 16, v26
	global_store_dwordx4 v[30:31], v[22:25], off
	v_and_b32_e32 v19, 0xffff0000, v26
	v_lshlrev_b32_e32 v20, 16, v27
	v_and_b32_e32 v21, 0xffff0000, v27
	v_lshlrev_b32_e32 v22, 16, v28
	v_and_b32_e32 v23, 0xffff0000, v28
	v_lshlrev_b32_e32 v24, 16, v29
	v_and_b32_e32 v25, 0xffff0000, v29
	v_pk_fma_f32 v[20:21], v[56:57], v[8:9], v[20:21]
	v_pk_fma_f32 v[18:19], v[54:55], v[6:7], v[18:19]
	v_pk_fma_f32 v[24:25], v[48:49], v[4:5], v[24:25]
	v_pk_fma_f32 v[22:23], v[46:47], v[2:3], v[22:23]
	v_cvt_pk_bf16_f32 v18, v18, v19
	v_cvt_pk_bf16_f32 v19, v20, v21
	s_nop 0
	v_cvt_pk_bf16_f32 v20, v22, v23
	v_cvt_pk_bf16_f32 v21, v24, v25
	global_load_dwordx4 v[22:25], v[32:33], off
	s_nop 0
	global_store_dwordx4 v[30:31], v[18:21], off offset:256
	s_waitcnt vmcnt(1)
	s_nop 0
	v_lshlrev_b32_e32 v18, 16, v22
	v_and_b32_e32 v19, 0xffff0000, v22
	v_lshlrev_b32_e32 v20, 16, v23
	v_and_b32_e32 v21, 0xffff0000, v23
	v_lshlrev_b32_e32 v22, 16, v24
	v_and_b32_e32 v23, 0xffff0000, v24
	v_lshlrev_b32_e32 v24, 16, v25
	v_and_b32_e32 v25, 0xffff0000, v25
	v_pk_fma_f32 v[16:17], v[52:53], v[16:17], v[20:21]
	v_pk_fma_f32 v[14:15], v[50:51], v[14:15], v[18:19]
	v_pk_fma_f32 v[18:19], v[44:45], v[12:13], v[24:25]
	v_pk_fma_f32 v[12:13], v[42:43], v[10:11], v[22:23]
	v_cvt_pk_bf16_f32 v10, v14, v15
	v_cvt_pk_bf16_f32 v11, v16, v17
	s_nop 0
	v_cvt_pk_bf16_f32 v12, v12, v13
	v_cvt_pk_bf16_f32 v13, v18, v19
	global_load_dwordx4 v[14:17], v[32:33], off offset:256
	s_nop 0
	global_store_dwordx4 v[32:33], v[10:13], off
	s_waitcnt vmcnt(1)
	s_nop 0
	v_lshlrev_b32_e32 v10, 16, v14
	v_and_b32_e32 v11, 0xffff0000, v14
	v_lshlrev_b32_e32 v12, 16, v15
	v_and_b32_e32 v13, 0xffff0000, v15
	v_lshlrev_b32_e32 v14, 16, v16
	v_and_b32_e32 v15, 0xffff0000, v16
	v_lshlrev_b32_e32 v16, 16, v17
	v_and_b32_e32 v17, 0xffff0000, v17
	v_pk_fma_f32 v[6:7], v[38:39], v[6:7], v[10:11]
	v_pk_fma_f32 v[10:11], v[36:37], v[4:5], v[16:17]
	v_pk_fma_f32 v[4:5], v[34:35], v[2:3], v[14:15]
	v_pk_fma_f32 v[8:9], v[40:41], v[8:9], v[12:13]
	v_cvt_pk_bf16_f32 v2, v6, v7
	s_nop 0
	v_cvt_pk_bf16_f32 v3, v8, v9
	v_cvt_pk_bf16_f32 v4, v4, v5
	v_cvt_pk_bf16_f32 v5, v10, v11
	global_store_dwordx4 v[32:33], v[2:5], off offset:256
	s_cbranch_vccnz .LBB0_869
	s_andn2_b64 vcc, exec, s[10:11]
	s_cbranch_vccnz .LBB0_868
	s_barrier
	s_branch .LBB0_868

.LBB0_1910:
	v_add_u32_e32 v6, s62, v171
	v_add_u32_e32 v2, v6, v192
	v_ashrrev_i32_e32 v3, 31, v2
	v_add_u32_e32 v6, v6, v193
	v_lshl_add_u64 v[4:5], v[2:3], 2, s[10:11]
	v_add_u32_e32 v2, 0x80, v2
	v_ashrrev_i32_e32 v7, 31, v6
	v_ashrrev_i32_e32 v3, 31, v2
	v_lshl_add_u64 v[8:9], v[6:7], 2, s[10:11]
	v_add_u32_e32 v6, 0x80, v6
	v_lshl_add_u64 v[2:3], v[2:3], 2, s[10:11]
	v_ashrrev_i32_e32 v7, 31, v6
	v_lshl_add_u64 v[6:7], v[6:7], 2, s[10:11]
	global_load_dword v236, v[4:5], off
	s_nop 0
	global_load_dword v237, v[2:3], off
	s_nop 0
	global_load_dword v238, v[8:9], off
	global_load_dword v239, v[6:7], off
	v_mov_b32_e32 v175, v169
	v_mov_b32_e32 v179, v169
	s_add_u32 s37, s42, 0x100
	s_mov_b32 s79, -2
	s_mov_b64 s[46:47], 0
	s_addc_u32 s80, s43, 0
	v_lshl_add_u64 v[180:181], s[18:19], 0, v[174:175]
	v_lshl_add_u64 v[182:183], s[18:19], 0, v[178:179]
	ds_read_b128 v[18:21], v197
	ds_read_b128 v[22:25], v197 offset:1024
	ds_read_b128 v[26:29], v197 offset:2048
	ds_read_b128 v[30:33], v197 offset:3072
	ds_read_b128 v[2:5], v198
	ds_read_b128 v[6:9], v198 offset:1024
	ds_read_b128 v[10:13], v198 offset:2048
	ds_read_b128 v[14:17], v198 offset:3072
	s_add_u32 s42, s46, 0x100
	s_addc_u32 s43, s47, 0
	s_add_u32 s48, s37, s46
	s_addc_u32 s49, s80, s47
	s_cmpk_eq_i32 s46, 0x300
	s_cselect_b64 vcc, -1, 0
	s_and_b64 s[44:45], vcc, exec
	s_cselect_b32 s81, 0, s42
	s_cselect_b32 s76, 0, s43
	s_cselect_b32 s44, s38, s48
	s_cselect_b32 s45, s39, s49
	s_add_u32 s48, s8, s81
	s_addc_u32 s49, s9, s76
	v_lshl_add_u64 v[228:229], v[180:181], 0, s[46:47]
	s_add_i32 m0, s41, 0xc000
	ds_read_b128 v[184:187], v199
	ds_read_b128 v[188:191], v199 offset:1024
	ds_read_b128 v[204:207], v199 offset:2048
	ds_read_b128 v[208:211], v199 offset:3072
	ds_read_b128 v[212:215], v199 offset:4096
	ds_read_b128 v[216:219], v199 offset:5120
	ds_read_b128 v[220:223], v199 offset:6144
	ds_read_b128 v[224:227], v199 offset:7168
	global_load_lds_dwordx4 v[228:229], off
	v_lshl_add_u64 v[228:229], v[182:183], 0, s[46:47]
	s_add_i32 m0, s41, 0xe000
	s_nop 0
	global_load_lds_dwordx4 v[228:229], off
	s_waitcnt vmcnt(8)
	s_waitcnt lgkmcnt(0)
	s_barrier
	s_setprio 1
	s_waitcnt lgkmcnt(0)
	v_mfma_f32_16x16x128_f8f6f4 v[158:161], v[18:25], v[184:191], 0
	v_mfma_f32_16x16x128_f8f6f4 v[150:153], v[26:33], v[184:191], 0
	v_mfma_f32_16x16x128_f8f6f4 v[142:145], v[18:25], v[204:211], 0
	v_mfma_f32_16x16x128_f8f6f4 v[134:137], v[26:33], v[204:211], 0
	v_mfma_f32_16x16x128_f8f6f4 v[126:129], v[18:25], v[212:219], 0
	v_mfma_f32_16x16x128_f8f6f4 v[118:121], v[26:33], v[212:219], 0
	v_mfma_f32_16x16x128_f8f6f4 v[110:113], v[18:25], v[220:227], 0
	v_mfma_f32_16x16x128_f8f6f4 v[102:105], v[26:33], v[220:227], 0
	s_setprio 0
	s_setprio 1
	v_mfma_f32_16x16x128_f8f6f4 v[154:157], v[2:9], v[184:191], 0
	v_mfma_f32_16x16x128_f8f6f4 v[146:149], v[10:17], v[184:191], 0
	v_mfma_f32_16x16x128_f8f6f4 v[138:141], v[2:9], v[204:211], 0
	v_mfma_f32_16x16x128_f8f6f4 v[130:133], v[10:17], v[204:211], 0
	v_mfma_f32_16x16x128_f8f6f4 v[122:125], v[2:9], v[212:219], 0
	v_mfma_f32_16x16x128_f8f6f4 v[114:117], v[10:17], v[212:219], 0
	v_mfma_f32_16x16x128_f8f6f4 v[106:109], v[2:9], v[220:227], 0
	v_mfma_f32_16x16x128_f8f6f4 v[98:101], v[10:17], v[220:227], 0
	s_setprio 0
	s_barrier
	s_add_i32 s46, s5, s52
	v_lshl_add_u64 v[184:185], s[44:45], 0, v[164:165]
	s_mov_b32 m0, s46
	ds_read_b128 v[204:207], v199 offset:16384
	ds_read_b128 v[208:211], v199 offset:17408
	ds_read_b128 v[212:215], v199 offset:18432
	ds_read_b128 v[216:219], v199 offset:19456
	ds_read_b128 v[220:223], v199 offset:20480
	ds_read_b128 v[224:227], v199 offset:21504
	ds_read_b128 v[228:231], v199 offset:22528
	ds_read_b128 v[232:235], v199 offset:23552
	global_load_lds_dwordx4 v[184:185], off
	s_add_i32 m0, s46, 0x2000
	s_add_u32 s46, s44, 0x20000
	v_lshl_add_u64 v[186:187], s[44:45], 0, v[166:167]
	s_addc_u32 s47, s45, 0
	s_add_i32 s76, s66, s52
	global_load_lds_dwordx4 v[186:187], off
	v_lshl_add_u64 v[188:189], s[46:47], 0, v[164:165]
	s_mov_b32 m0, s76
	v_cndmask_b32_e32 v168, v202, v179, vcc
	global_load_lds_dwordx4 v[188:189], off
	v_lshl_add_u64 v[188:189], s[46:47], 0, v[166:167]
	s_add_i32 m0, s76, 0x2000
	v_lshl_add_u64 v[190:191], s[48:49], 0, v[168:169]
	global_load_lds_dwordx4 v[188:189], off
	s_mov_b32 m0, s41
	v_cndmask_b32_e32 v188, v176, v201, vcc
	global_load_lds_dwordx4 v168, s[48:49]
	s_mov_b32 m0, s53
	v_mov_b32_e32 v189, v169
	global_load_lds_dwordx4 v188, s[48:49]
	s_waitcnt vmcnt(8)
	s_waitcnt lgkmcnt(0)
	v_lshl_add_u64 v[188:189], s[48:49], 0, v[188:189]
	s_barrier
	s_setprio 1
	s_waitcnt lgkmcnt(0)
	v_mfma_f32_16x16x128_f8f6f4 v[94:97], v[18:25], v[204:211], 0
	v_mfma_f32_16x16x128_f8f6f4 v[86:89], v[26:33], v[204:211], 0
	v_mfma_f32_16x16x128_f8f6f4 v[78:81], v[18:25], v[212:219], 0
	v_mfma_f32_16x16x128_f8f6f4 v[70:73], v[26:33], v[212:219], 0
	v_mfma_f32_16x16x128_f8f6f4 v[58:61], v[18:25], v[220:227], 0
	v_mfma_f32_16x16x128_f8f6f4 v[46:49], v[26:33], v[220:227], 0
	v_mfma_f32_16x16x128_f8f6f4 v[38:41], v[18:25], v[228:235], 0
	v_mfma_f32_16x16x128_f8f6f4 v[34:37], v[26:33], v[228:235], 0
	s_setprio 0
	s_setprio 1
	v_mfma_f32_16x16x128_f8f6f4 v[90:93], v[2:9], v[204:211], 0
	v_mfma_f32_16x16x128_f8f6f4 v[82:85], v[10:17], v[204:211], 0
	v_mfma_f32_16x16x128_f8f6f4 v[74:77], v[2:9], v[212:219], 0
	v_mfma_f32_16x16x128_f8f6f4 v[66:69], v[10:17], v[212:219], 0
	v_mfma_f32_16x16x128_f8f6f4 v[50:53], v[2:9], v[220:227], 0
	v_mfma_f32_16x16x128_f8f6f4 v[42:45], v[10:17], v[220:227], 0
	v_mfma_f32_16x16x128_f8f6f4 v[62:65], v[2:9], v[228:235], 0
	v_mfma_f32_16x16x128_f8f6f4 v[54:57], v[10:17], v[228:235], 0
	s_setprio 0
	s_barrier
	s_add_i32 s46, 0, 0x18000
	s_add_i32 s47, 0, 0x1c000
	v_add_u32_e32 v14, s46, v177
	v_add_u32_e32 v30, s47, v177
	ds_read_b128 v[2:5], v14
	ds_read_b128 v[6:9], v14 offset:1024
	ds_read_b128 v[10:13], v14 offset:2048
	ds_read_b128 v[14:17], v14 offset:3072
	ds_read_b128 v[18:21], v30
	ds_read_b128 v[22:25], v30 offset:1024
	ds_read_b128 v[26:29], v30 offset:2048
	ds_read_b128 v[30:33], v30 offset:3072
	s_mov_b32 m0, s59
	v_cndmask_b32_e32 v168, v174, v175, vcc
	ds_read_b128 v[204:207], v199 offset:32768
	ds_read_b128 v[208:211], v199 offset:33792
	ds_read_b128 v[212:215], v199 offset:34816
	ds_read_b128 v[216:219], v199 offset:35840
	ds_read_b128 v[220:223], v199 offset:36864
	ds_read_b128 v[224:227], v199 offset:37888
	ds_read_b128 v[228:231], v199 offset:38912
	ds_read_b128 v[232:235], v199 offset:39936
	v_cndmask_b32_e32 v170, v178, v200, vcc
	global_load_lds_dwordx4 v168, s[48:49]
	s_mov_b32 m0, s60
	s_nop 0
	global_load_lds_dwordx4 v170, s[48:49]
	s_waitcnt vmcnt(8)
	s_waitcnt lgkmcnt(0)
	s_barrier
	s_setprio 1
	s_waitcnt lgkmcnt(0)
	v_mfma_f32_16x16x128_f8f6f4 v[158:161], v[2:9], v[204:211], v[158:161]
	v_mfma_f32_16x16x128_f8f6f4 v[150:153], v[10:17], v[204:211], v[150:153]
	v_mfma_f32_16x16x128_f8f6f4 v[142:145], v[2:9], v[212:219], v[142:145]
	v_mfma_f32_16x16x128_f8f6f4 v[134:137], v[10:17], v[212:219], v[134:137]
	v_mfma_f32_16x16x128_f8f6f4 v[126:129], v[2:9], v[220:227], v[126:129]
	v_mfma_f32_16x16x128_f8f6f4 v[118:121], v[10:17], v[220:227], v[118:121]
	v_mfma_f32_16x16x128_f8f6f4 v[110:113], v[2:9], v[228:235], v[110:113]
	v_mfma_f32_16x16x128_f8f6f4 v[102:105], v[10:17], v[228:235], v[102:105]
	s_setprio 0
	s_setprio 1
	v_mfma_f32_16x16x128_f8f6f4 v[154:157], v[18:25], v[204:211], v[154:157]
	v_mfma_f32_16x16x128_f8f6f4 v[146:149], v[26:33], v[204:211], v[146:149]
	v_mfma_f32_16x16x128_f8f6f4 v[138:141], v[18:25], v[212:219], v[138:141]
	v_mfma_f32_16x16x128_f8f6f4 v[130:133], v[26:33], v[212:219], v[130:133]
	v_mfma_f32_16x16x128_f8f6f4 v[122:125], v[18:25], v[220:227], v[122:125]
	v_mfma_f32_16x16x128_f8f6f4 v[114:117], v[26:33], v[220:227], v[114:117]
	v_mfma_f32_16x16x128_f8f6f4 v[106:109], v[18:25], v[228:235], v[106:109]
	v_mfma_f32_16x16x128_f8f6f4 v[98:101], v[26:33], v[228:235], v[98:101]
	s_setprio 0
	s_barrier
	s_add_i32 s46, s46, s52
	v_lshl_add_u64 v[184:185], v[184:185], 0, s[16:17]
	s_mov_b32 m0, s46
	ds_read_b128 v[204:207], v199 offset:49152
	ds_read_b128 v[208:211], v199 offset:50176
	ds_read_b128 v[212:215], v199 offset:51200
	ds_read_b128 v[216:219], v199 offset:52224
	ds_read_b128 v[220:223], v199 offset:53248
	ds_read_b128 v[224:227], v199 offset:54272
	ds_read_b128 v[228:231], v199 offset:55296
	ds_read_b128 v[232:235], v199 offset:56320
	global_load_lds_dwordx4 v[184:185], off
	s_add_i32 m0, s46, 0x2000
	s_add_u32 s44, s44, 0x20080
	v_lshl_add_u64 v[184:185], v[186:187], 0, s[16:17]
	s_addc_u32 s45, s45, 0
	s_add_i32 s46, s47, s52
	global_load_lds_dwordx4 v[184:185], off
	v_lshl_add_u64 v[184:185], s[44:45], 0, v[164:165]
	s_mov_b32 m0, s46
	s_nop 0
	global_load_lds_dwordx4 v[184:185], off
	v_lshl_add_u64 v[184:185], s[44:45], 0, v[166:167]
	s_add_i32 m0, s46, 0x2000
	s_nop 0
	global_load_lds_dwordx4 v[184:185], off
	v_lshl_add_u64 v[184:185], v[190:191], 0, s[16:17]
	s_mov_b32 m0, s63
	s_nop 0
	global_load_lds_dwordx4 v[184:185], off
	v_lshl_add_u64 v[184:185], v[188:189], 0, s[16:17]
	s_mov_b32 m0, s64
	s_nop 0
	global_load_lds_dwordx4 v[184:185], off
	s_waitcnt vmcnt(8)
	s_waitcnt lgkmcnt(0)
	s_barrier
	s_setprio 1
	s_waitcnt lgkmcnt(0)
	v_mfma_f32_16x16x128_f8f6f4 v[94:97], v[2:9], v[204:211], v[94:97]
	v_mfma_f32_16x16x128_f8f6f4 v[86:89], v[10:17], v[204:211], v[86:89]
	v_mfma_f32_16x16x128_f8f6f4 v[78:81], v[2:9], v[212:219], v[78:81]
	v_mfma_f32_16x16x128_f8f6f4 v[70:73], v[10:17], v[212:219], v[70:73]
	v_mfma_f32_16x16x128_f8f6f4 v[58:61], v[2:9], v[220:227], v[58:61]
	v_mfma_f32_16x16x128_f8f6f4 v[46:49], v[10:17], v[220:227], v[46:49]
	v_mfma_f32_16x16x128_f8f6f4 v[38:41], v[2:9], v[228:235], v[38:41]
	v_mfma_f32_16x16x128_f8f6f4 v[34:37], v[10:17], v[228:235], v[34:37]
	s_setprio 0
	s_setprio 1
	v_mfma_f32_16x16x128_f8f6f4 v[90:93], v[18:25], v[204:211], v[90:93]
	v_mfma_f32_16x16x128_f8f6f4 v[82:85], v[26:33], v[204:211], v[82:85]
	v_mfma_f32_16x16x128_f8f6f4 v[74:77], v[18:25], v[212:219], v[74:77]
	v_mfma_f32_16x16x128_f8f6f4 v[66:69], v[26:33], v[212:219], v[66:69]
	v_mfma_f32_16x16x128_f8f6f4 v[50:53], v[18:25], v[220:227], v[50:53]
	v_mfma_f32_16x16x128_f8f6f4 v[42:45], v[26:33], v[220:227], v[42:45]
	v_mfma_f32_16x16x128_f8f6f4 v[62:65], v[18:25], v[228:235], v[62:65]
	v_mfma_f32_16x16x128_f8f6f4 v[54:57], v[26:33], v[228:235], v[54:57]
	s_setprio 0
	s_barrier
	s_add_i32 s79, s79, 2
	s_cmp_gt_u32 s79, 5
	s_mov_b64 s[46:47], s[42:43]
.LBB0_1911:
	ds_read_b128 v[18:21], v197
	ds_read_b128 v[22:25], v197 offset:1024
	ds_read_b128 v[26:29], v197 offset:2048
	ds_read_b128 v[30:33], v197 offset:3072
	ds_read_b128 v[2:5], v198
	ds_read_b128 v[6:9], v198 offset:1024
	ds_read_b128 v[10:13], v198 offset:2048
	ds_read_b128 v[14:17], v198 offset:3072
	s_add_u32 s42, s46, 0x100
	s_addc_u32 s43, s47, 0
	s_add_u32 s48, s37, s46
	s_addc_u32 s49, s80, s47
	s_cmpk_eq_i32 s46, 0x300
	s_cselect_b64 vcc, -1, 0
	s_and_b64 s[44:45], vcc, exec
	s_cselect_b32 s81, 0, s42
	s_cselect_b32 s76, 0, s43
	s_cselect_b32 s44, s38, s48
	s_cselect_b32 s45, s39, s49
	s_add_u32 s48, s8, s81
	s_addc_u32 s49, s9, s76
	v_lshl_add_u64 v[228:229], v[180:181], 0, s[46:47]
	s_add_i32 m0, s41, 0xc000
	ds_read_b128 v[184:187], v199
	ds_read_b128 v[188:191], v199 offset:1024
	ds_read_b128 v[204:207], v199 offset:2048
	ds_read_b128 v[208:211], v199 offset:3072
	ds_read_b128 v[212:215], v199 offset:4096
	ds_read_b128 v[216:219], v199 offset:5120
	ds_read_b128 v[220:223], v199 offset:6144
	ds_read_b128 v[224:227], v199 offset:7168
	global_load_lds_dwordx4 v[228:229], off
	v_lshl_add_u64 v[228:229], v[182:183], 0, s[46:47]
	s_add_i32 m0, s41, 0xe000
	s_nop 0
	global_load_lds_dwordx4 v[228:229], off
	s_waitcnt vmcnt(8)
	s_waitcnt lgkmcnt(0)
	s_barrier
	s_setprio 1
	s_waitcnt lgkmcnt(0)
	v_mfma_f32_16x16x128_f8f6f4 v[158:161], v[18:25], v[184:191], v[158:161]
	v_mfma_f32_16x16x128_f8f6f4 v[150:153], v[26:33], v[184:191], v[150:153]
	v_mfma_f32_16x16x128_f8f6f4 v[142:145], v[18:25], v[204:211], v[142:145]
	v_mfma_f32_16x16x128_f8f6f4 v[134:137], v[26:33], v[204:211], v[134:137]
	v_mfma_f32_16x16x128_f8f6f4 v[126:129], v[18:25], v[212:219], v[126:129]
	v_mfma_f32_16x16x128_f8f6f4 v[118:121], v[26:33], v[212:219], v[118:121]
	v_mfma_f32_16x16x128_f8f6f4 v[110:113], v[18:25], v[220:227], v[110:113]
	v_mfma_f32_16x16x128_f8f6f4 v[102:105], v[26:33], v[220:227], v[102:105]
	s_setprio 0
	s_setprio 1
	v_mfma_f32_16x16x128_f8f6f4 v[154:157], v[2:9], v[184:191], v[154:157]
	v_mfma_f32_16x16x128_f8f6f4 v[146:149], v[10:17], v[184:191], v[146:149]
	v_mfma_f32_16x16x128_f8f6f4 v[138:141], v[2:9], v[204:211], v[138:141]
	v_mfma_f32_16x16x128_f8f6f4 v[130:133], v[10:17], v[204:211], v[130:133]
	v_mfma_f32_16x16x128_f8f6f4 v[122:125], v[2:9], v[212:219], v[122:125]
	v_mfma_f32_16x16x128_f8f6f4 v[114:117], v[10:17], v[212:219], v[114:117]
	v_mfma_f32_16x16x128_f8f6f4 v[106:109], v[2:9], v[220:227], v[106:109]
	v_mfma_f32_16x16x128_f8f6f4 v[98:101], v[10:17], v[220:227], v[98:101]
	s_setprio 0
	s_barrier
	s_add_i32 s46, s5, s52
	v_lshl_add_u64 v[184:185], s[44:45], 0, v[164:165]
	s_mov_b32 m0, s46
	ds_read_b128 v[204:207], v199 offset:16384
	ds_read_b128 v[208:211], v199 offset:17408
	ds_read_b128 v[212:215], v199 offset:18432
	ds_read_b128 v[216:219], v199 offset:19456
	ds_read_b128 v[220:223], v199 offset:20480
	ds_read_b128 v[224:227], v199 offset:21504
	ds_read_b128 v[228:231], v199 offset:22528
	ds_read_b128 v[232:235], v199 offset:23552
	global_load_lds_dwordx4 v[184:185], off
	s_add_i32 m0, s46, 0x2000
	s_add_u32 s46, s44, 0x20000
	v_lshl_add_u64 v[186:187], s[44:45], 0, v[166:167]
	s_addc_u32 s47, s45, 0
	s_add_i32 s76, s66, s52
	global_load_lds_dwordx4 v[186:187], off
	v_lshl_add_u64 v[188:189], s[46:47], 0, v[164:165]
	s_mov_b32 m0, s76
	v_cndmask_b32_e32 v168, v202, v179, vcc
	global_load_lds_dwordx4 v[188:189], off
	v_lshl_add_u64 v[188:189], s[46:47], 0, v[166:167]
	s_add_i32 m0, s76, 0x2000
	v_lshl_add_u64 v[190:191], s[48:49], 0, v[168:169]
	global_load_lds_dwordx4 v[188:189], off
	s_mov_b32 m0, s41
	v_cndmask_b32_e32 v188, v176, v201, vcc
	global_load_lds_dwordx4 v168, s[48:49]
	s_mov_b32 m0, s53
	v_mov_b32_e32 v189, v169
	global_load_lds_dwordx4 v188, s[48:49]
	s_waitcnt vmcnt(8)
	s_waitcnt lgkmcnt(0)
	v_lshl_or_b32 v179, v236, 10, v194
	v_lshl_or_b32 v175, v237, 10, v194
	v_lshl_or_b32 v201, v238, 10, v194
	v_lshl_or_b32 v200, v239, 10, v194
	v_lshl_add_u64 v[188:189], s[48:49], 0, v[188:189]
	s_barrier
	s_setprio 1
	s_waitcnt lgkmcnt(0)
	v_mfma_f32_16x16x128_f8f6f4 v[94:97], v[18:25], v[204:211], v[94:97]
	v_mfma_f32_16x16x128_f8f6f4 v[86:89], v[26:33], v[204:211], v[86:89]
	v_mfma_f32_16x16x128_f8f6f4 v[78:81], v[18:25], v[212:219], v[78:81]
	v_mfma_f32_16x16x128_f8f6f4 v[70:73], v[26:33], v[212:219], v[70:73]
	v_mfma_f32_16x16x128_f8f6f4 v[58:61], v[18:25], v[220:227], v[58:61]
	v_mfma_f32_16x16x128_f8f6f4 v[46:49], v[26:33], v[220:227], v[46:49]
	v_mfma_f32_16x16x128_f8f6f4 v[38:41], v[18:25], v[228:235], v[38:41]
	v_mfma_f32_16x16x128_f8f6f4 v[34:37], v[26:33], v[228:235], v[34:37]
	s_setprio 0
	s_setprio 1
	v_mfma_f32_16x16x128_f8f6f4 v[90:93], v[2:9], v[204:211], v[90:93]
	v_mfma_f32_16x16x128_f8f6f4 v[82:85], v[10:17], v[204:211], v[82:85]
	v_mfma_f32_16x16x128_f8f6f4 v[74:77], v[2:9], v[212:219], v[74:77]
	v_mfma_f32_16x16x128_f8f6f4 v[66:69], v[10:17], v[212:219], v[66:69]
	v_mfma_f32_16x16x128_f8f6f4 v[50:53], v[2:9], v[220:227], v[50:53]
	v_mfma_f32_16x16x128_f8f6f4 v[42:45], v[10:17], v[220:227], v[42:45]
	v_mfma_f32_16x16x128_f8f6f4 v[62:65], v[2:9], v[228:235], v[62:65]
	v_mfma_f32_16x16x128_f8f6f4 v[54:57], v[10:17], v[228:235], v[54:57]
	s_setprio 0
	s_barrier
	s_add_i32 s46, 0, 0x18000
	s_add_i32 s47, 0, 0x1c000
	v_add_u32_e32 v14, s46, v177
	v_add_u32_e32 v30, s47, v177
	ds_read_b128 v[2:5], v14
	ds_read_b128 v[6:9], v14 offset:1024
	ds_read_b128 v[10:13], v14 offset:2048
	ds_read_b128 v[14:17], v14 offset:3072
	ds_read_b128 v[18:21], v30
	ds_read_b128 v[22:25], v30 offset:1024
	ds_read_b128 v[26:29], v30 offset:2048
	ds_read_b128 v[30:33], v30 offset:3072
	s_mov_b32 m0, s59
	v_cndmask_b32_e32 v168, v174, v175, vcc
	ds_read_b128 v[204:207], v199 offset:32768
	ds_read_b128 v[208:211], v199 offset:33792
	ds_read_b128 v[212:215], v199 offset:34816
	ds_read_b128 v[216:219], v199 offset:35840
	ds_read_b128 v[220:223], v199 offset:36864
	ds_read_b128 v[224:227], v199 offset:37888
	ds_read_b128 v[228:231], v199 offset:38912
	ds_read_b128 v[232:235], v199 offset:39936
	v_cndmask_b32_e32 v170, v178, v200, vcc
	global_load_lds_dwordx4 v168, s[48:49]
	s_mov_b32 m0, s60
	s_nop 0
	global_load_lds_dwordx4 v170, s[48:49]
	s_waitcnt vmcnt(8)
	s_waitcnt lgkmcnt(0)
	s_barrier
	s_setprio 1
	s_waitcnt lgkmcnt(0)
	v_mfma_f32_16x16x128_f8f6f4 v[158:161], v[2:9], v[204:211], v[158:161]
	v_mfma_f32_16x16x128_f8f6f4 v[150:153], v[10:17], v[204:211], v[150:153]
	v_mfma_f32_16x16x128_f8f6f4 v[142:145], v[2:9], v[212:219], v[142:145]
	v_mfma_f32_16x16x128_f8f6f4 v[134:137], v[10:17], v[212:219], v[134:137]
	v_mfma_f32_16x16x128_f8f6f4 v[126:129], v[2:9], v[220:227], v[126:129]
	v_mfma_f32_16x16x128_f8f6f4 v[118:121], v[10:17], v[220:227], v[118:121]
	v_mfma_f32_16x16x128_f8f6f4 v[110:113], v[2:9], v[228:235], v[110:113]
	v_mfma_f32_16x16x128_f8f6f4 v[102:105], v[10:17], v[228:235], v[102:105]
	s_setprio 0
	s_setprio 1
	v_mfma_f32_16x16x128_f8f6f4 v[154:157], v[18:25], v[204:211], v[154:157]
	v_mfma_f32_16x16x128_f8f6f4 v[146:149], v[26:33], v[204:211], v[146:149]
	v_mfma_f32_16x16x128_f8f6f4 v[138:141], v[18:25], v[212:219], v[138:141]
	v_mfma_f32_16x16x128_f8f6f4 v[130:133], v[26:33], v[212:219], v[130:133]
	v_mfma_f32_16x16x128_f8f6f4 v[122:125], v[18:25], v[220:227], v[122:125]
	v_mfma_f32_16x16x128_f8f6f4 v[114:117], v[26:33], v[220:227], v[114:117]
	v_mfma_f32_16x16x128_f8f6f4 v[106:109], v[18:25], v[228:235], v[106:109]
	v_mfma_f32_16x16x128_f8f6f4 v[98:101], v[26:33], v[228:235], v[98:101]
	s_setprio 0
	s_barrier
	s_add_i32 s46, s46, s52
	v_lshl_add_u64 v[184:185], v[184:185], 0, s[16:17]
	s_mov_b32 m0, s46
	ds_read_b128 v[204:207], v199 offset:49152
	ds_read_b128 v[208:211], v199 offset:50176
	ds_read_b128 v[212:215], v199 offset:51200
	ds_read_b128 v[216:219], v199 offset:52224
	ds_read_b128 v[220:223], v199 offset:53248
	ds_read_b128 v[224:227], v199 offset:54272
	ds_read_b128 v[228:231], v199 offset:55296
	ds_read_b128 v[232:235], v199 offset:56320
	global_load_lds_dwordx4 v[184:185], off
	s_add_i32 m0, s46, 0x2000
	s_add_u32 s44, s44, 0x20080
	v_lshl_add_u64 v[184:185], v[186:187], 0, s[16:17]
	s_addc_u32 s45, s45, 0
	s_add_i32 s46, s47, s52
	global_load_lds_dwordx4 v[184:185], off
	v_lshl_add_u64 v[184:185], s[44:45], 0, v[164:165]
	s_mov_b32 m0, s46
	s_nop 0
	global_load_lds_dwordx4 v[184:185], off
	v_lshl_add_u64 v[184:185], s[44:45], 0, v[166:167]
	s_add_i32 m0, s46, 0x2000
	s_nop 0
	global_load_lds_dwordx4 v[184:185], off
	v_lshl_add_u64 v[184:185], v[190:191], 0, s[16:17]
	s_mov_b32 m0, s63
	s_nop 0
	global_load_lds_dwordx4 v[184:185], off
	v_lshl_add_u64 v[184:185], v[188:189], 0, s[16:17]
	s_mov_b32 m0, s64
	s_nop 0
	global_load_lds_dwordx4 v[184:185], off
	s_waitcnt vmcnt(8)
	s_waitcnt lgkmcnt(0)
	s_barrier
	s_setprio 1
	s_waitcnt lgkmcnt(0)
	v_mfma_f32_16x16x128_f8f6f4 v[94:97], v[2:9], v[204:211], v[94:97]
	v_mfma_f32_16x16x128_f8f6f4 v[86:89], v[10:17], v[204:211], v[86:89]
	v_mfma_f32_16x16x128_f8f6f4 v[78:81], v[2:9], v[212:219], v[78:81]
	v_mfma_f32_16x16x128_f8f6f4 v[70:73], v[10:17], v[212:219], v[70:73]
	v_mfma_f32_16x16x128_f8f6f4 v[58:61], v[2:9], v[220:227], v[58:61]
	v_mfma_f32_16x16x128_f8f6f4 v[46:49], v[10:17], v[220:227], v[46:49]
	v_mfma_f32_16x16x128_f8f6f4 v[38:41], v[2:9], v[228:235], v[38:41]
	v_mfma_f32_16x16x128_f8f6f4 v[34:37], v[10:17], v[228:235], v[34:37]
	s_setprio 0
	s_setprio 1
	v_mfma_f32_16x16x128_f8f6f4 v[90:93], v[18:25], v[204:211], v[90:93]
	v_mfma_f32_16x16x128_f8f6f4 v[82:85], v[26:33], v[204:211], v[82:85]
	v_mfma_f32_16x16x128_f8f6f4 v[74:77], v[18:25], v[212:219], v[74:77]
	v_mfma_f32_16x16x128_f8f6f4 v[66:69], v[26:33], v[212:219], v[66:69]
	v_mfma_f32_16x16x128_f8f6f4 v[50:53], v[18:25], v[220:227], v[50:53]
	v_mfma_f32_16x16x128_f8f6f4 v[42:45], v[26:33], v[220:227], v[42:45]
	v_mfma_f32_16x16x128_f8f6f4 v[62:65], v[18:25], v[228:235], v[62:65]
	v_mfma_f32_16x16x128_f8f6f4 v[54:57], v[26:33], v[228:235], v[54:57]
	s_setprio 0
	s_barrier
	s_add_i32 s79, s79, 2
	s_cmp_gt_u32 s79, 5
	s_mov_b64 s[46:47], s[42:43]
	s_cbranch_scc0 .LBB0_1911
	s_and_b64 vcc, exec, s[20:21]
	s_cbranch_vccz .LBB0_1914
	s_barrier
.LBB0_1914:
	s_mov_b32 s100, 0xbcb8aa3b
	s_mov_b32 s101, 0x45800000
	v_pk_mul_f32 v[16:17], v[158:159], s[100:101] op_sel_hi:[1,0]
	v_pk_mul_f32 v[18:19], v[160:161], s[100:101] op_sel_hi:[1,0]
	v_pk_mul_f32 v[20:21], v[150:151], s[100:101] op_sel_hi:[1,0]
	v_pk_mul_f32 v[22:23], v[152:153], s[100:101] op_sel_hi:[1,0]
	v_exp_f32_e32 v16, v16
	v_exp_f32_e32 v17, v17
	v_exp_f32_e32 v18, v18
	v_exp_f32_e32 v19, v19
	v_exp_f32_e32 v20, v20
	v_exp_f32_e32 v21, v21
	v_exp_f32_e32 v22, v22
	v_exp_f32_e32 v23, v23
	v_pk_fma_f32 v[16:17], v[16:17], s[100:101], s[100:101] op_sel:[0,1,1] op_sel_hi:[1,1,1]
	v_pk_fma_f32 v[18:19], v[18:19], s[100:101], s[100:101] op_sel:[0,1,1] op_sel_hi:[1,1,1]
	v_pk_fma_f32 v[20:21], v[20:21], s[100:101], s[100:101] op_sel:[0,1,1] op_sel_hi:[1,1,1]
	v_pk_fma_f32 v[22:23], v[22:23], s[100:101], s[100:101] op_sel:[0,1,1] op_sel_hi:[1,1,1]
	v_rcp_f32_e32 v16, v16
	v_rcp_f32_e32 v17, v17
	v_rcp_f32_e32 v18, v18
	v_rcp_f32_e32 v19, v19
	v_rcp_f32_e32 v20, v20
	v_rcp_f32_e32 v21, v21
	v_rcp_f32_e32 v22, v22
	v_rcp_f32_e32 v23, v23
	v_pk_mul_f32 v[158:159], v[158:159], v[154:155]
	v_pk_mul_f32 v[160:161], v[160:161], v[156:157]
	v_pk_mul_f32 v[150:151], v[150:151], v[146:147]
	v_pk_mul_f32 v[152:153], v[152:153], v[148:149]
	v_pk_mul_f32 v[158:159], v[158:159], v[16:17]
	v_pk_mul_f32 v[160:161], v[160:161], v[18:19]
	v_pk_mul_f32 v[150:151], v[150:151], v[20:21]
	v_pk_mul_f32 v[152:153], v[152:153], v[22:23]
	v_cvt_pk_fp8_f32 v8, v158, v159
	v_cvt_pk_fp8_f32 v9, v150, v151
	v_cvt_pk_fp8_f32 v8, v160, v161 op_sel:[0,0,1]
	v_cvt_pk_fp8_f32 v9, v152, v153 op_sel:[0,0,1]
	v_pk_mul_f32 v[16:17], v[142:143], s[100:101] op_sel_hi:[1,0]
	v_pk_mul_f32 v[18:19], v[144:145], s[100:101] op_sel_hi:[1,0]
	v_pk_mul_f32 v[20:21], v[134:135], s[100:101] op_sel_hi:[1,0]
	v_pk_mul_f32 v[22:23], v[136:137], s[100:101] op_sel_hi:[1,0]
	v_exp_f32_e32 v16, v16
	v_exp_f32_e32 v17, v17
	v_exp_f32_e32 v18, v18
	v_exp_f32_e32 v19, v19
	v_exp_f32_e32 v20, v20
	v_exp_f32_e32 v21, v21
	v_exp_f32_e32 v22, v22
	v_exp_f32_e32 v23, v23
	v_pk_fma_f32 v[16:17], v[16:17], s[100:101], s[100:101] op_sel:[0,1,1] op_sel_hi:[1,1,1]
	v_pk_fma_f32 v[18:19], v[18:19], s[100:101], s[100:101] op_sel:[0,1,1] op_sel_hi:[1,1,1]
	v_pk_fma_f32 v[20:21], v[20:21], s[100:101], s[100:101] op_sel:[0,1,1] op_sel_hi:[1,1,1]
	v_pk_fma_f32 v[22:23], v[22:23], s[100:101], s[100:101] op_sel:[0,1,1] op_sel_hi:[1,1,1]
	v_rcp_f32_e32 v16, v16
	v_rcp_f32_e32 v17, v17
	v_rcp_f32_e32 v18, v18
	v_rcp_f32_e32 v19, v19
	v_rcp_f32_e32 v20, v20
	v_rcp_f32_e32 v21, v21
	v_rcp_f32_e32 v22, v22
	v_rcp_f32_e32 v23, v23
	v_pk_mul_f32 v[142:143], v[142:143], v[138:139]
	v_pk_mul_f32 v[144:145], v[144:145], v[140:141]
	v_pk_mul_f32 v[134:135], v[134:135], v[130:131]
	v_pk_mul_f32 v[136:137], v[136:137], v[132:133]
	v_pk_mul_f32 v[142:143], v[142:143], v[16:17]
	v_pk_mul_f32 v[144:145], v[144:145], v[18:19]
	v_pk_mul_f32 v[134:135], v[134:135], v[20:21]
	v_pk_mul_f32 v[136:137], v[136:137], v[22:23]
	v_cvt_pk_fp8_f32 v10, v142, v143
	v_cvt_pk_fp8_f32 v11, v134, v135
	v_cvt_pk_fp8_f32 v10, v144, v145 op_sel:[0,0,1]
	v_cvt_pk_fp8_f32 v11, v136, v137 op_sel:[0,0,1]
	v_lshl_or_b32 v2, s40, 7, v196
	v_lshl_add_u32 v6, s78, 8, v195
	v_mov_b64_e32 v[4:5], s[14:15]
	v_ashrrev_i32_e32 v3, 31, v2
	v_mad_i64_i32 v[14:15], s[42:43], v6, s67, v[4:5]
	v_permlane16_swap_b32_e32 v8, v10
	v_permlane16_swap_b32_e32 v9, v11
	v_lshl_add_u64 v[14:15], v[14:15], 0, v[2:3]
	global_store_dwordx4 v[14:15], v[8:11], off
	v_pk_mul_f32 v[16:17], v[126:127], s[100:101] op_sel_hi:[1,0]
	v_pk_mul_f32 v[18:19], v[128:129], s[100:101] op_sel_hi:[1,0]
	v_pk_mul_f32 v[20:21], v[118:119], s[100:101] op_sel_hi:[1,0]
	v_pk_mul_f32 v[22:23], v[120:121], s[100:101] op_sel_hi:[1,0]
	v_exp_f32_e32 v16, v16
	v_exp_f32_e32 v17, v17
	v_exp_f32_e32 v18, v18
	v_exp_f32_e32 v19, v19
	v_exp_f32_e32 v20, v20
	v_exp_f32_e32 v21, v21
	v_exp_f32_e32 v22, v22
	v_exp_f32_e32 v23, v23
	v_pk_fma_f32 v[16:17], v[16:17], s[100:101], s[100:101] op_sel:[0,1,1] op_sel_hi:[1,1,1]
	v_pk_fma_f32 v[18:19], v[18:19], s[100:101], s[100:101] op_sel:[0,1,1] op_sel_hi:[1,1,1]
	v_pk_fma_f32 v[20:21], v[20:21], s[100:101], s[100:101] op_sel:[0,1,1] op_sel_hi:[1,1,1]
	v_pk_fma_f32 v[22:23], v[22:23], s[100:101], s[100:101] op_sel:[0,1,1] op_sel_hi:[1,1,1]
	v_rcp_f32_e32 v16, v16
	v_rcp_f32_e32 v17, v17
	v_rcp_f32_e32 v18, v18
	v_rcp_f32_e32 v19, v19
	v_rcp_f32_e32 v20, v20
	v_rcp_f32_e32 v21, v21
	v_rcp_f32_e32 v22, v22
	v_rcp_f32_e32 v23, v23
	v_pk_mul_f32 v[126:127], v[126:127], v[122:123]
	v_pk_mul_f32 v[128:129], v[128:129], v[124:125]
	v_pk_mul_f32 v[118:119], v[118:119], v[114:115]
	v_pk_mul_f32 v[120:121], v[120:121], v[116:117]
	v_pk_mul_f32 v[126:127], v[126:127], v[16:17]
	v_pk_mul_f32 v[128:129], v[128:129], v[18:19]
	v_pk_mul_f32 v[118:119], v[118:119], v[20:21]
	v_pk_mul_f32 v[120:121], v[120:121], v[22:23]
	v_cvt_pk_fp8_f32 v8, v126, v127
	v_cvt_pk_fp8_f32 v9, v118, v119
	v_cvt_pk_fp8_f32 v8, v128, v129 op_sel:[0,0,1]
	v_cvt_pk_fp8_f32 v9, v120, v121 op_sel:[0,0,1]
	v_pk_mul_f32 v[16:17], v[110:111], s[100:101] op_sel_hi:[1,0]
	v_pk_mul_f32 v[18:19], v[112:113], s[100:101] op_sel_hi:[1,0]
	v_pk_mul_f32 v[20:21], v[102:103], s[100:101] op_sel_hi:[1,0]
	v_pk_mul_f32 v[22:23], v[104:105], s[100:101] op_sel_hi:[1,0]
	v_exp_f32_e32 v16, v16
	v_exp_f32_e32 v17, v17
	v_exp_f32_e32 v18, v18
	v_exp_f32_e32 v19, v19
	v_exp_f32_e32 v20, v20
	v_exp_f32_e32 v21, v21
	v_exp_f32_e32 v22, v22
	v_exp_f32_e32 v23, v23
	v_pk_fma_f32 v[16:17], v[16:17], s[100:101], s[100:101] op_sel:[0,1,1] op_sel_hi:[1,1,1]
	v_pk_fma_f32 v[18:19], v[18:19], s[100:101], s[100:101] op_sel:[0,1,1] op_sel_hi:[1,1,1]
	v_pk_fma_f32 v[20:21], v[20:21], s[100:101], s[100:101] op_sel:[0,1,1] op_sel_hi:[1,1,1]
	v_pk_fma_f32 v[22:23], v[22:23], s[100:101], s[100:101] op_sel:[0,1,1] op_sel_hi:[1,1,1]
	v_rcp_f32_e32 v16, v16
	v_rcp_f32_e32 v17, v17
	v_rcp_f32_e32 v18, v18
	v_rcp_f32_e32 v19, v19
	v_rcp_f32_e32 v20, v20
	v_rcp_f32_e32 v21, v21
	v_rcp_f32_e32 v22, v22
	v_rcp_f32_e32 v23, v23
	v_pk_mul_f32 v[110:111], v[110:111], v[106:107]
	v_pk_mul_f32 v[112:113], v[112:113], v[108:109]
	v_pk_mul_f32 v[102:103], v[102:103], v[98:99]
	v_pk_mul_f32 v[104:105], v[104:105], v[100:101]
	v_pk_mul_f32 v[110:111], v[110:111], v[16:17]
	v_pk_mul_f32 v[112:113], v[112:113], v[18:19]
	v_pk_mul_f32 v[102:103], v[102:103], v[20:21]
	v_pk_mul_f32 v[104:105], v[104:105], v[22:23]
	v_cvt_pk_fp8_f32 v10, v110, v111
	v_cvt_pk_fp8_f32 v11, v102, v103
	v_cvt_pk_fp8_f32 v10, v112, v113 op_sel:[0,0,1]
	v_cvt_pk_fp8_f32 v11, v104, v105 op_sel:[0,0,1]
	v_or_b32_e32 v7, 32, v6
	v_mad_i64_i32 v[12:13], s[42:43], v7, s67, v[4:5]
	v_permlane16_swap_b32_e32 v8, v10
	v_permlane16_swap_b32_e32 v9, v11
	v_lshl_add_u64 v[12:13], v[12:13], 0, v[2:3]
	global_store_dwordx4 v[12:13], v[8:11], off
	v_pk_mul_f32 v[16:17], v[94:95], s[100:101] op_sel_hi:[1,0]
	v_pk_mul_f32 v[18:19], v[96:97], s[100:101] op_sel_hi:[1,0]
	v_pk_mul_f32 v[20:21], v[86:87], s[100:101] op_sel_hi:[1,0]
	v_pk_mul_f32 v[22:23], v[88:89], s[100:101] op_sel_hi:[1,0]
	v_exp_f32_e32 v16, v16
	v_exp_f32_e32 v17, v17
	v_exp_f32_e32 v18, v18
	v_exp_f32_e32 v19, v19
	v_exp_f32_e32 v20, v20
	v_exp_f32_e32 v21, v21
	v_exp_f32_e32 v22, v22
	v_exp_f32_e32 v23, v23
	v_pk_fma_f32 v[16:17], v[16:17], s[100:101], s[100:101] op_sel:[0,1,1] op_sel_hi:[1,1,1]
	v_pk_fma_f32 v[18:19], v[18:19], s[100:101], s[100:101] op_sel:[0,1,1] op_sel_hi:[1,1,1]
	v_pk_fma_f32 v[20:21], v[20:21], s[100:101], s[100:101] op_sel:[0,1,1] op_sel_hi:[1,1,1]
	v_pk_fma_f32 v[22:23], v[22:23], s[100:101], s[100:101] op_sel:[0,1,1] op_sel_hi:[1,1,1]
	v_rcp_f32_e32 v16, v16
	v_rcp_f32_e32 v17, v17
	v_rcp_f32_e32 v18, v18
	v_rcp_f32_e32 v19, v19
	v_rcp_f32_e32 v20, v20
	v_rcp_f32_e32 v21, v21
	v_rcp_f32_e32 v22, v22
	v_rcp_f32_e32 v23, v23
	v_pk_mul_f32 v[94:95], v[94:95], v[90:91]
	v_pk_mul_f32 v[96:97], v[96:97], v[92:93]
	v_pk_mul_f32 v[86:87], v[86:87], v[82:83]
	v_pk_mul_f32 v[88:89], v[88:89], v[84:85]
	v_pk_mul_f32 v[94:95], v[94:95], v[16:17]
	v_pk_mul_f32 v[96:97], v[96:97], v[18:19]
	v_pk_mul_f32 v[86:87], v[86:87], v[20:21]
	v_pk_mul_f32 v[88:89], v[88:89], v[22:23]
	v_cvt_pk_fp8_f32 v8, v94, v95
	v_cvt_pk_fp8_f32 v9, v86, v87
	v_cvt_pk_fp8_f32 v8, v96, v97 op_sel:[0,0,1]
	v_cvt_pk_fp8_f32 v9, v88, v89 op_sel:[0,0,1]
	v_pk_mul_f32 v[16:17], v[78:79], s[100:101] op_sel_hi:[1,0]
	v_pk_mul_f32 v[18:19], v[80:81], s[100:101] op_sel_hi:[1,0]
	v_pk_mul_f32 v[20:21], v[70:71], s[100:101] op_sel_hi:[1,0]
	v_pk_mul_f32 v[22:23], v[72:73], s[100:101] op_sel_hi:[1,0]
	v_exp_f32_e32 v16, v16
	v_exp_f32_e32 v17, v17
	v_exp_f32_e32 v18, v18
	v_exp_f32_e32 v19, v19
	v_exp_f32_e32 v20, v20
	v_exp_f32_e32 v21, v21
	v_exp_f32_e32 v22, v22
	v_exp_f32_e32 v23, v23
	v_pk_fma_f32 v[16:17], v[16:17], s[100:101], s[100:101] op_sel:[0,1,1] op_sel_hi:[1,1,1]
	v_pk_fma_f32 v[18:19], v[18:19], s[100:101], s[100:101] op_sel:[0,1,1] op_sel_hi:[1,1,1]
	v_pk_fma_f32 v[20:21], v[20:21], s[100:101], s[100:101] op_sel:[0,1,1] op_sel_hi:[1,1,1]
	v_pk_fma_f32 v[22:23], v[22:23], s[100:101], s[100:101] op_sel:[0,1,1] op_sel_hi:[1,1,1]
	v_rcp_f32_e32 v16, v16
	v_rcp_f32_e32 v17, v17
	v_rcp_f32_e32 v18, v18
	v_rcp_f32_e32 v19, v19
	v_rcp_f32_e32 v20, v20
	v_rcp_f32_e32 v21, v21
	v_rcp_f32_e32 v22, v22
	v_rcp_f32_e32 v23, v23
	v_pk_mul_f32 v[78:79], v[78:79], v[74:75]
	v_pk_mul_f32 v[80:81], v[80:81], v[76:77]
	v_pk_mul_f32 v[70:71], v[70:71], v[66:67]
	v_pk_mul_f32 v[72:73], v[72:73], v[68:69]
	v_pk_mul_f32 v[78:79], v[78:79], v[16:17]
	v_pk_mul_f32 v[80:81], v[80:81], v[18:19]
	v_pk_mul_f32 v[70:71], v[70:71], v[20:21]
	v_pk_mul_f32 v[72:73], v[72:73], v[22:23]
	v_cvt_pk_fp8_f32 v10, v78, v79
	v_cvt_pk_fp8_f32 v11, v70, v71
	v_cvt_pk_fp8_f32 v10, v80, v81 op_sel:[0,0,1]
	v_cvt_pk_fp8_f32 v11, v72, v73 op_sel:[0,0,1]
	v_add_u32_e32 v7, 0x80, v6
	v_mad_i64_i32 v[12:13], s[42:43], v7, s67, v[4:5]
	v_permlane16_swap_b32_e32 v8, v10
	v_permlane16_swap_b32_e32 v9, v11
	v_lshl_add_u64 v[12:13], v[12:13], 0, v[2:3]
	global_store_dwordx4 v[12:13], v[8:11], off
	v_pk_mul_f32 v[16:17], v[58:59], s[100:101] op_sel_hi:[1,0]
	v_pk_mul_f32 v[18:19], v[60:61], s[100:101] op_sel_hi:[1,0]
	v_pk_mul_f32 v[20:21], v[46:47], s[100:101] op_sel_hi:[1,0]
	v_pk_mul_f32 v[22:23], v[48:49], s[100:101] op_sel_hi:[1,0]
	v_exp_f32_e32 v16, v16
	v_exp_f32_e32 v17, v17
	v_exp_f32_e32 v18, v18
	v_exp_f32_e32 v19, v19
	v_exp_f32_e32 v20, v20
	v_exp_f32_e32 v21, v21
	v_exp_f32_e32 v22, v22
	v_exp_f32_e32 v23, v23
	v_pk_fma_f32 v[16:17], v[16:17], s[100:101], s[100:101] op_sel:[0,1,1] op_sel_hi:[1,1,1]
	v_pk_fma_f32 v[18:19], v[18:19], s[100:101], s[100:101] op_sel:[0,1,1] op_sel_hi:[1,1,1]
	v_pk_fma_f32 v[20:21], v[20:21], s[100:101], s[100:101] op_sel:[0,1,1] op_sel_hi:[1,1,1]
	v_pk_fma_f32 v[22:23], v[22:23], s[100:101], s[100:101] op_sel:[0,1,1] op_sel_hi:[1,1,1]
	v_rcp_f32_e32 v16, v16
	v_rcp_f32_e32 v17, v17
	v_rcp_f32_e32 v18, v18
	v_rcp_f32_e32 v19, v19
	v_rcp_f32_e32 v20, v20
	v_rcp_f32_e32 v21, v21
	v_rcp_f32_e32 v22, v22
	v_rcp_f32_e32 v23, v23
	v_pk_mul_f32 v[58:59], v[58:59], v[50:51]
	v_pk_mul_f32 v[60:61], v[60:61], v[52:53]
	v_pk_mul_f32 v[46:47], v[46:47], v[42:43]
	v_pk_mul_f32 v[48:49], v[48:49], v[44:45]
	v_pk_mul_f32 v[58:59], v[58:59], v[16:17]
	v_pk_mul_f32 v[60:61], v[60:61], v[18:19]
	v_pk_mul_f32 v[46:47], v[46:47], v[20:21]
	v_pk_mul_f32 v[48:49], v[48:49], v[22:23]
	v_cvt_pk_fp8_f32 v8, v58, v59
	v_cvt_pk_fp8_f32 v9, v46, v47
	v_cvt_pk_fp8_f32 v8, v60, v61 op_sel:[0,0,1]
	v_cvt_pk_fp8_f32 v9, v48, v49 op_sel:[0,0,1]
	v_pk_mul_f32 v[16:17], v[38:39], s[100:101] op_sel_hi:[1,0]
	v_pk_mul_f32 v[18:19], v[40:41], s[100:101] op_sel_hi:[1,0]
	v_pk_mul_f32 v[20:21], v[34:35], s[100:101] op_sel_hi:[1,0]
	v_pk_mul_f32 v[22:23], v[36:37], s[100:101] op_sel_hi:[1,0]
	v_exp_f32_e32 v16, v16
	v_exp_f32_e32 v17, v17
	v_exp_f32_e32 v18, v18
	v_exp_f32_e32 v19, v19
	v_exp_f32_e32 v20, v20
	v_exp_f32_e32 v21, v21
	v_exp_f32_e32 v22, v22
	v_exp_f32_e32 v23, v23
	v_pk_fma_f32 v[16:17], v[16:17], s[100:101], s[100:101] op_sel:[0,1,1] op_sel_hi:[1,1,1]
	v_pk_fma_f32 v[18:19], v[18:19], s[100:101], s[100:101] op_sel:[0,1,1] op_sel_hi:[1,1,1]
	v_pk_fma_f32 v[20:21], v[20:21], s[100:101], s[100:101] op_sel:[0,1,1] op_sel_hi:[1,1,1]
	v_pk_fma_f32 v[22:23], v[22:23], s[100:101], s[100:101] op_sel:[0,1,1] op_sel_hi:[1,1,1]
	v_rcp_f32_e32 v16, v16
	v_rcp_f32_e32 v17, v17
	v_rcp_f32_e32 v18, v18
	v_rcp_f32_e32 v19, v19
	v_rcp_f32_e32 v20, v20
	v_rcp_f32_e32 v21, v21
	v_rcp_f32_e32 v22, v22
	v_rcp_f32_e32 v23, v23
	v_pk_mul_f32 v[38:39], v[38:39], v[62:63]
	v_pk_mul_f32 v[40:41], v[40:41], v[64:65]
	v_pk_mul_f32 v[34:35], v[34:35], v[54:55]
	v_pk_mul_f32 v[36:37], v[36:37], v[56:57]
	v_pk_mul_f32 v[38:39], v[38:39], v[16:17]
	v_pk_mul_f32 v[40:41], v[40:41], v[18:19]
	v_pk_mul_f32 v[34:35], v[34:35], v[20:21]
	v_pk_mul_f32 v[36:37], v[36:37], v[22:23]
	v_cvt_pk_fp8_f32 v10, v38, v39
	v_cvt_pk_fp8_f32 v11, v34, v35
	v_cvt_pk_fp8_f32 v10, v40, v41 op_sel:[0,0,1]
	v_cvt_pk_fp8_f32 v11, v36, v37 op_sel:[0,0,1]
	v_add_u32_e32 v6, 0xa0, v6
	v_mad_i64_i32 v[4:5], s[42:43], v6, s67, v[4:5]
	v_permlane16_swap_b32_e32 v8, v10
	v_permlane16_swap_b32_e32 v9, v11
	v_lshl_add_u64 v[2:3], v[4:5], 0, v[2:3]
	s_andn2_b64 vcc, exec, s[0:1]
	s_mov_b64 s[0:1], -1
	global_store_dwordx4 v[2:3], v[8:11], off
	s_cbranch_vccnz .LBB0_1903
	s_andn2_b64 vcc, exec, s[12:13]
	s_cbranch_vccnz .LBB0_1902
	s_barrier
	s_branch .LBB0_1902

.LBB0_2042:
	s_add_u32 s8, s72, 0xdd00000
	s_addc_u32 s9, s73, 0
	s_lshl_b32 s10, s10, 5
	s_lshl_b32 s14, s11, 6
	s_lshl_b32 s16, s11, 13
	s_and_b32 s17, s10, 0x60
	s_mov_b64 s[10:11], 0x80
	s_add_i32 m0, s38, 0x18000
	v_lshl_add_u64 v[8:9], v[8:9], 0, s[10:11]
	s_lshl_b32 s18, s17, 7
	s_waitcnt vmcnt(2)
	s_barrier
	global_load_lds_dwordx4 v[8:9], off
	v_lshl_add_u64 v[6:7], v[6:7], 0, s[10:11]
	s_add_i32 m0, s38, 0x1a000
	s_add_i32 s43, s38, 0x8000
	s_add_i32 s44, s38, 0xa000
	global_load_lds_dwordx4 v[6:7], off
	v_lshl_add_u64 v[2:3], v[2:3], 0, s[10:11]
	s_mov_b32 m0, s43
	s_add_u32 s12, s22, 0x70080
	global_load_lds_dwordx4 v[2:3], off
	v_lshl_add_u64 v[2:3], v[4:5], 0, s[10:11]
	s_mov_b32 m0, s44
	s_addc_u32 s13, s23, 0
	global_load_lds_dwordx4 v[2:3], off
	s_add_i32 m0, s38, 0x1c000
	v_lshl_add_u64 v[2:3], s[12:13], 0, v[166:167]
	global_load_lds_dwordx4 v[2:3], off
	v_lshl_add_u64 v[2:3], s[12:13], 0, v[162:163]
	s_add_i32 m0, s38, 0x1e000
	s_movk_i32 s12, 0x3c0
	global_load_lds_dwordx4 v[2:3], off
	v_and_b32_e32 v2, 48, v0
	v_lshlrev_b32_e32 v3, 6, v0
	v_and_or_b32 v2, v3, s12, v2
	v_lshlrev_b32_e32 v3, 2, v0
	v_and_b32_e32 v3, 32, v3
	s_waitcnt vmcnt(6)
	s_cmpk_lt_u32 s1, 0x100
	v_bitop3_b32 v4, v2, s16, v3 bitop3:0xde
	v_bitop3_b32 v186, s18, v2, v3 bitop3:0xf6
	s_cselect_b64 s[12:13], -1, 0
	s_ashr_i32 s1, s0, 31
	s_add_i32 s46, 0, 0x10000
	s_add_i32 s47, 0, 0x14000
	v_and_or_b32 v187, v0, 31, s14
	s_ashr_i32 s45, s28, 31
	v_and_or_b32 v188, v10, 16, s17
	v_add3_u32 v172, v14, v11, v12
	v_mov_b32_e32 v173, v167
	v_add3_u32 v174, v13, v11, v12
	v_mov_b32_e32 v175, v167
	v_mov_b64_e32 v[176:177], s[0:1]
	v_add_u32_e32 v189, s46, v186
	v_add_u32_e32 v190, s47, v186
	v_add_u32_e32 v191, 0, v4
	s_mov_b32 s14, 0x3e800000
	s_mov_b64 s[18:19], s[22:23]
	s_mov_b64 s[16:17], s[20:21]
	s_barrier
	s_branch .LBB0_2045

.LBB0_2047:
	s_add_u32 s20, s20, 0x70080
	s_addc_u32 s21, s21, 0
	s_add_u32 s52, s22, 0x100
	s_addc_u32 s53, s23, 0
	s_mov_b32 s59, -2
	ds_read_b128 v[18:21], v189
	ds_read_b128 v[22:25], v189 offset:1024
	ds_read_b128 v[26:29], v189 offset:2048
	ds_read_b128 v[30:33], v189 offset:3072
	ds_read_b128 v[2:5], v190
	ds_read_b128 v[6:9], v190 offset:1024
	ds_read_b128 v[10:13], v190 offset:2048
	ds_read_b128 v[14:17], v190 offset:3072
	s_add_u32 s22, s20, 0xfff90080
	s_addc_u32 s23, s21, -1
	s_cmp_eq_u32 s59, 24
	s_cselect_b32 s25, s17, s23
	s_cselect_b32 s24, s16, s22
	s_cselect_b32 s23, s19, s53
	s_cselect_b32 s22, s18, s52
	v_lshl_add_u64 v[216:217], s[20:21], 0, v[172:173]
	s_add_i32 m0, s38, 0xc000
	ds_read_b128 v[178:181], v191
	ds_read_b128 v[182:185], v191 offset:1024
	ds_read_b128 v[192:195], v191 offset:2048
	ds_read_b128 v[196:199], v191 offset:3072
	ds_read_b128 v[200:203], v191 offset:4096
	ds_read_b128 v[204:207], v191 offset:5120
	ds_read_b128 v[208:211], v191 offset:6144
	ds_read_b128 v[212:215], v191 offset:7168
	global_load_lds_dwordx4 v[216:217], off
	v_lshl_add_u64 v[216:217], s[20:21], 0, v[174:175]
	s_add_i32 m0, s38, 0xe000
	s_nop 0
	global_load_lds_dwordx4 v[216:217], off
	s_waitcnt vmcnt(8)
	s_waitcnt lgkmcnt(0)
	s_barrier
	s_setprio 1
	s_waitcnt lgkmcnt(0)
	v_mfma_f32_16x16x128_f8f6f4 v[158:161], v[18:25], v[178:185], 0
	v_mfma_f32_16x16x128_f8f6f4 v[154:157], v[26:33], v[178:185], 0
	v_mfma_f32_16x16x128_f8f6f4 v[150:153], v[18:25], v[192:199], 0
	v_mfma_f32_16x16x128_f8f6f4 v[146:149], v[26:33], v[192:199], 0
	v_mfma_f32_16x16x128_f8f6f4 v[142:145], v[18:25], v[200:207], 0
	v_mfma_f32_16x16x128_f8f6f4 v[138:141], v[26:33], v[200:207], 0
	v_mfma_f32_16x16x128_f8f6f4 v[134:137], v[18:25], v[208:215], 0
	v_mfma_f32_16x16x128_f8f6f4 v[130:133], v[26:33], v[208:215], 0
	s_setprio 0
	s_setprio 1
	v_mfma_f32_16x16x128_f8f6f4 v[126:129], v[2:9], v[178:185], 0
	v_mfma_f32_16x16x128_f8f6f4 v[122:125], v[10:17], v[178:185], 0
	v_mfma_f32_16x16x128_f8f6f4 v[118:121], v[2:9], v[192:199], 0
	v_mfma_f32_16x16x128_f8f6f4 v[114:117], v[10:17], v[192:199], 0
	v_mfma_f32_16x16x128_f8f6f4 v[110:113], v[2:9], v[200:207], 0
	v_mfma_f32_16x16x128_f8f6f4 v[106:109], v[10:17], v[200:207], 0
	v_mfma_f32_16x16x128_f8f6f4 v[102:105], v[2:9], v[208:215], 0
	v_mfma_f32_16x16x128_f8f6f4 v[98:101], v[10:17], v[208:215], 0
	s_setprio 0
	s_barrier
	s_add_i32 s60, s46, s35
	v_lshl_add_u64 v[178:179], s[22:23], 0, v[166:167]
	s_mov_b32 m0, s60
	ds_read_b128 v[192:195], v191 offset:16384
	ds_read_b128 v[196:199], v191 offset:17408
	ds_read_b128 v[200:203], v191 offset:18432
	ds_read_b128 v[204:207], v191 offset:19456
	ds_read_b128 v[208:211], v191 offset:20480
	ds_read_b128 v[212:215], v191 offset:21504
	ds_read_b128 v[216:219], v191 offset:22528
	ds_read_b128 v[220:223], v191 offset:23552
	global_load_lds_dwordx4 v[178:179], off
	s_add_i32 m0, s60, 0x2000
	s_add_u32 s60, s22, 0x70000
	v_lshl_add_u64 v[180:181], s[22:23], 0, v[162:163]
	s_addc_u32 s61, s23, 0
	s_add_i32 s62, s47, s35
	global_load_lds_dwordx4 v[180:181], off
	v_lshl_add_u64 v[182:183], s[60:61], 0, v[166:167]
	s_mov_b32 m0, s62
	v_lshl_add_u64 v[184:185], s[24:25], 0, v[164:165]
	global_load_lds_dwordx4 v[182:183], off
	v_lshl_add_u64 v[182:183], s[60:61], 0, v[162:163]
	s_add_i32 m0, s62, 0x2000
	s_nop 0
	global_load_lds_dwordx4 v[182:183], off
	v_lshl_add_u64 v[182:183], s[24:25], 0, v[168:169]
	s_mov_b32 m0, s38
	s_nop 0
	global_load_lds_dwordx4 v[182:183], off
	s_mov_b32 m0, s39
	s_nop 0
	global_load_lds_dwordx4 v[184:185], off
	s_waitcnt vmcnt(8)
	s_waitcnt lgkmcnt(0)
	s_barrier
	s_setprio 1
	s_waitcnt lgkmcnt(0)
	v_mfma_f32_16x16x128_f8f6f4 v[94:97], v[18:25], v[192:199], 0
	v_mfma_f32_16x16x128_f8f6f4 v[90:93], v[26:33], v[192:199], 0
	v_mfma_f32_16x16x128_f8f6f4 v[86:89], v[18:25], v[200:207], 0
	v_mfma_f32_16x16x128_f8f6f4 v[82:85], v[26:33], v[200:207], 0
	v_mfma_f32_16x16x128_f8f6f4 v[78:81], v[18:25], v[208:215], 0
	v_mfma_f32_16x16x128_f8f6f4 v[74:77], v[26:33], v[208:215], 0
	v_mfma_f32_16x16x128_f8f6f4 v[70:73], v[18:25], v[216:223], 0
	v_mfma_f32_16x16x128_f8f6f4 v[66:69], v[26:33], v[216:223], 0
	s_setprio 0
	s_setprio 1
	v_mfma_f32_16x16x128_f8f6f4 v[62:65], v[2:9], v[192:199], 0
	v_mfma_f32_16x16x128_f8f6f4 v[58:61], v[10:17], v[192:199], 0
	v_mfma_f32_16x16x128_f8f6f4 v[54:57], v[2:9], v[200:207], 0
	v_mfma_f32_16x16x128_f8f6f4 v[50:53], v[10:17], v[200:207], 0
	v_mfma_f32_16x16x128_f8f6f4 v[46:49], v[2:9], v[208:215], 0
	v_mfma_f32_16x16x128_f8f6f4 v[42:45], v[10:17], v[208:215], 0
	v_mfma_f32_16x16x128_f8f6f4 v[38:41], v[2:9], v[216:223], 0
	v_mfma_f32_16x16x128_f8f6f4 v[34:37], v[10:17], v[216:223], 0
	s_setprio 0
	s_barrier
	s_add_i32 s60, 0, 0x18000
	s_add_i32 s61, 0, 0x1c000
	v_add_u32_e32 v14, s60, v186
	v_add_u32_e32 v30, s61, v186
	ds_read_b128 v[2:5], v14
	ds_read_b128 v[6:9], v14 offset:1024
	ds_read_b128 v[10:13], v14 offset:2048
	ds_read_b128 v[14:17], v14 offset:3072
	ds_read_b128 v[18:21], v30
	ds_read_b128 v[22:25], v30 offset:1024
	ds_read_b128 v[26:29], v30 offset:2048
	ds_read_b128 v[30:33], v30 offset:3072
	s_add_u32 s24, s24, 0x70000
	s_addc_u32 s25, s25, 0
	s_mov_b32 m0, s40
	v_lshl_add_u64 v[224:225], s[24:25], 0, v[168:169]
	ds_read_b128 v[192:195], v191 offset:32768
	ds_read_b128 v[196:199], v191 offset:33792
	ds_read_b128 v[200:203], v191 offset:34816
	ds_read_b128 v[204:207], v191 offset:35840
	ds_read_b128 v[208:211], v191 offset:36864
	ds_read_b128 v[212:215], v191 offset:37888
	ds_read_b128 v[216:219], v191 offset:38912
	ds_read_b128 v[220:223], v191 offset:39936
	global_load_lds_dwordx4 v[224:225], off
	v_lshl_add_u64 v[224:225], s[24:25], 0, v[164:165]
	s_mov_b32 m0, s41
	s_nop 0
	global_load_lds_dwordx4 v[224:225], off
	s_waitcnt vmcnt(8)
	s_waitcnt lgkmcnt(0)
	s_barrier
	s_setprio 1
	s_waitcnt lgkmcnt(0)
	v_mfma_f32_16x16x128_f8f6f4 v[158:161], v[2:9], v[192:199], v[158:161]
	v_mfma_f32_16x16x128_f8f6f4 v[154:157], v[10:17], v[192:199], v[154:157]
	v_mfma_f32_16x16x128_f8f6f4 v[150:153], v[2:9], v[200:207], v[150:153]
	v_mfma_f32_16x16x128_f8f6f4 v[146:149], v[10:17], v[200:207], v[146:149]
	v_mfma_f32_16x16x128_f8f6f4 v[142:145], v[2:9], v[208:215], v[142:145]
	v_mfma_f32_16x16x128_f8f6f4 v[138:141], v[10:17], v[208:215], v[138:141]
	v_mfma_f32_16x16x128_f8f6f4 v[134:137], v[2:9], v[216:223], v[134:137]
	v_mfma_f32_16x16x128_f8f6f4 v[130:133], v[10:17], v[216:223], v[130:133]
	s_setprio 0
	s_setprio 1
	v_mfma_f32_16x16x128_f8f6f4 v[126:129], v[18:25], v[192:199], v[126:129]
	v_mfma_f32_16x16x128_f8f6f4 v[122:125], v[26:33], v[192:199], v[122:125]
	v_mfma_f32_16x16x128_f8f6f4 v[118:121], v[18:25], v[200:207], v[118:121]
	v_mfma_f32_16x16x128_f8f6f4 v[114:117], v[26:33], v[200:207], v[114:117]
	v_mfma_f32_16x16x128_f8f6f4 v[110:113], v[18:25], v[208:215], v[110:113]
	v_mfma_f32_16x16x128_f8f6f4 v[106:109], v[26:33], v[208:215], v[106:109]
	v_mfma_f32_16x16x128_f8f6f4 v[102:105], v[18:25], v[216:223], v[102:105]
	v_mfma_f32_16x16x128_f8f6f4 v[98:101], v[26:33], v[216:223], v[98:101]
	s_setprio 0
	s_barrier
	s_add_i32 s24, s60, s35
	v_lshl_add_u64 v[178:179], v[178:179], 0, s[10:11]
	s_mov_b32 m0, s24
	ds_read_b128 v[192:195], v191 offset:49152
	ds_read_b128 v[196:199], v191 offset:50176
	ds_read_b128 v[200:203], v191 offset:51200
	ds_read_b128 v[204:207], v191 offset:52224
	ds_read_b128 v[208:211], v191 offset:53248
	ds_read_b128 v[212:215], v191 offset:54272
	ds_read_b128 v[216:219], v191 offset:55296
	ds_read_b128 v[220:223], v191 offset:56320
	global_load_lds_dwordx4 v[178:179], off
	s_add_i32 m0, s24, 0x2000
	s_add_u32 s22, s22, 0x70080
	v_lshl_add_u64 v[178:179], v[180:181], 0, s[10:11]
	s_addc_u32 s23, s23, 0
	s_add_i32 s24, s61, s35
	global_load_lds_dwordx4 v[178:179], off
	v_lshl_add_u64 v[178:179], s[22:23], 0, v[166:167]
	s_mov_b32 m0, s24
	s_nop 0
	global_load_lds_dwordx4 v[178:179], off
	v_lshl_add_u64 v[178:179], s[22:23], 0, v[162:163]
	s_add_i32 m0, s24, 0x2000
	s_nop 0
	global_load_lds_dwordx4 v[178:179], off
	v_lshl_add_u64 v[178:179], v[182:183], 0, s[10:11]
	s_mov_b32 m0, s43
	s_nop 0
	global_load_lds_dwordx4 v[178:179], off
	v_lshl_add_u64 v[178:179], v[184:185], 0, s[10:11]
	s_mov_b32 m0, s44
	s_nop 0
	global_load_lds_dwordx4 v[178:179], off
	s_waitcnt vmcnt(8)
	s_waitcnt lgkmcnt(0)
	s_barrier
	s_setprio 1
	s_waitcnt lgkmcnt(0)
	v_mfma_f32_16x16x128_f8f6f4 v[94:97], v[2:9], v[192:199], v[94:97]
	v_mfma_f32_16x16x128_f8f6f4 v[90:93], v[10:17], v[192:199], v[90:93]
	v_mfma_f32_16x16x128_f8f6f4 v[86:89], v[2:9], v[200:207], v[86:89]
	v_mfma_f32_16x16x128_f8f6f4 v[82:85], v[10:17], v[200:207], v[82:85]
	v_mfma_f32_16x16x128_f8f6f4 v[78:81], v[2:9], v[208:215], v[78:81]
	v_mfma_f32_16x16x128_f8f6f4 v[74:77], v[10:17], v[208:215], v[74:77]
	v_mfma_f32_16x16x128_f8f6f4 v[70:73], v[2:9], v[216:223], v[70:73]
	v_mfma_f32_16x16x128_f8f6f4 v[66:69], v[10:17], v[216:223], v[66:69]
	s_setprio 0
	s_setprio 1
	v_mfma_f32_16x16x128_f8f6f4 v[62:65], v[18:25], v[192:199], v[62:65]
	v_mfma_f32_16x16x128_f8f6f4 v[58:61], v[26:33], v[192:199], v[58:61]
	v_mfma_f32_16x16x128_f8f6f4 v[54:57], v[18:25], v[200:207], v[54:57]
	v_mfma_f32_16x16x128_f8f6f4 v[50:53], v[26:33], v[200:207], v[50:53]
	v_mfma_f32_16x16x128_f8f6f4 v[46:49], v[18:25], v[208:215], v[46:49]
	v_mfma_f32_16x16x128_f8f6f4 v[42:45], v[26:33], v[208:215], v[42:45]
	v_mfma_f32_16x16x128_f8f6f4 v[38:41], v[18:25], v[216:223], v[38:41]
	v_mfma_f32_16x16x128_f8f6f4 v[34:37], v[26:33], v[216:223], v[34:37]
	s_setprio 0
	s_barrier
	s_add_i32 s59, s59, 2
	s_add_u32 s20, s20, 0x100
	s_addc_u32 s21, s21, 0
	s_add_u32 s52, s52, 0x100
	s_addc_u32 s53, s53, 0
	s_cmp_gt_u32 s59, 25
.LBB0_2048:
	ds_read_b128 v[18:21], v189
	ds_read_b128 v[22:25], v189 offset:1024
	ds_read_b128 v[26:29], v189 offset:2048
	ds_read_b128 v[30:33], v189 offset:3072
	ds_read_b128 v[2:5], v190
	ds_read_b128 v[6:9], v190 offset:1024
	ds_read_b128 v[10:13], v190 offset:2048
	ds_read_b128 v[14:17], v190 offset:3072
	s_add_u32 s22, s20, 0xfff90080
	s_addc_u32 s23, s21, -1
	s_cmp_eq_u32 s59, 24
	s_cselect_b32 s25, s17, s23
	s_cselect_b32 s24, s16, s22
	s_cselect_b32 s23, s19, s53
	s_cselect_b32 s22, s18, s52
	v_lshl_add_u64 v[216:217], s[20:21], 0, v[172:173]
	s_add_i32 m0, s38, 0xc000
	ds_read_b128 v[178:181], v191
	ds_read_b128 v[182:185], v191 offset:1024
	ds_read_b128 v[192:195], v191 offset:2048
	ds_read_b128 v[196:199], v191 offset:3072
	ds_read_b128 v[200:203], v191 offset:4096
	ds_read_b128 v[204:207], v191 offset:5120
	ds_read_b128 v[208:211], v191 offset:6144
	ds_read_b128 v[212:215], v191 offset:7168
	global_load_lds_dwordx4 v[216:217], off
	v_lshl_add_u64 v[216:217], s[20:21], 0, v[174:175]
	s_add_i32 m0, s38, 0xe000
	s_nop 0
	global_load_lds_dwordx4 v[216:217], off
	s_waitcnt vmcnt(8)
	s_waitcnt lgkmcnt(0)
	s_barrier
	s_setprio 1
	s_waitcnt lgkmcnt(0)
	v_mfma_f32_16x16x128_f8f6f4 v[158:161], v[18:25], v[178:185], v[158:161]
	v_mfma_f32_16x16x128_f8f6f4 v[154:157], v[26:33], v[178:185], v[154:157]
	v_mfma_f32_16x16x128_f8f6f4 v[150:153], v[18:25], v[192:199], v[150:153]
	v_mfma_f32_16x16x128_f8f6f4 v[146:149], v[26:33], v[192:199], v[146:149]
	v_mfma_f32_16x16x128_f8f6f4 v[142:145], v[18:25], v[200:207], v[142:145]
	v_mfma_f32_16x16x128_f8f6f4 v[138:141], v[26:33], v[200:207], v[138:141]
	v_mfma_f32_16x16x128_f8f6f4 v[134:137], v[18:25], v[208:215], v[134:137]
	v_mfma_f32_16x16x128_f8f6f4 v[130:133], v[26:33], v[208:215], v[130:133]
	s_setprio 0
	s_setprio 1
	v_mfma_f32_16x16x128_f8f6f4 v[126:129], v[2:9], v[178:185], v[126:129]
	v_mfma_f32_16x16x128_f8f6f4 v[122:125], v[10:17], v[178:185], v[122:125]
	v_mfma_f32_16x16x128_f8f6f4 v[118:121], v[2:9], v[192:199], v[118:121]
	v_mfma_f32_16x16x128_f8f6f4 v[114:117], v[10:17], v[192:199], v[114:117]
	v_mfma_f32_16x16x128_f8f6f4 v[110:113], v[2:9], v[200:207], v[110:113]
	v_mfma_f32_16x16x128_f8f6f4 v[106:109], v[10:17], v[200:207], v[106:109]
	v_mfma_f32_16x16x128_f8f6f4 v[102:105], v[2:9], v[208:215], v[102:105]
	v_mfma_f32_16x16x128_f8f6f4 v[98:101], v[10:17], v[208:215], v[98:101]
	s_setprio 0
	s_barrier
	s_add_i32 s60, s46, s35
	v_lshl_add_u64 v[178:179], s[22:23], 0, v[166:167]
	s_mov_b32 m0, s60
	ds_read_b128 v[192:195], v191 offset:16384
	ds_read_b128 v[196:199], v191 offset:17408
	ds_read_b128 v[200:203], v191 offset:18432
	ds_read_b128 v[204:207], v191 offset:19456
	ds_read_b128 v[208:211], v191 offset:20480
	ds_read_b128 v[212:215], v191 offset:21504
	ds_read_b128 v[216:219], v191 offset:22528
	ds_read_b128 v[220:223], v191 offset:23552
	global_load_lds_dwordx4 v[178:179], off
	s_add_i32 m0, s60, 0x2000
	s_add_u32 s60, s22, 0x70000
	v_lshl_add_u64 v[180:181], s[22:23], 0, v[162:163]
	s_addc_u32 s61, s23, 0
	s_add_i32 s62, s47, s35
	global_load_lds_dwordx4 v[180:181], off
	v_lshl_add_u64 v[182:183], s[60:61], 0, v[166:167]
	s_mov_b32 m0, s62
	v_lshl_add_u64 v[184:185], s[24:25], 0, v[164:165]
	global_load_lds_dwordx4 v[182:183], off
	v_lshl_add_u64 v[182:183], s[60:61], 0, v[162:163]
	s_add_i32 m0, s62, 0x2000
	s_nop 0
	global_load_lds_dwordx4 v[182:183], off
	v_lshl_add_u64 v[182:183], s[24:25], 0, v[168:169]
	s_mov_b32 m0, s38
	s_nop 0
	global_load_lds_dwordx4 v[182:183], off
	s_mov_b32 m0, s39
	s_nop 0
	global_load_lds_dwordx4 v[184:185], off
	s_waitcnt vmcnt(8)
	s_waitcnt lgkmcnt(0)
	s_barrier
	s_setprio 1
	s_waitcnt lgkmcnt(0)
	v_mfma_f32_16x16x128_f8f6f4 v[94:97], v[18:25], v[192:199], v[94:97]
	v_mfma_f32_16x16x128_f8f6f4 v[90:93], v[26:33], v[192:199], v[90:93]
	v_mfma_f32_16x16x128_f8f6f4 v[86:89], v[18:25], v[200:207], v[86:89]
	v_mfma_f32_16x16x128_f8f6f4 v[82:85], v[26:33], v[200:207], v[82:85]
	v_mfma_f32_16x16x128_f8f6f4 v[78:81], v[18:25], v[208:215], v[78:81]
	v_mfma_f32_16x16x128_f8f6f4 v[74:77], v[26:33], v[208:215], v[74:77]
	v_mfma_f32_16x16x128_f8f6f4 v[70:73], v[18:25], v[216:223], v[70:73]
	v_mfma_f32_16x16x128_f8f6f4 v[66:69], v[26:33], v[216:223], v[66:69]
	s_setprio 0
	s_setprio 1
	v_mfma_f32_16x16x128_f8f6f4 v[62:65], v[2:9], v[192:199], v[62:65]
	v_mfma_f32_16x16x128_f8f6f4 v[58:61], v[10:17], v[192:199], v[58:61]
	v_mfma_f32_16x16x128_f8f6f4 v[54:57], v[2:9], v[200:207], v[54:57]
	v_mfma_f32_16x16x128_f8f6f4 v[50:53], v[10:17], v[200:207], v[50:53]
	v_mfma_f32_16x16x128_f8f6f4 v[46:49], v[2:9], v[208:215], v[46:49]
	v_mfma_f32_16x16x128_f8f6f4 v[42:45], v[10:17], v[208:215], v[42:45]
	v_mfma_f32_16x16x128_f8f6f4 v[38:41], v[2:9], v[216:223], v[38:41]
	v_mfma_f32_16x16x128_f8f6f4 v[34:37], v[10:17], v[216:223], v[34:37]
	s_setprio 0
	s_barrier
	s_add_i32 s60, 0, 0x18000
	s_add_i32 s61, 0, 0x1c000
	v_add_u32_e32 v14, s60, v186
	v_add_u32_e32 v30, s61, v186
	ds_read_b128 v[2:5], v14
	ds_read_b128 v[6:9], v14 offset:1024
	ds_read_b128 v[10:13], v14 offset:2048
	ds_read_b128 v[14:17], v14 offset:3072
	ds_read_b128 v[18:21], v30
	ds_read_b128 v[22:25], v30 offset:1024
	ds_read_b128 v[26:29], v30 offset:2048
	ds_read_b128 v[30:33], v30 offset:3072
	s_add_u32 s24, s24, 0x70000
	s_addc_u32 s25, s25, 0
	s_mov_b32 m0, s40
	v_lshl_add_u64 v[224:225], s[24:25], 0, v[168:169]
	ds_read_b128 v[192:195], v191 offset:32768
	ds_read_b128 v[196:199], v191 offset:33792
	ds_read_b128 v[200:203], v191 offset:34816
	ds_read_b128 v[204:207], v191 offset:35840
	ds_read_b128 v[208:211], v191 offset:36864
	ds_read_b128 v[212:215], v191 offset:37888
	ds_read_b128 v[216:219], v191 offset:38912
	ds_read_b128 v[220:223], v191 offset:39936
	global_load_lds_dwordx4 v[224:225], off
	v_lshl_add_u64 v[224:225], s[24:25], 0, v[164:165]
	s_mov_b32 m0, s41
	s_nop 0
	global_load_lds_dwordx4 v[224:225], off
	s_waitcnt vmcnt(8)
	s_waitcnt lgkmcnt(0)
	s_barrier
	s_setprio 1
	s_waitcnt lgkmcnt(0)
	v_mfma_f32_16x16x128_f8f6f4 v[158:161], v[2:9], v[192:199], v[158:161]
	v_mfma_f32_16x16x128_f8f6f4 v[154:157], v[10:17], v[192:199], v[154:157]
	v_mfma_f32_16x16x128_f8f6f4 v[150:153], v[2:9], v[200:207], v[150:153]
	v_mfma_f32_16x16x128_f8f6f4 v[146:149], v[10:17], v[200:207], v[146:149]
	v_mfma_f32_16x16x128_f8f6f4 v[142:145], v[2:9], v[208:215], v[142:145]
	v_mfma_f32_16x16x128_f8f6f4 v[138:141], v[10:17], v[208:215], v[138:141]
	v_mfma_f32_16x16x128_f8f6f4 v[134:137], v[2:9], v[216:223], v[134:137]
	v_mfma_f32_16x16x128_f8f6f4 v[130:133], v[10:17], v[216:223], v[130:133]
	s_setprio 0
	s_setprio 1
	v_mfma_f32_16x16x128_f8f6f4 v[126:129], v[18:25], v[192:199], v[126:129]
	v_mfma_f32_16x16x128_f8f6f4 v[122:125], v[26:33], v[192:199], v[122:125]
	v_mfma_f32_16x16x128_f8f6f4 v[118:121], v[18:25], v[200:207], v[118:121]
	v_mfma_f32_16x16x128_f8f6f4 v[114:117], v[26:33], v[200:207], v[114:117]
	v_mfma_f32_16x16x128_f8f6f4 v[110:113], v[18:25], v[208:215], v[110:113]
	v_mfma_f32_16x16x128_f8f6f4 v[106:109], v[26:33], v[208:215], v[106:109]
	v_mfma_f32_16x16x128_f8f6f4 v[102:105], v[18:25], v[216:223], v[102:105]
	v_mfma_f32_16x16x128_f8f6f4 v[98:101], v[26:33], v[216:223], v[98:101]
	s_setprio 0
	s_barrier
	s_add_i32 s24, s60, s35
	v_lshl_add_u64 v[178:179], v[178:179], 0, s[10:11]
	s_mov_b32 m0, s24
	ds_read_b128 v[192:195], v191 offset:49152
	ds_read_b128 v[196:199], v191 offset:50176
	ds_read_b128 v[200:203], v191 offset:51200
	ds_read_b128 v[204:207], v191 offset:52224
	ds_read_b128 v[208:211], v191 offset:53248
	ds_read_b128 v[212:215], v191 offset:54272
	ds_read_b128 v[216:219], v191 offset:55296
	ds_read_b128 v[220:223], v191 offset:56320
	global_load_lds_dwordx4 v[178:179], off
	s_add_i32 m0, s24, 0x2000
	s_add_u32 s22, s22, 0x70080
	v_lshl_add_u64 v[178:179], v[180:181], 0, s[10:11]
	s_addc_u32 s23, s23, 0
	s_add_i32 s24, s61, s35
	global_load_lds_dwordx4 v[178:179], off
	v_lshl_add_u64 v[178:179], s[22:23], 0, v[166:167]
	s_mov_b32 m0, s24
	s_nop 0
	global_load_lds_dwordx4 v[178:179], off
	v_lshl_add_u64 v[178:179], s[22:23], 0, v[162:163]
	s_add_i32 m0, s24, 0x2000
	s_nop 0
	global_load_lds_dwordx4 v[178:179], off
	v_lshl_add_u64 v[178:179], v[182:183], 0, s[10:11]
	s_mov_b32 m0, s43
	s_nop 0
	global_load_lds_dwordx4 v[178:179], off
	v_lshl_add_u64 v[178:179], v[184:185], 0, s[10:11]
	s_mov_b32 m0, s44
	s_nop 0
	global_load_lds_dwordx4 v[178:179], off
	s_waitcnt vmcnt(8)
	s_waitcnt lgkmcnt(0)
	s_barrier
	s_setprio 1
	s_waitcnt lgkmcnt(0)
	v_mfma_f32_16x16x128_f8f6f4 v[94:97], v[2:9], v[192:199], v[94:97]
	v_mfma_f32_16x16x128_f8f6f4 v[90:93], v[10:17], v[192:199], v[90:93]
	v_mfma_f32_16x16x128_f8f6f4 v[86:89], v[2:9], v[200:207], v[86:89]
	v_mfma_f32_16x16x128_f8f6f4 v[82:85], v[10:17], v[200:207], v[82:85]
	v_mfma_f32_16x16x128_f8f6f4 v[78:81], v[2:9], v[208:215], v[78:81]
	v_mfma_f32_16x16x128_f8f6f4 v[74:77], v[10:17], v[208:215], v[74:77]
	v_mfma_f32_16x16x128_f8f6f4 v[70:73], v[2:9], v[216:223], v[70:73]
	v_mfma_f32_16x16x128_f8f6f4 v[66:69], v[10:17], v[216:223], v[66:69]
	s_setprio 0
	s_setprio 1
	v_mfma_f32_16x16x128_f8f6f4 v[62:65], v[18:25], v[192:199], v[62:65]
	v_mfma_f32_16x16x128_f8f6f4 v[58:61], v[26:33], v[192:199], v[58:61]
	v_mfma_f32_16x16x128_f8f6f4 v[54:57], v[18:25], v[200:207], v[54:57]
	v_mfma_f32_16x16x128_f8f6f4 v[50:53], v[26:33], v[200:207], v[50:53]
	v_mfma_f32_16x16x128_f8f6f4 v[46:49], v[18:25], v[208:215], v[46:49]
	v_mfma_f32_16x16x128_f8f6f4 v[42:45], v[26:33], v[208:215], v[42:45]
	v_mfma_f32_16x16x128_f8f6f4 v[38:41], v[18:25], v[216:223], v[38:41]
	v_mfma_f32_16x16x128_f8f6f4 v[34:37], v[26:33], v[216:223], v[34:37]
	s_setprio 0
	s_barrier
	s_add_i32 s59, s59, 2
	s_add_u32 s20, s20, 0x100
	s_addc_u32 s21, s21, 0
	s_add_u32 s52, s52, 0x100
	s_addc_u32 s53, s53, 0
	s_cmp_gt_u32 s59, 25
	s_cbranch_scc0 .LBB0_2048
	s_and_b64 vcc, exec, s[12:13]
	s_cbranch_vccz .LBB0_2051
	s_barrier

.LBB0_2179:
	s_add_u32 s10, s72, 0xdd00000
	s_addc_u32 s11, s73, 0
	s_lshl_b32 s16, s0, 6
	s_lshl_b32 s15, s0, 13
	s_lshl_b32 s0, s1, 5
	s_mov_b64 s[12:13], 0x80
	s_and_b32 s18, s0, 0x60
	s_add_i32 m0, s43, 0x18000
	v_lshl_add_u64 v[8:9], v[8:9], 0, s[12:13]
	s_lshl_b32 s19, s18, 7
	s_waitcnt vmcnt(2)
	s_barrier
	global_load_lds_dwordx4 v[8:9], off
	v_lshl_add_u64 v[6:7], v[6:7], 0, s[12:13]
	s_add_i32 m0, s43, 0x1a000
	s_add_i32 s48, s43, 0x8000
	s_add_i32 s49, s43, 0xa000
	global_load_lds_dwordx4 v[6:7], off
	v_lshl_add_u64 v[2:3], v[2:3], 0, s[12:13]
	s_mov_b32 m0, s48
	s_add_u32 s0, s24, 0x70080
	global_load_lds_dwordx4 v[2:3], off
	v_lshl_add_u64 v[2:3], v[4:5], 0, s[12:13]
	s_mov_b32 m0, s49
	s_addc_u32 s1, s25, 0
	global_load_lds_dwordx4 v[2:3], off
	s_add_i32 m0, s43, 0x1c000
	v_lshl_add_u64 v[2:3], s[0:1], 0, v[164:165]
	global_load_lds_dwordx4 v[2:3], off
	v_lshl_add_u64 v[2:3], s[0:1], 0, v[168:169]
	s_add_i32 m0, s43, 0x1e000
	s_movk_i32 s0, 0x3c0
	global_load_lds_dwordx4 v[2:3], off
	v_and_b32_e32 v2, 48, v0
	v_lshlrev_b32_e32 v3, 6, v0
	v_and_or_b32 v2, v3, s0, v2
	v_lshlrev_b32_e32 v3, 2, v0
	v_and_b32_e32 v3, 32, v3
	s_waitcnt vmcnt(6)
	s_cmpk_lt_u32 s14, 0x100
	v_bitop3_b32 v4, v2, s15, v3 bitop3:0xde
	v_bitop3_b32 v186, s19, v2, v3 bitop3:0xf6
	s_cselect_b64 s[14:15], -1, 0
	v_mov_b64_e32 v[176:177], s[6:7]
	s_add_i32 s7, 0, 0x10000
	s_add_i32 s51, 0, 0x14000
	v_and_or_b32 v187, v0, 31, s16
	s_ashr_i32 s50, s28, 31
	v_and_or_b32 v188, v12, 16, s18
	v_add3_u32 v172, v13, v10, v11
	v_mov_b32_e32 v173, v165
	v_add3_u32 v174, v14, v10, v11
	v_mov_b32_e32 v175, v165
	v_add_u32_e32 v189, s7, v186
	v_add_u32_e32 v190, s51, v186
	v_add_u32_e32 v191, 0, v4
	s_mov_b32 s16, 0x3e800000
	s_mov_b64 s[18:19], s[22:23]
	s_mov_b64 s[20:21], s[24:25]
	s_barrier
	s_branch .LBB0_2182

.LBB0_2188:
	s_add_u32 s22, s22, 0x70080
	s_addc_u32 s23, s23, 0
	s_add_u32 s61, s24, 0x100
	s_addc_u32 s62, s25, 0
	s_mov_b32 s63, -2
	ds_read_b128 v[18:21], v189
	ds_read_b128 v[22:25], v189 offset:1024
	ds_read_b128 v[26:29], v189 offset:2048
	ds_read_b128 v[30:33], v189 offset:3072
	ds_read_b128 v[2:5], v190
	ds_read_b128 v[6:9], v190 offset:1024
	ds_read_b128 v[10:13], v190 offset:2048
	ds_read_b128 v[14:17], v190 offset:3072
	s_add_u32 s24, s22, 0xfff90080
	s_addc_u32 s25, s23, -1
	s_cmp_eq_u32 s63, 24
	s_cselect_b32 s27, s19, s25
	s_cselect_b32 s26, s18, s24
	s_cselect_b32 s25, s21, s62
	s_cselect_b32 s24, s20, s61
	v_lshl_add_u64 v[216:217], s[22:23], 0, v[172:173]
	s_add_i32 m0, s43, 0xc000
	ds_read_b128 v[178:181], v191
	ds_read_b128 v[182:185], v191 offset:1024
	ds_read_b128 v[192:195], v191 offset:2048
	ds_read_b128 v[196:199], v191 offset:3072
	ds_read_b128 v[200:203], v191 offset:4096
	ds_read_b128 v[204:207], v191 offset:5120
	ds_read_b128 v[208:211], v191 offset:6144
	ds_read_b128 v[212:215], v191 offset:7168
	global_load_lds_dwordx4 v[216:217], off
	v_lshl_add_u64 v[216:217], s[22:23], 0, v[174:175]
	s_add_i32 m0, s43, 0xe000
	s_nop 0
	global_load_lds_dwordx4 v[216:217], off
	s_waitcnt vmcnt(8)
	s_waitcnt lgkmcnt(0)
	s_barrier
	s_setprio 1
	s_waitcnt lgkmcnt(0)
	v_mfma_f32_16x16x128_f8f6f4 v[158:161], v[18:25], v[178:185], 0
	v_mfma_f32_16x16x128_f8f6f4 v[154:157], v[26:33], v[178:185], 0
	v_mfma_f32_16x16x128_f8f6f4 v[150:153], v[18:25], v[192:199], 0
	v_mfma_f32_16x16x128_f8f6f4 v[146:149], v[26:33], v[192:199], 0
	v_mfma_f32_16x16x128_f8f6f4 v[142:145], v[18:25], v[200:207], 0
	v_mfma_f32_16x16x128_f8f6f4 v[138:141], v[26:33], v[200:207], 0
	v_mfma_f32_16x16x128_f8f6f4 v[134:137], v[18:25], v[208:215], 0
	v_mfma_f32_16x16x128_f8f6f4 v[130:133], v[26:33], v[208:215], 0
	s_setprio 0
	s_setprio 1
	v_mfma_f32_16x16x128_f8f6f4 v[126:129], v[2:9], v[178:185], 0
	v_mfma_f32_16x16x128_f8f6f4 v[122:125], v[10:17], v[178:185], 0
	v_mfma_f32_16x16x128_f8f6f4 v[118:121], v[2:9], v[192:199], 0
	v_mfma_f32_16x16x128_f8f6f4 v[114:117], v[10:17], v[192:199], 0
	v_mfma_f32_16x16x128_f8f6f4 v[110:113], v[2:9], v[200:207], 0
	v_mfma_f32_16x16x128_f8f6f4 v[106:109], v[10:17], v[200:207], 0
	v_mfma_f32_16x16x128_f8f6f4 v[102:105], v[2:9], v[208:215], 0
	v_mfma_f32_16x16x128_f8f6f4 v[98:101], v[10:17], v[208:215], 0
	s_setprio 0
	s_barrier
	s_add_i32 s64, s7, s42
	v_lshl_add_u64 v[178:179], s[24:25], 0, v[164:165]
	s_mov_b32 m0, s64
	ds_read_b128 v[192:195], v191 offset:16384
	ds_read_b128 v[196:199], v191 offset:17408
	ds_read_b128 v[200:203], v191 offset:18432
	ds_read_b128 v[204:207], v191 offset:19456
	ds_read_b128 v[208:211], v191 offset:20480
	ds_read_b128 v[212:215], v191 offset:21504
	ds_read_b128 v[216:219], v191 offset:22528
	ds_read_b128 v[220:223], v191 offset:23552
	global_load_lds_dwordx4 v[178:179], off
	s_add_i32 m0, s64, 0x2000
	s_add_u32 s64, s24, 0x70000
	v_lshl_add_u64 v[180:181], s[24:25], 0, v[168:169]
	s_addc_u32 s65, s25, 0
	s_add_i32 s66, s51, s42
	global_load_lds_dwordx4 v[180:181], off
	v_lshl_add_u64 v[182:183], s[64:65], 0, v[164:165]
	s_mov_b32 m0, s66
	v_lshl_add_u64 v[184:185], s[26:27], 0, v[166:167]
	global_load_lds_dwordx4 v[182:183], off
	v_lshl_add_u64 v[182:183], s[64:65], 0, v[168:169]
	s_add_i32 m0, s66, 0x2000
	s_nop 0
	global_load_lds_dwordx4 v[182:183], off
	v_lshl_add_u64 v[182:183], s[26:27], 0, v[162:163]
	s_mov_b32 m0, s43
	s_nop 0
	global_load_lds_dwordx4 v[182:183], off
	s_mov_b32 m0, s44
	s_nop 0
	global_load_lds_dwordx4 v[184:185], off
	s_waitcnt vmcnt(8)
	s_waitcnt lgkmcnt(0)
	s_barrier
	s_setprio 1
	s_waitcnt lgkmcnt(0)
	v_mfma_f32_16x16x128_f8f6f4 v[94:97], v[18:25], v[192:199], 0
	v_mfma_f32_16x16x128_f8f6f4 v[90:93], v[26:33], v[192:199], 0
	v_mfma_f32_16x16x128_f8f6f4 v[86:89], v[18:25], v[200:207], 0
	v_mfma_f32_16x16x128_f8f6f4 v[82:85], v[26:33], v[200:207], 0
	v_mfma_f32_16x16x128_f8f6f4 v[78:81], v[18:25], v[208:215], 0
	v_mfma_f32_16x16x128_f8f6f4 v[74:77], v[26:33], v[208:215], 0
	v_mfma_f32_16x16x128_f8f6f4 v[70:73], v[18:25], v[216:223], 0
	v_mfma_f32_16x16x128_f8f6f4 v[66:69], v[26:33], v[216:223], 0
	s_setprio 0
	s_setprio 1
	v_mfma_f32_16x16x128_f8f6f4 v[62:65], v[2:9], v[192:199], 0
	v_mfma_f32_16x16x128_f8f6f4 v[58:61], v[10:17], v[192:199], 0
	v_mfma_f32_16x16x128_f8f6f4 v[54:57], v[2:9], v[200:207], 0
	v_mfma_f32_16x16x128_f8f6f4 v[50:53], v[10:17], v[200:207], 0
	v_mfma_f32_16x16x128_f8f6f4 v[46:49], v[2:9], v[208:215], 0
	v_mfma_f32_16x16x128_f8f6f4 v[42:45], v[10:17], v[208:215], 0
	v_mfma_f32_16x16x128_f8f6f4 v[38:41], v[2:9], v[216:223], 0
	v_mfma_f32_16x16x128_f8f6f4 v[34:37], v[10:17], v[216:223], 0
	s_setprio 0
	s_barrier
	s_add_i32 s64, 0, 0x18000
	s_add_i32 s65, 0, 0x1c000
	v_add_u32_e32 v14, s64, v186
	v_add_u32_e32 v30, s65, v186
	ds_read_b128 v[2:5], v14
	ds_read_b128 v[6:9], v14 offset:1024
	ds_read_b128 v[10:13], v14 offset:2048
	ds_read_b128 v[14:17], v14 offset:3072
	ds_read_b128 v[18:21], v30
	ds_read_b128 v[22:25], v30 offset:1024
	ds_read_b128 v[26:29], v30 offset:2048
	ds_read_b128 v[30:33], v30 offset:3072
	s_add_u32 s26, s26, 0x70000
	s_addc_u32 s27, s27, 0
	s_mov_b32 m0, s45
	v_lshl_add_u64 v[224:225], s[26:27], 0, v[162:163]
	ds_read_b128 v[192:195], v191 offset:32768
	ds_read_b128 v[196:199], v191 offset:33792
	ds_read_b128 v[200:203], v191 offset:34816
	ds_read_b128 v[204:207], v191 offset:35840
	ds_read_b128 v[208:211], v191 offset:36864
	ds_read_b128 v[212:215], v191 offset:37888
	ds_read_b128 v[216:219], v191 offset:38912
	ds_read_b128 v[220:223], v191 offset:39936
	global_load_lds_dwordx4 v[224:225], off
	v_lshl_add_u64 v[224:225], s[26:27], 0, v[166:167]
	s_mov_b32 m0, s46
	s_nop 0
	global_load_lds_dwordx4 v[224:225], off
	s_waitcnt vmcnt(8)
	s_waitcnt lgkmcnt(0)
	s_barrier
	s_setprio 1
	s_waitcnt lgkmcnt(0)
	v_mfma_f32_16x16x128_f8f6f4 v[158:161], v[2:9], v[192:199], v[158:161]
	v_mfma_f32_16x16x128_f8f6f4 v[154:157], v[10:17], v[192:199], v[154:157]
	v_mfma_f32_16x16x128_f8f6f4 v[150:153], v[2:9], v[200:207], v[150:153]
	v_mfma_f32_16x16x128_f8f6f4 v[146:149], v[10:17], v[200:207], v[146:149]
	v_mfma_f32_16x16x128_f8f6f4 v[142:145], v[2:9], v[208:215], v[142:145]
	v_mfma_f32_16x16x128_f8f6f4 v[138:141], v[10:17], v[208:215], v[138:141]
	v_mfma_f32_16x16x128_f8f6f4 v[134:137], v[2:9], v[216:223], v[134:137]
	v_mfma_f32_16x16x128_f8f6f4 v[130:133], v[10:17], v[216:223], v[130:133]
	s_setprio 0
	s_setprio 1
	v_mfma_f32_16x16x128_f8f6f4 v[126:129], v[18:25], v[192:199], v[126:129]
	v_mfma_f32_16x16x128_f8f6f4 v[122:125], v[26:33], v[192:199], v[122:125]
	v_mfma_f32_16x16x128_f8f6f4 v[118:121], v[18:25], v[200:207], v[118:121]
	v_mfma_f32_16x16x128_f8f6f4 v[114:117], v[26:33], v[200:207], v[114:117]
	v_mfma_f32_16x16x128_f8f6f4 v[110:113], v[18:25], v[208:215], v[110:113]
	v_mfma_f32_16x16x128_f8f6f4 v[106:109], v[26:33], v[208:215], v[106:109]
	v_mfma_f32_16x16x128_f8f6f4 v[102:105], v[18:25], v[216:223], v[102:105]
	v_mfma_f32_16x16x128_f8f6f4 v[98:101], v[26:33], v[216:223], v[98:101]
	s_setprio 0
	s_barrier
	s_add_i32 s26, s64, s42
	v_lshl_add_u64 v[178:179], v[178:179], 0, s[12:13]
	s_mov_b32 m0, s26
	ds_read_b128 v[192:195], v191 offset:49152
	ds_read_b128 v[196:199], v191 offset:50176
	ds_read_b128 v[200:203], v191 offset:51200
	ds_read_b128 v[204:207], v191 offset:52224
	ds_read_b128 v[208:211], v191 offset:53248
	ds_read_b128 v[212:215], v191 offset:54272
	ds_read_b128 v[216:219], v191 offset:55296
	ds_read_b128 v[220:223], v191 offset:56320
	global_load_lds_dwordx4 v[178:179], off
	s_add_i32 m0, s26, 0x2000
	s_add_u32 s24, s24, 0x70080
	v_lshl_add_u64 v[178:179], v[180:181], 0, s[12:13]
	s_addc_u32 s25, s25, 0
	s_add_i32 s26, s65, s42
	global_load_lds_dwordx4 v[178:179], off
	v_lshl_add_u64 v[178:179], s[24:25], 0, v[164:165]
	s_mov_b32 m0, s26
	s_nop 0
	global_load_lds_dwordx4 v[178:179], off
	v_lshl_add_u64 v[178:179], s[24:25], 0, v[168:169]
	s_add_i32 m0, s26, 0x2000
	s_nop 0
	global_load_lds_dwordx4 v[178:179], off
	v_lshl_add_u64 v[178:179], v[182:183], 0, s[12:13]
	s_mov_b32 m0, s48
	s_nop 0
	global_load_lds_dwordx4 v[178:179], off
	v_lshl_add_u64 v[178:179], v[184:185], 0, s[12:13]
	s_mov_b32 m0, s49
	s_nop 0
	global_load_lds_dwordx4 v[178:179], off
	s_waitcnt vmcnt(8)
	s_waitcnt lgkmcnt(0)
	s_barrier
	s_setprio 1
	s_waitcnt lgkmcnt(0)
	v_mfma_f32_16x16x128_f8f6f4 v[94:97], v[2:9], v[192:199], v[94:97]
	v_mfma_f32_16x16x128_f8f6f4 v[90:93], v[10:17], v[192:199], v[90:93]
	v_mfma_f32_16x16x128_f8f6f4 v[86:89], v[2:9], v[200:207], v[86:89]
	v_mfma_f32_16x16x128_f8f6f4 v[82:85], v[10:17], v[200:207], v[82:85]
	v_mfma_f32_16x16x128_f8f6f4 v[78:81], v[2:9], v[208:215], v[78:81]
	v_mfma_f32_16x16x128_f8f6f4 v[74:77], v[10:17], v[208:215], v[74:77]
	v_mfma_f32_16x16x128_f8f6f4 v[70:73], v[2:9], v[216:223], v[70:73]
	v_mfma_f32_16x16x128_f8f6f4 v[66:69], v[10:17], v[216:223], v[66:69]
	s_setprio 0
	s_setprio 1
	v_mfma_f32_16x16x128_f8f6f4 v[62:65], v[18:25], v[192:199], v[62:65]
	v_mfma_f32_16x16x128_f8f6f4 v[58:61], v[26:33], v[192:199], v[58:61]
	v_mfma_f32_16x16x128_f8f6f4 v[54:57], v[18:25], v[200:207], v[54:57]
	v_mfma_f32_16x16x128_f8f6f4 v[50:53], v[26:33], v[200:207], v[50:53]
	v_mfma_f32_16x16x128_f8f6f4 v[46:49], v[18:25], v[208:215], v[46:49]
	v_mfma_f32_16x16x128_f8f6f4 v[42:45], v[26:33], v[208:215], v[42:45]
	v_mfma_f32_16x16x128_f8f6f4 v[38:41], v[18:25], v[216:223], v[38:41]
	v_mfma_f32_16x16x128_f8f6f4 v[34:37], v[26:33], v[216:223], v[34:37]
	s_setprio 0
	s_barrier
	s_add_i32 s63, s63, 2
	s_add_u32 s22, s22, 0x100
	s_addc_u32 s23, s23, 0
	s_add_u32 s61, s61, 0x100
	s_addc_u32 s62, s62, 0
	s_cmp_gt_u32 s63, 25
.LBB0_2189:
	ds_read_b128 v[18:21], v189
	ds_read_b128 v[22:25], v189 offset:1024
	ds_read_b128 v[26:29], v189 offset:2048
	ds_read_b128 v[30:33], v189 offset:3072
	ds_read_b128 v[2:5], v190
	ds_read_b128 v[6:9], v190 offset:1024
	ds_read_b128 v[10:13], v190 offset:2048
	ds_read_b128 v[14:17], v190 offset:3072
	s_add_u32 s24, s22, 0xfff90080
	s_addc_u32 s25, s23, -1
	s_cmp_eq_u32 s63, 24
	s_cselect_b32 s27, s19, s25
	s_cselect_b32 s26, s18, s24
	s_cselect_b32 s25, s21, s62
	s_cselect_b32 s24, s20, s61
	v_lshl_add_u64 v[216:217], s[22:23], 0, v[172:173]
	s_add_i32 m0, s43, 0xc000
	ds_read_b128 v[178:181], v191
	ds_read_b128 v[182:185], v191 offset:1024
	ds_read_b128 v[192:195], v191 offset:2048
	ds_read_b128 v[196:199], v191 offset:3072
	ds_read_b128 v[200:203], v191 offset:4096
	ds_read_b128 v[204:207], v191 offset:5120
	ds_read_b128 v[208:211], v191 offset:6144
	ds_read_b128 v[212:215], v191 offset:7168
	global_load_lds_dwordx4 v[216:217], off
	v_lshl_add_u64 v[216:217], s[22:23], 0, v[174:175]
	s_add_i32 m0, s43, 0xe000
	s_nop 0
	global_load_lds_dwordx4 v[216:217], off
	s_waitcnt vmcnt(8)
	s_waitcnt lgkmcnt(0)
	s_barrier
	s_setprio 1
	s_waitcnt lgkmcnt(0)
	v_mfma_f32_16x16x128_f8f6f4 v[158:161], v[18:25], v[178:185], v[158:161]
	v_mfma_f32_16x16x128_f8f6f4 v[154:157], v[26:33], v[178:185], v[154:157]
	v_mfma_f32_16x16x128_f8f6f4 v[150:153], v[18:25], v[192:199], v[150:153]
	v_mfma_f32_16x16x128_f8f6f4 v[146:149], v[26:33], v[192:199], v[146:149]
	v_mfma_f32_16x16x128_f8f6f4 v[142:145], v[18:25], v[200:207], v[142:145]
	v_mfma_f32_16x16x128_f8f6f4 v[138:141], v[26:33], v[200:207], v[138:141]
	v_mfma_f32_16x16x128_f8f6f4 v[134:137], v[18:25], v[208:215], v[134:137]
	v_mfma_f32_16x16x128_f8f6f4 v[130:133], v[26:33], v[208:215], v[130:133]
	s_setprio 0
	s_setprio 1
	v_mfma_f32_16x16x128_f8f6f4 v[126:129], v[2:9], v[178:185], v[126:129]
	v_mfma_f32_16x16x128_f8f6f4 v[122:125], v[10:17], v[178:185], v[122:125]
	v_mfma_f32_16x16x128_f8f6f4 v[118:121], v[2:9], v[192:199], v[118:121]
	v_mfma_f32_16x16x128_f8f6f4 v[114:117], v[10:17], v[192:199], v[114:117]
	v_mfma_f32_16x16x128_f8f6f4 v[110:113], v[2:9], v[200:207], v[110:113]
	v_mfma_f32_16x16x128_f8f6f4 v[106:109], v[10:17], v[200:207], v[106:109]
	v_mfma_f32_16x16x128_f8f6f4 v[102:105], v[2:9], v[208:215], v[102:105]
	v_mfma_f32_16x16x128_f8f6f4 v[98:101], v[10:17], v[208:215], v[98:101]
	s_setprio 0
	s_barrier
	s_add_i32 s64, s7, s42
	v_lshl_add_u64 v[178:179], s[24:25], 0, v[164:165]
	s_mov_b32 m0, s64
	ds_read_b128 v[192:195], v191 offset:16384
	ds_read_b128 v[196:199], v191 offset:17408
	ds_read_b128 v[200:203], v191 offset:18432
	ds_read_b128 v[204:207], v191 offset:19456
	ds_read_b128 v[208:211], v191 offset:20480
	ds_read_b128 v[212:215], v191 offset:21504
	ds_read_b128 v[216:219], v191 offset:22528
	ds_read_b128 v[220:223], v191 offset:23552
	global_load_lds_dwordx4 v[178:179], off
	s_add_i32 m0, s64, 0x2000
	s_add_u32 s64, s24, 0x70000
	v_lshl_add_u64 v[180:181], s[24:25], 0, v[168:169]
	s_addc_u32 s65, s25, 0
	s_add_i32 s66, s51, s42
	global_load_lds_dwordx4 v[180:181], off
	v_lshl_add_u64 v[182:183], s[64:65], 0, v[164:165]
	s_mov_b32 m0, s66
	v_lshl_add_u64 v[184:185], s[26:27], 0, v[166:167]
	global_load_lds_dwordx4 v[182:183], off
	v_lshl_add_u64 v[182:183], s[64:65], 0, v[168:169]
	s_add_i32 m0, s66, 0x2000
	s_nop 0
	global_load_lds_dwordx4 v[182:183], off
	v_lshl_add_u64 v[182:183], s[26:27], 0, v[162:163]
	s_mov_b32 m0, s43
	s_nop 0
	global_load_lds_dwordx4 v[182:183], off
	s_mov_b32 m0, s44
	s_nop 0
	global_load_lds_dwordx4 v[184:185], off
	s_waitcnt vmcnt(8)
	s_waitcnt lgkmcnt(0)
	s_barrier
	s_setprio 1
	s_waitcnt lgkmcnt(0)
	v_mfma_f32_16x16x128_f8f6f4 v[94:97], v[18:25], v[192:199], v[94:97]
	v_mfma_f32_16x16x128_f8f6f4 v[90:93], v[26:33], v[192:199], v[90:93]
	v_mfma_f32_16x16x128_f8f6f4 v[86:89], v[18:25], v[200:207], v[86:89]
	v_mfma_f32_16x16x128_f8f6f4 v[82:85], v[26:33], v[200:207], v[82:85]
	v_mfma_f32_16x16x128_f8f6f4 v[78:81], v[18:25], v[208:215], v[78:81]
	v_mfma_f32_16x16x128_f8f6f4 v[74:77], v[26:33], v[208:215], v[74:77]
	v_mfma_f32_16x16x128_f8f6f4 v[70:73], v[18:25], v[216:223], v[70:73]
	v_mfma_f32_16x16x128_f8f6f4 v[66:69], v[26:33], v[216:223], v[66:69]
	s_setprio 0
	s_setprio 1
	v_mfma_f32_16x16x128_f8f6f4 v[62:65], v[2:9], v[192:199], v[62:65]
	v_mfma_f32_16x16x128_f8f6f4 v[58:61], v[10:17], v[192:199], v[58:61]
	v_mfma_f32_16x16x128_f8f6f4 v[54:57], v[2:9], v[200:207], v[54:57]
	v_mfma_f32_16x16x128_f8f6f4 v[50:53], v[10:17], v[200:207], v[50:53]
	v_mfma_f32_16x16x128_f8f6f4 v[46:49], v[2:9], v[208:215], v[46:49]
	v_mfma_f32_16x16x128_f8f6f4 v[42:45], v[10:17], v[208:215], v[42:45]
	v_mfma_f32_16x16x128_f8f6f4 v[38:41], v[2:9], v[216:223], v[38:41]
	v_mfma_f32_16x16x128_f8f6f4 v[34:37], v[10:17], v[216:223], v[34:37]
	s_setprio 0
	s_barrier
	s_add_i32 s64, 0, 0x18000
	s_add_i32 s65, 0, 0x1c000
	v_add_u32_e32 v14, s64, v186
	v_add_u32_e32 v30, s65, v186
	ds_read_b128 v[2:5], v14
	ds_read_b128 v[6:9], v14 offset:1024
	ds_read_b128 v[10:13], v14 offset:2048
	ds_read_b128 v[14:17], v14 offset:3072
	ds_read_b128 v[18:21], v30
	ds_read_b128 v[22:25], v30 offset:1024
	ds_read_b128 v[26:29], v30 offset:2048
	ds_read_b128 v[30:33], v30 offset:3072
	s_add_u32 s26, s26, 0x70000
	s_addc_u32 s27, s27, 0
	s_mov_b32 m0, s45
	v_lshl_add_u64 v[224:225], s[26:27], 0, v[162:163]
	ds_read_b128 v[192:195], v191 offset:32768
	ds_read_b128 v[196:199], v191 offset:33792
	ds_read_b128 v[200:203], v191 offset:34816
	ds_read_b128 v[204:207], v191 offset:35840
	ds_read_b128 v[208:211], v191 offset:36864
	ds_read_b128 v[212:215], v191 offset:37888
	ds_read_b128 v[216:219], v191 offset:38912
	ds_read_b128 v[220:223], v191 offset:39936
	global_load_lds_dwordx4 v[224:225], off
	v_lshl_add_u64 v[224:225], s[26:27], 0, v[166:167]
	s_mov_b32 m0, s46
	s_nop 0
	global_load_lds_dwordx4 v[224:225], off
	s_waitcnt vmcnt(8)
	s_waitcnt lgkmcnt(0)
	s_barrier
	s_setprio 1
	s_waitcnt lgkmcnt(0)
	v_mfma_f32_16x16x128_f8f6f4 v[158:161], v[2:9], v[192:199], v[158:161]
	v_mfma_f32_16x16x128_f8f6f4 v[154:157], v[10:17], v[192:199], v[154:157]
	v_mfma_f32_16x16x128_f8f6f4 v[150:153], v[2:9], v[200:207], v[150:153]
	v_mfma_f32_16x16x128_f8f6f4 v[146:149], v[10:17], v[200:207], v[146:149]
	v_mfma_f32_16x16x128_f8f6f4 v[142:145], v[2:9], v[208:215], v[142:145]
	v_mfma_f32_16x16x128_f8f6f4 v[138:141], v[10:17], v[208:215], v[138:141]
	v_mfma_f32_16x16x128_f8f6f4 v[134:137], v[2:9], v[216:223], v[134:137]
	v_mfma_f32_16x16x128_f8f6f4 v[130:133], v[10:17], v[216:223], v[130:133]
	s_setprio 0
	s_setprio 1
	v_mfma_f32_16x16x128_f8f6f4 v[126:129], v[18:25], v[192:199], v[126:129]
	v_mfma_f32_16x16x128_f8f6f4 v[122:125], v[26:33], v[192:199], v[122:125]
	v_mfma_f32_16x16x128_f8f6f4 v[118:121], v[18:25], v[200:207], v[118:121]
	v_mfma_f32_16x16x128_f8f6f4 v[114:117], v[26:33], v[200:207], v[114:117]
	v_mfma_f32_16x16x128_f8f6f4 v[110:113], v[18:25], v[208:215], v[110:113]
	v_mfma_f32_16x16x128_f8f6f4 v[106:109], v[26:33], v[208:215], v[106:109]
	v_mfma_f32_16x16x128_f8f6f4 v[102:105], v[18:25], v[216:223], v[102:105]
	v_mfma_f32_16x16x128_f8f6f4 v[98:101], v[26:33], v[216:223], v[98:101]
	s_setprio 0
	s_barrier
	s_add_i32 s26, s64, s42
	v_lshl_add_u64 v[178:179], v[178:179], 0, s[12:13]
	s_mov_b32 m0, s26
	ds_read_b128 v[192:195], v191 offset:49152
	ds_read_b128 v[196:199], v191 offset:50176
	ds_read_b128 v[200:203], v191 offset:51200
	ds_read_b128 v[204:207], v191 offset:52224
	ds_read_b128 v[208:211], v191 offset:53248
	ds_read_b128 v[212:215], v191 offset:54272
	ds_read_b128 v[216:219], v191 offset:55296
	ds_read_b128 v[220:223], v191 offset:56320
	global_load_lds_dwordx4 v[178:179], off
	s_add_i32 m0, s26, 0x2000
	s_add_u32 s24, s24, 0x70080
	v_lshl_add_u64 v[178:179], v[180:181], 0, s[12:13]
	s_addc_u32 s25, s25, 0
	s_add_i32 s26, s65, s42
	global_load_lds_dwordx4 v[178:179], off
	v_lshl_add_u64 v[178:179], s[24:25], 0, v[164:165]
	s_mov_b32 m0, s26
	s_nop 0
	global_load_lds_dwordx4 v[178:179], off
	v_lshl_add_u64 v[178:179], s[24:25], 0, v[168:169]
	s_add_i32 m0, s26, 0x2000
	s_nop 0
	global_load_lds_dwordx4 v[178:179], off
	v_lshl_add_u64 v[178:179], v[182:183], 0, s[12:13]
	s_mov_b32 m0, s48
	s_nop 0
	global_load_lds_dwordx4 v[178:179], off
	v_lshl_add_u64 v[178:179], v[184:185], 0, s[12:13]
	s_mov_b32 m0, s49
	s_nop 0
	global_load_lds_dwordx4 v[178:179], off
	s_waitcnt vmcnt(8)
	s_waitcnt lgkmcnt(0)
	s_barrier
	s_setprio 1
	s_waitcnt lgkmcnt(0)
	v_mfma_f32_16x16x128_f8f6f4 v[94:97], v[2:9], v[192:199], v[94:97]
	v_mfma_f32_16x16x128_f8f6f4 v[90:93], v[10:17], v[192:199], v[90:93]
	v_mfma_f32_16x16x128_f8f6f4 v[86:89], v[2:9], v[200:207], v[86:89]
	v_mfma_f32_16x16x128_f8f6f4 v[82:85], v[10:17], v[200:207], v[82:85]
	v_mfma_f32_16x16x128_f8f6f4 v[78:81], v[2:9], v[208:215], v[78:81]
	v_mfma_f32_16x16x128_f8f6f4 v[74:77], v[10:17], v[208:215], v[74:77]
	v_mfma_f32_16x16x128_f8f6f4 v[70:73], v[2:9], v[216:223], v[70:73]
	v_mfma_f32_16x16x128_f8f6f4 v[66:69], v[10:17], v[216:223], v[66:69]
	s_setprio 0
	s_setprio 1
	v_mfma_f32_16x16x128_f8f6f4 v[62:65], v[18:25], v[192:199], v[62:65]
	v_mfma_f32_16x16x128_f8f6f4 v[58:61], v[26:33], v[192:199], v[58:61]
	v_mfma_f32_16x16x128_f8f6f4 v[54:57], v[18:25], v[200:207], v[54:57]
	v_mfma_f32_16x16x128_f8f6f4 v[50:53], v[26:33], v[200:207], v[50:53]
	v_mfma_f32_16x16x128_f8f6f4 v[46:49], v[18:25], v[208:215], v[46:49]
	v_mfma_f32_16x16x128_f8f6f4 v[42:45], v[26:33], v[208:215], v[42:45]
	v_mfma_f32_16x16x128_f8f6f4 v[38:41], v[18:25], v[216:223], v[38:41]
	v_mfma_f32_16x16x128_f8f6f4 v[34:37], v[26:33], v[216:223], v[34:37]
	s_setprio 0
	s_barrier
	s_add_i32 s63, s63, 2
	s_add_u32 s22, s22, 0x100
	s_addc_u32 s23, s23, 0
	s_add_u32 s61, s61, 0x100
	s_addc_u32 s62, s62, 0
	s_cmp_gt_u32 s63, 25
	s_cbranch_scc0 .LBB0_2189
	s_and_b64 vcc, exec, s[14:15]
	s_cbranch_vccz .LBB0_2192
	s_barrier
